# baseline (speedup 1.0000x reference)
.LE_cdone1:
	s_waitcnt lgkmcnt(0)
	s_barrier
	v_mov_b32_e32 v252, 0x20800
	ds_read_b32 v200, v252
	ds_read_b32 v201, v252 offset:4
	ds_read_b32 v202, v252 offset:8
	s_waitcnt lgkmcnt(0)
	s_nop 1
	v_readfirstlane_b32 s31, v200
	v_readfirstlane_b32 s29, v201
	v_readfirstlane_b32 s30, v202
	s_nop 3
	s_barrier
	s_lshl_b32 s49, s29, 19
	s_lshl_b32 s64, s32, 13
	s_add_u32 s49, s49, s64
	s_mov_b32 s51, s64
	s_add_u32 s52, s51, 0x0
	s_add_u32 s53, s51, 0x1000
	s_add_u32 s54, s51, 0x8000
	s_add_u32 s55, s51, 0x9000
	s_add_u32 s56, s51, 0x10000
	s_add_u32 s57, s51, 0x11000
	s_add_u32 s58, s51, 0x18000
	s_add_u32 s59, s51, 0x19000
	s_lshl_b32 s64, s29, 8
	s_lshl_b32 s65, s30, 1
	s_add_u32 s64, s64, s65
	s_lshr_b32 s65, s32, 1
	s_add_u32 s64, s64, s65
	s_lshl_b32 s64, s64, 11
	s_and_b32 s65, s32, 1
	s_lshl_b32 s65, s65, 9
	s_add_u32 s50, s64, s65
	s_sub_u32 s60, s28, 1
	s_lshl_b32 s64, s30, 2
	s_add_u32 s64, s64, s32
	s_lshl_b32 s64, s64, 16
	s_add_u32 s44, s4, s64
	s_addc_u32 s45, s5, 0
	global_load_dwordx4 a[0:3], v192, s[44:45] offset:0
	global_load_dwordx4 a[4:7], v192, s[44:45] offset:1024
	global_load_dwordx4 a[8:11], v192, s[44:45] offset:2048
	global_load_dwordx4 a[12:15], v192, s[44:45] offset:3072
	s_add_u32 s44, s44, 0x1000
	s_addc_u32 s45, s45, 0
	global_load_dwordx4 a[16:19], v192, s[44:45] offset:0
	global_load_dwordx4 a[20:23], v192, s[44:45] offset:1024
	global_load_dwordx4 a[24:27], v192, s[44:45] offset:2048
	global_load_dwordx4 a[28:31], v192, s[44:45] offset:3072
	s_add_u32 s44, s44, 0x1000
	s_addc_u32 s45, s45, 0
	global_load_dwordx4 a[32:35], v192, s[44:45] offset:0
	global_load_dwordx4 a[36:39], v192, s[44:45] offset:1024
	global_load_dwordx4 a[40:43], v192, s[44:45] offset:2048
	global_load_dwordx4 a[44:47], v192, s[44:45] offset:3072
	s_add_u32 s44, s44, 0x1000
	s_addc_u32 s45, s45, 0
	global_load_dwordx4 a[48:51], v192, s[44:45] offset:0
	global_load_dwordx4 a[52:55], v192, s[44:45] offset:1024
	global_load_dwordx4 a[56:59], v192, s[44:45] offset:2048
	global_load_dwordx4 a[60:63], v192, s[44:45] offset:3072
	s_add_u32 s44, s44, 0x1000
	s_addc_u32 s45, s45, 0
	global_load_dwordx4 a[64:67], v192, s[44:45] offset:0
	global_load_dwordx4 a[68:71], v192, s[44:45] offset:1024
	global_load_dwordx4 a[72:75], v192, s[44:45] offset:2048
	global_load_dwordx4 a[76:79], v192, s[44:45] offset:3072
	s_add_u32 s44, s44, 0x1000
	s_addc_u32 s45, s45, 0
	global_load_dwordx4 a[80:83], v192, s[44:45] offset:0
	global_load_dwordx4 a[84:87], v192, s[44:45] offset:1024
	global_load_dwordx4 a[88:91], v192, s[44:45] offset:2048
	global_load_dwordx4 a[92:95], v192, s[44:45] offset:3072
	s_add_u32 s44, s44, 0x1000
	s_addc_u32 s45, s45, 0
	global_load_dwordx4 a[96:99], v192, s[44:45] offset:0
	global_load_dwordx4 a[100:103], v192, s[44:45] offset:1024
	global_load_dwordx4 a[104:107], v192, s[44:45] offset:2048
	global_load_dwordx4 a[108:111], v192, s[44:45] offset:3072
	s_add_u32 s44, s44, 0x1000
	s_addc_u32 s45, s45, 0
	global_load_dwordx4 a[112:115], v192, s[44:45] offset:0
	global_load_dwordx4 a[116:119], v192, s[44:45] offset:1024
	global_load_dwordx4 a[120:123], v192, s[44:45] offset:2048
	global_load_dwordx4 a[124:127], v192, s[44:45] offset:3072
	s_add_u32 s44, s44, 0x1000
	s_addc_u32 s45, s45, 0
	s_waitcnt vmcnt(16)
	global_load_dwordx4 a[128:131], v192, s[44:45] offset:0
	global_load_dwordx4 a[132:135], v192, s[44:45] offset:1024
	global_load_dwordx4 a[136:139], v192, s[44:45] offset:2048
	global_load_dwordx4 a[140:143], v192, s[44:45] offset:3072
	s_add_u32 s44, s44, 0x1000
	s_addc_u32 s45, s45, 0
	global_load_dwordx4 a[144:147], v192, s[44:45] offset:0
	global_load_dwordx4 a[148:151], v192, s[44:45] offset:1024
	global_load_dwordx4 a[152:155], v192, s[44:45] offset:2048
	global_load_dwordx4 a[156:159], v192, s[44:45] offset:3072
	s_add_u32 s44, s44, 0x1000
	s_addc_u32 s45, s45, 0
	global_load_dwordx4 a[160:163], v192, s[44:45] offset:0
	global_load_dwordx4 a[164:167], v192, s[44:45] offset:1024
	global_load_dwordx4 a[168:171], v192, s[44:45] offset:2048
	global_load_dwordx4 a[172:175], v192, s[44:45] offset:3072
	s_add_u32 s44, s44, 0x1000
	s_addc_u32 s45, s45, 0
	global_load_dwordx4 a[176:179], v192, s[44:45] offset:0
	global_load_dwordx4 a[180:183], v192, s[44:45] offset:1024
	global_load_dwordx4 a[184:187], v192, s[44:45] offset:2048
	global_load_dwordx4 a[188:191], v192, s[44:45] offset:3072
	s_add_u32 s44, s44, 0x1000
	s_addc_u32 s45, s45, 0
	global_load_dwordx4 a[192:195], v192, s[44:45] offset:0
	global_load_dwordx4 a[196:199], v192, s[44:45] offset:1024
	global_load_dwordx4 a[200:203], v192, s[44:45] offset:2048
	global_load_dwordx4 a[204:207], v192, s[44:45] offset:3072
	s_add_u32 s44, s44, 0x1000
	s_addc_u32 s45, s45, 0
	global_load_dwordx4 a[208:211], v192, s[44:45] offset:0
	global_load_dwordx4 a[212:215], v192, s[44:45] offset:1024
	global_load_dwordx4 a[216:219], v192, s[44:45] offset:2048
	global_load_dwordx4 a[220:223], v192, s[44:45] offset:3072
	s_add_u32 s44, s44, 0x1000
	s_addc_u32 s45, s45, 0
	global_load_dwordx4 v[160:163], v192, s[44:45] offset:0
	global_load_dwordx4 v[164:167], v192, s[44:45] offset:1024
	global_load_dwordx4 v[168:171], v192, s[44:45] offset:2048
	global_load_dwordx4 v[172:175], v192, s[44:45] offset:3072
	s_add_u32 s44, s44, 0x1000
	s_addc_u32 s45, s45, 0
	global_load_dwordx4 v[176:179], v192, s[44:45] offset:0
	global_load_dwordx4 v[180:183], v192, s[44:45] offset:1024
	global_load_dwordx4 v[184:187], v192, s[44:45] offset:2048
	global_load_dwordx4 v[188:191], v192, s[44:45] offset:3072
	s_add_u32 s44, s44, 0x1000
	s_addc_u32 s45, s45, 0
	v_mov_b32_e32 v128, 0
	v_mov_b32_e32 v129, 0
	v_mov_b32_e32 v130, 0
	v_mov_b32_e32 v131, 0
	v_mov_b32_e32 v132, 0
	v_mov_b32_e32 v133, 0
	v_mov_b32_e32 v134, 0
	v_mov_b32_e32 v135, 0
	v_mov_b32_e32 v136, 0
	v_mov_b32_e32 v137, 0
	v_mov_b32_e32 v138, 0
	v_mov_b32_e32 v139, 0
	v_mov_b32_e32 v140, 0
	v_mov_b32_e32 v141, 0
	v_mov_b32_e32 v142, 0
	v_mov_b32_e32 v143, 0
	v_mov_b32_e32 v144, 0
	v_mov_b32_e32 v145, 0
	v_mov_b32_e32 v146, 0
	v_mov_b32_e32 v147, 0
	v_mov_b32_e32 v148, 0
	v_mov_b32_e32 v149, 0
	v_mov_b32_e32 v150, 0
	v_mov_b32_e32 v151, 0
	v_mov_b32_e32 v152, 0
	v_mov_b32_e32 v153, 0
	v_mov_b32_e32 v154, 0
	v_mov_b32_e32 v155, 0
	v_mov_b32_e32 v156, 0
	v_mov_b32_e32 v157, 0
	v_mov_b32_e32 v158, 0
	v_mov_b32_e32 v159, 0
	s_lshl_b32 s64, s30, 5
	s_lshl_b32 s65, s32, 3
	s_add_u32 s64, s64, s65
	v_lshlrev_b32_e32 v255, 2, v254
	v_add_u32_e32 v255, s64, v255
	v_lshlrev_b32_e32 v249, 3, v253
	v_lshl_add_u32 v249, v254, 2, v249
	v_lshlrev_b32_e32 v250, 12, v253
	v_lshl_add_u32 v250, v254, 4, v250
	v_lshrrev_b32_e32 v200, 3, v253
	v_and_b32_e32 v201, 7, v253
	v_lshl_add_u32 v202, v200, 10, v201
	v_add_u32_e32 v202, s64, v202
	v_lshl_add_u32 v202, v202, 1, v254
	v_lshlrev_b32_e32 v202, 2, v202
	global_load_dword v248, v202, s[14:15]
	v_mov_b32_e32 v203, 0xbfb8aa3b
	v_mov_b32_e32 v204, 0xc038aa3b
	v_cmp_eq_u32_e32 vcc, 2, v200
	s_nop 1
	v_cndmask_b32_e32 v203, v203, v204, vcc
	v_lshlrev_b32_e32 v205, 2, v255
	v_add_u32_e32 v206, 0x0, v205
	global_load_dwordx4 v[232:235], v206, s[16:17]
	v_add_u32_e32 v206, 0x1000, v205
	global_load_dwordx4 v[236:239], v206, s[16:17]
	v_add_u32_e32 v206, 0x2000, v205
	global_load_dwordx4 v[240:243], v206, s[16:17]
	v_add_u32_e32 v206, 0x3000, v205
	global_load_dwordx4 v[244:247], v206, s[16:17]
	s_waitcnt vmcnt(0)
	v_mul_f32_e32 v248, v203, v248
	s_mov_b32 s65, 0xbfb8aa3b
	v_mul_f32_e32 v232, s65, v232
	v_mul_f32_e32 v233, s65, v233
	v_mul_f32_e32 v234, s65, v234
	v_mul_f32_e32 v235, s65, v235
	s_mov_b32 s65, 0xbfb8aa3b
	v_mul_f32_e32 v236, s65, v236
	v_mul_f32_e32 v237, s65, v237
	v_mul_f32_e32 v238, s65, v238
	v_mul_f32_e32 v239, s65, v239
	s_mov_b32 s65, 0xc038aa3b
	v_mul_f32_e32 v240, s65, v240
	v_mul_f32_e32 v241, s65, v241
	v_mul_f32_e32 v242, s65, v242
	v_mul_f32_e32 v243, s65, v243
	s_mov_b32 s65, 0xbfb8aa3b
	v_mul_f32_e32 v244, s65, v244
	v_mul_f32_e32 v245, s65, v245
	v_mul_f32_e32 v246, s65, v246
	v_mul_f32_e32 v247, s65, v247
	s_lshl_b32 s65, s29, 20
	s_lshl_b32 s66, s64, 2
	s_add_u32 s65, s65, s66
	s_add_u32 s62, s26, s65
	s_addc_u32 s63, s27, 0
	s_waitcnt vmcnt(0)
	v_add_u32_e32 v224, 0x0, v192
	v_add_u32_e32 v225, 0x1000, v192
	v_add_u32_e32 v226, 0x8000, v192
	v_add_u32_e32 v227, 0x9000, v192
	v_add_u32_e32 v252, 0x10000, v192
	v_add_u32_e32 v253, 0x11000, v192
	v_add_u32_e32 v254, 0x18000, v192
	v_add_u32_e32 v255, 0x19000, v192
	s_mov_b32 s33, 0
	s_lshl_b32 s64, s33, 11
	s_lshl_b32 s65, s29, 8
	s_add_u32 s64, s64, s65
	s_lshl_b32 s64, s64, 3
	s_add_u32 s42, s12, s64
	s_addc_u32 s43, s13, 0
	global_load_dword v228, v249, s[42:43] offset:0
	global_load_dword v229, v249, s[42:43] offset:256
	s_waitcnt vmcnt(0)
	v_mfma_f32_32x32x2_f32 v[0:15], v248, v228, v[232:247]
	v_mfma_f32_32x32x2_f32 v[16:31], v248, v229, v[232:247]
	s_nop 15
	s_nop 3
	s_lshl_b32 s64, s33, 11
	s_lshl_b32 s65, s29, 8
	s_add_u32 s64, s64, s65
	s_add_u32 s64, s64, 64
	s_lshl_b32 s64, s64, 3
	s_add_u32 s42, s12, s64
	s_addc_u32 s43, s13, 0
	global_load_dword v228, v249, s[42:43] offset:0
	global_load_dword v229, v249, s[42:43] offset:256
	s_waitcnt vmcnt(0)
	v_mfma_f32_32x32x2_f32 v[32:47], v248, v228, v[232:247]
	v_mfma_f32_32x32x2_f32 v[48:63], v248, v229, v[232:247]
	s_nop 15
	s_nop 3
	s_lshl_b32 s64, s33, 11
	s_lshl_b32 s65, s29, 8
	s_add_u32 s64, s64, s65
	s_add_u32 s64, s64, 128
	s_lshl_b32 s64, s64, 3
	s_add_u32 s42, s12, s64
	s_addc_u32 s43, s13, 0
	global_load_dword v228, v249, s[42:43] offset:0
	global_load_dword v229, v249, s[42:43] offset:256
	s_waitcnt vmcnt(0)
	v_mfma_f32_32x32x2_f32 v[64:79], v248, v228, v[232:247]
	v_mfma_f32_32x32x2_f32 v[80:95], v248, v229, v[232:247]
	s_nop 15
	s_nop 3
	s_lshl_b32 s64, s33, 11
	s_lshl_b32 s65, s29, 8
	s_add_u32 s64, s64, s65
	s_add_u32 s64, s64, 192
	s_lshl_b32 s64, s64, 3
	s_add_u32 s42, s12, s64
	s_addc_u32 s43, s13, 0
	global_load_dword v228, v249, s[42:43] offset:0
	global_load_dword v229, v249, s[42:43] offset:256
	s_waitcnt vmcnt(0)
	v_mfma_f32_32x32x2_f32 v[96:111], v248, v228, v[232:247]
	v_mfma_f32_32x32x2_f32 v[112:127], v248, v229, v[232:247]
	s_nop 15
	s_nop 3
	s_waitcnt vmcnt(0)
	s_waitcnt lgkmcnt(0)
	s_lshl_b32 s64, s33, 3
	s_add_u32 s64, s64, s29
	s_lshl_b32 s64, s64, 5
	s_add_u32 s64, s64, s30
	s_lshl_b32 s64, s64, 2
	s_add_u32 s40, s8, s64
	s_addc_u32 s41, s9, 0
	s_and_b32 s64, s33, 1
	s_lshl_b32 s64, s64, 22
	s_add_u32 s64, s64, s50
	s_add_u32 s36, s6, s64
	s_addc_u32 s37, s7, 0
	v_exp_f32_e32 v200, v0
	v_exp_f32_e32 v201, v1
	v_exp_f32_e32 v202, v2
	v_exp_f32_e32 v203, v3
	v_exp_f32_e32 v204, v4
	v_exp_f32_e32 v205, v5
	v_exp_f32_e32 v206, v6
	v_exp_f32_e32 v207, v7
	v_exp_f32_e32 v208, v8
	v_exp_f32_e32 v209, v9
	v_exp_f32_e32 v210, v10
	v_exp_f32_e32 v211, v11
	v_exp_f32_e32 v212, v12
	v_exp_f32_e32 v213, v13
	v_exp_f32_e32 v214, v14
	v_exp_f32_e32 v215, v15
	v_add_f32_e32 v200, 1.0, v200
	v_add_f32_e32 v201, 1.0, v201
	v_add_f32_e32 v202, 1.0, v202
	v_add_f32_e32 v203, 1.0, v203
	v_add_f32_e32 v204, 1.0, v204
	v_add_f32_e32 v205, 1.0, v205
	v_add_f32_e32 v206, 1.0, v206
	v_add_f32_e32 v207, 1.0, v207
	v_add_f32_e32 v208, 1.0, v208
	v_add_f32_e32 v209, 1.0, v209
	v_add_f32_e32 v210, 1.0, v210
	v_add_f32_e32 v211, 1.0, v211
	v_add_f32_e32 v212, 1.0, v212
	v_add_f32_e32 v213, 1.0, v213
	v_add_f32_e32 v214, 1.0, v214
	v_add_f32_e32 v215, 1.0, v215
	v_rcp_f32_e32 v200, v200
	v_rcp_f32_e32 v201, v201
	v_rcp_f32_e32 v202, v202
	v_rcp_f32_e32 v203, v203
	v_rcp_f32_e32 v204, v204
	v_rcp_f32_e32 v205, v205
	v_rcp_f32_e32 v206, v206
	v_rcp_f32_e32 v207, v207
	v_rcp_f32_e32 v208, v208
	v_rcp_f32_e32 v209, v209
	v_rcp_f32_e32 v210, v210
	v_rcp_f32_e32 v211, v211
	v_rcp_f32_e32 v212, v212
	v_rcp_f32_e32 v213, v213
	v_rcp_f32_e32 v214, v214
	v_rcp_f32_e32 v215, v215
	v_fmamk_f32 v208, v208, 0xc0b8aa3b, v198
	v_fmamk_f32 v209, v209, 0xc0b8aa3b, v198
	v_fmamk_f32 v210, v210, 0xc0b8aa3b, v198
	v_fmamk_f32 v211, v211, 0xc0b8aa3b, v198
	v_mul_f32_e32 v204, v204, v128
	v_mul_f32_e32 v205, v205, v129
	v_mul_f32_e32 v206, v206, v130
	v_mul_f32_e32 v207, v207, v131
	v_fma_f32 v128, v200, v208, v204
	v_fma_f32 v129, v201, v209, v205
	v_fma_f32 v130, v202, v210, v206
	v_fma_f32 v131, v203, v211, v207
	v_exp_f32_e32 v200, v128
	v_exp_f32_e32 v201, v129
	v_exp_f32_e32 v202, v130
	v_exp_f32_e32 v203, v131
	v_add_f32_e32 v200, 1.0, v200
	v_add_f32_e32 v201, 1.0, v201
	v_add_f32_e32 v202, 1.0, v202
	v_add_f32_e32 v203, 1.0, v203
	v_rcp_f32_e32 v200, v200
	v_rcp_f32_e32 v201, v201
	v_rcp_f32_e32 v202, v202
	v_rcp_f32_e32 v203, v203
	v_fma_f32 v200, v200, 2.0, -1.0
	v_fma_f32 v201, v201, 2.0, -1.0
	v_fma_f32 v202, v202, 2.0, -1.0
	v_fma_f32 v203, v203, 2.0, -1.0
	v_mul_f32_e32 v216, v212, v200
	v_mul_f32_e32 v217, v213, v201
	v_mul_f32_e32 v218, v214, v202
	v_mul_f32_e32 v219, v215, v203
	v_cvt_pk_f16_f32 v220, v216, v217
	v_cvt_pk_f16_f32 v221, v218, v219
	v_exp_f32_e32 v200, v16
	v_exp_f32_e32 v201, v17
	v_exp_f32_e32 v202, v18
	v_exp_f32_e32 v203, v19
	v_exp_f32_e32 v204, v20
	v_exp_f32_e32 v205, v21
	v_exp_f32_e32 v206, v22
	v_exp_f32_e32 v207, v23
	v_exp_f32_e32 v208, v24
	v_exp_f32_e32 v209, v25
	v_exp_f32_e32 v210, v26
	v_exp_f32_e32 v211, v27
	v_exp_f32_e32 v212, v28
	v_exp_f32_e32 v213, v29
	v_exp_f32_e32 v214, v30
	v_exp_f32_e32 v215, v31
	v_add_f32_e32 v200, 1.0, v200
	v_add_f32_e32 v201, 1.0, v201
	v_add_f32_e32 v202, 1.0, v202
	v_add_f32_e32 v203, 1.0, v203
	v_add_f32_e32 v204, 1.0, v204
	v_add_f32_e32 v205, 1.0, v205
	v_add_f32_e32 v206, 1.0, v206
	v_add_f32_e32 v207, 1.0, v207
	v_add_f32_e32 v208, 1.0, v208
	v_add_f32_e32 v209, 1.0, v209
	v_add_f32_e32 v210, 1.0, v210
	v_add_f32_e32 v211, 1.0, v211
	v_add_f32_e32 v212, 1.0, v212
	v_add_f32_e32 v213, 1.0, v213
	v_add_f32_e32 v214, 1.0, v214
	v_add_f32_e32 v215, 1.0, v215
	v_rcp_f32_e32 v200, v200
	v_rcp_f32_e32 v201, v201
	v_rcp_f32_e32 v202, v202
	v_rcp_f32_e32 v203, v203
	v_rcp_f32_e32 v204, v204
	v_rcp_f32_e32 v205, v205
	v_rcp_f32_e32 v206, v206
	v_rcp_f32_e32 v207, v207
	v_rcp_f32_e32 v208, v208
	v_rcp_f32_e32 v209, v209
	v_rcp_f32_e32 v210, v210
	v_rcp_f32_e32 v211, v211
	v_rcp_f32_e32 v212, v212
	v_rcp_f32_e32 v213, v213
	v_rcp_f32_e32 v214, v214
	v_rcp_f32_e32 v215, v215
	v_fmamk_f32 v208, v208, 0xc0b8aa3b, v198
	v_fmamk_f32 v209, v209, 0xc0b8aa3b, v198
	v_fmamk_f32 v210, v210, 0xc0b8aa3b, v198
	v_fmamk_f32 v211, v211, 0xc0b8aa3b, v198
	v_mul_f32_e32 v204, v204, v132
	v_mul_f32_e32 v205, v205, v133
	v_mul_f32_e32 v206, v206, v134
	v_mul_f32_e32 v207, v207, v135
	v_fma_f32 v132, v200, v208, v204
	v_fma_f32 v133, v201, v209, v205
	v_fma_f32 v134, v202, v210, v206
	v_fma_f32 v135, v203, v211, v207
	v_exp_f32_e32 v200, v132
	v_exp_f32_e32 v201, v133
	v_exp_f32_e32 v202, v134
	v_exp_f32_e32 v203, v135
	v_add_f32_e32 v200, 1.0, v200
	v_add_f32_e32 v201, 1.0, v201
	v_add_f32_e32 v202, 1.0, v202
	v_add_f32_e32 v203, 1.0, v203
	v_rcp_f32_e32 v200, v200
	v_rcp_f32_e32 v201, v201
	v_rcp_f32_e32 v202, v202
	v_rcp_f32_e32 v203, v203
	v_fma_f32 v200, v200, 2.0, -1.0
	v_fma_f32 v201, v201, 2.0, -1.0
	v_fma_f32 v202, v202, 2.0, -1.0
	v_fma_f32 v203, v203, 2.0, -1.0
	v_mul_f32_e32 v216, v212, v200
	v_mul_f32_e32 v217, v213, v201
	v_mul_f32_e32 v218, v214, v202
	v_mul_f32_e32 v219, v215, v203
	v_cvt_pk_f16_f32 v222, v216, v217
	v_cvt_pk_f16_f32 v223, v218, v219
	s_nop 1
	v_permlane32_swap_b32_e32 v220, v222
	v_permlane32_swap_b32_e32 v221, v223
	s_cmp_eq_u32 s31, 0
	s_cbranch_scc1 .LE_slow4
	global_store_dwordx4 v195, v[220:223], s[36:37] offset:0

.LE_pok19:
	s_waitcnt lgkmcnt(0)
	s_barrier
	s_mov_b32 m0, s52
	s_nop 0
	global_load_lds_dwordx4 v224, s[34:35] sc1
	global_load_lds_dwordx4 v224, s[34:35] offset:1024 sc1
	global_load_lds_dwordx4 v224, s[34:35] offset:2048 sc1
	global_load_lds_dwordx4 v224, s[34:35] offset:3072 sc1
	s_mov_b32 m0, s53
	s_nop 0
	global_load_lds_dwordx4 v225, s[34:35] sc1
	global_load_lds_dwordx4 v225, s[34:35] offset:1024 sc1
	global_load_lds_dwordx4 v225, s[34:35] offset:2048 sc1
	global_load_lds_dwordx4 v225, s[34:35] offset:3072 sc1
	s_mov_b32 m0, s54
	s_nop 0
	global_load_lds_dwordx4 v226, s[34:35] sc1
	global_load_lds_dwordx4 v226, s[34:35] offset:1024 sc1
	global_load_lds_dwordx4 v226, s[34:35] offset:2048 sc1
	global_load_lds_dwordx4 v226, s[34:35] offset:3072 sc1
	s_mov_b32 m0, s55
	s_nop 0
	global_load_lds_dwordx4 v227, s[34:35] sc1
	global_load_lds_dwordx4 v227, s[34:35] offset:1024 sc1
	global_load_lds_dwordx4 v227, s[34:35] offset:2048 sc1
	global_load_lds_dwordx4 v227, s[34:35] offset:3072 sc1
	s_waitcnt vmcnt(8)
	s_barrier
	s_mov_b32 m0, s56
	s_nop 0
	global_load_lds_dwordx4 v252, s[34:35] sc1
	ds_read_b128 a[224:227], v192 offset:0
	ds_read_b128 a[228:231], v192 offset:1024
	ds_read_b128 a[232:235], v192 offset:2048
	ds_read_b128 a[236:239], v192 offset:3072
	ds_read_b128 a[240:243], v192 offset:4096
	ds_read_b128 a[244:247], v192 offset:5120
	ds_read_b128 a[248:251], v192 offset:6144
	ds_read_b128 a[252:255], v192 offset:7168
.LE_loop16:
	s_sub_u32 s71, s33, 1
	s_add_u32 s61, s33, 1
	s_min_u32 s61, s61, s60
	s_and_b32 s64, s71, 1
	s_lshl_b32 s64, s64, 22
	s_add_u32 s64, s64, s50
	s_add_u32 s64, s64, 0x60000
	s_add_u32 s36, s6, s64
	s_addc_u32 s37, s7, 0
	s_lshl_b32 s64, s71, 3
	s_add_u32 s64, s64, s29
	s_lshl_b32 s64, s64, 5
	s_add_u32 s64, s64, s30
	s_lshl_b32 s64, s64, 2
	s_add_u32 s40, s8, s64
	s_addc_u32 s41, s9, 0
	s_lshl_b32 s64, s33, 11
	s_lshl_b32 s65, s29, 8
	s_add_u32 s64, s64, s65
	s_add_u32 s64, s64, 128
	s_lshl_b32 s64, s64, 3
	s_add_u32 s42, s12, s64
	s_addc_u32 s43, s13, 0
	s_nop 5
	global_load_dword v228, v249, s[42:43] offset:0
	global_load_dword v229, v249, s[42:43] offset:256
	s_waitcnt lgkmcnt(2)
	v_mfma_f32_32x32x16_f16 v[0:15], a[0:3], a[224:227], v[0:15]
	ds_read_b128 a[224:227], v192 offset:8192
	v_exp_f32_e32 v200, v96
	v_mfma_f32_32x32x16_f16 v[16:31], a[0:3], a[228:231], v[16:31]
	ds_read_b128 a[228:231], v192 offset:9216
	global_load_dword v251, v196, s[38:39] sc1
	v_exp_f32_e32 v201, v97
	v_add_f32_e32 v200, 1.0, v200
	v_mfma_f32_32x32x16_f16 v[0:15], a[4:7], a[232:235], v[0:15]
	ds_read_b128 a[232:235], v192 offset:10240
	v_exp_f32_e32 v202, v98
	v_add_f32_e32 v201, 1.0, v201
	v_mfma_f32_32x32x16_f16 v[16:31], a[4:7], a[236:239], v[16:31]
	ds_read_b128 a[236:239], v192 offset:11264
	global_load_lds_dwordx4 v252, s[34:35] offset:1024 sc1
	v_exp_f32_e32 v203, v99
	v_add_f32_e32 v202, 1.0, v202
	v_mfma_f32_32x32x16_f16 v[0:15], a[8:11], a[240:243], v[0:15]
	ds_read_b128 a[240:243], v192 offset:12288
	v_exp_f32_e32 v204, v100
	v_add_f32_e32 v203, 1.0, v203
	v_mfma_f32_32x32x16_f16 v[16:31], a[8:11], a[244:247], v[16:31]
	ds_read_b128 a[244:247], v192 offset:13312
	v_exp_f32_e32 v205, v101
	v_add_f32_e32 v204, 1.0, v204
	s_waitcnt lgkmcnt(2)
	v_mfma_f32_32x32x16_f16 v[0:15], a[12:15], a[248:251], v[0:15]
	ds_read_b128 a[248:251], v192 offset:14336
	v_exp_f32_e32 v206, v102
	v_add_f32_e32 v205, 1.0, v205
	v_mfma_f32_32x32x16_f16 v[16:31], a[12:15], a[252:255], v[16:31]
	ds_read_b128 a[252:255], v192 offset:15360
	global_load_lds_dwordx4 v252, s[34:35] offset:2048 sc1
	v_exp_f32_e32 v207, v103
	v_add_f32_e32 v206, 1.0, v206
	v_mfma_f32_32x32x16_f16 v[0:15], a[16:19], a[224:227], v[0:15]
	ds_read_b128 a[224:227], v192 offset:16384
	v_exp_f32_e32 v208, v104
	v_add_f32_e32 v207, 1.0, v207
	v_mfma_f32_32x32x16_f16 v[16:31], a[16:19], a[228:231], v[16:31]
	ds_read_b128 a[228:231], v192 offset:17408
	v_exp_f32_e32 v209, v105
	v_add_f32_e32 v208, 1.0, v208
	v_mfma_f32_32x32x16_f16 v[0:15], a[20:23], a[232:235], v[0:15]
	ds_read_b128 a[232:235], v192 offset:18432
	v_exp_f32_e32 v210, v106
	v_add_f32_e32 v209, 1.0, v209
	v_mfma_f32_32x32x16_f16 v[16:31], a[20:23], a[236:239], v[16:31]
	ds_read_b128 a[236:239], v192 offset:19456
	global_load_lds_dwordx4 v252, s[34:35] offset:3072 sc1
	v_exp_f32_e32 v211, v107
	v_add_f32_e32 v210, 1.0, v210
	s_waitcnt lgkmcnt(2)
	v_mfma_f32_32x32x16_f16 v[0:15], a[24:27], a[240:243], v[0:15]
	ds_read_b128 a[240:243], v192 offset:20480
	v_exp_f32_e32 v212, v108
	v_add_f32_e32 v211, 1.0, v211
	v_mfma_f32_32x32x16_f16 v[16:31], a[24:27], a[244:247], v[16:31]
	ds_read_b128 a[244:247], v192 offset:21504
	v_exp_f32_e32 v213, v109
	v_add_f32_e32 v212, 1.0, v212
	v_mfma_f32_32x32x16_f16 v[0:15], a[28:31], a[248:251], v[0:15]
	ds_read_b128 a[248:251], v192 offset:22528
	v_exp_f32_e32 v214, v110
	v_add_f32_e32 v213, 1.0, v213
	s_mov_b32 m0, s57
	v_mfma_f32_32x32x16_f16 v[16:31], a[28:31], a[252:255], v[16:31]
	ds_read_b128 a[252:255], v192 offset:23552
	global_load_lds_dwordx4 v253, s[34:35] sc1
	v_exp_f32_e32 v215, v111
	v_add_f32_e32 v214, 1.0, v214
	v_mfma_f32_32x32x16_f16 v[0:15], a[32:35], a[224:227], v[0:15]
	ds_read_b128 a[224:227], v192 offset:24576
	v_add_f32_e32 v215, 1.0, v215
	v_rcp_f32_e32 v200, v200
	v_mfma_f32_32x32x16_f16 v[16:31], a[32:35], a[228:231], v[16:31]
	ds_read_b128 a[228:231], v192 offset:25600
	v_rcp_f32_e32 v201, v201
	s_waitcnt lgkmcnt(2)
	v_mfma_f32_32x32x16_f16 v[0:15], a[36:39], a[232:235], v[0:15]
	ds_read_b128 a[232:235], v192 offset:26624
	v_rcp_f32_e32 v202, v202
	v_mfma_f32_32x32x16_f16 v[16:31], a[36:39], a[236:239], v[16:31]
	ds_read_b128 a[236:239], v192 offset:27648
	global_load_lds_dwordx4 v253, s[34:35] offset:1024 sc1
	v_rcp_f32_e32 v203, v203
	v_mfma_f32_32x32x16_f16 v[0:15], a[40:43], a[240:243], v[0:15]
	ds_read_b128 a[240:243], v192 offset:28672
	v_rcp_f32_e32 v204, v204
	v_mfma_f32_32x32x16_f16 v[16:31], a[40:43], a[244:247], v[16:31]
	ds_read_b128 a[244:247], v192 offset:29696
	v_rcp_f32_e32 v205, v205
	v_mul_f32_e32 v204, v204, v152
	v_mfma_f32_32x32x16_f16 v[0:15], a[44:47], a[248:251], v[0:15]
	ds_read_b128 a[248:251], v192 offset:30720
	v_rcp_f32_e32 v206, v206
	v_mul_f32_e32 v205, v205, v153
	v_mfma_f32_32x32x16_f16 v[16:31], a[44:47], a[252:255], v[16:31]
	ds_read_b128 a[252:255], v192 offset:31744
	global_load_lds_dwordx4 v253, s[34:35] offset:2048 sc1
	v_rcp_f32_e32 v207, v207
	v_mul_f32_e32 v206, v206, v154
	s_waitcnt vmcnt(10)
	s_barrier
	s_waitcnt lgkmcnt(2)
	v_mfma_f32_32x32x16_f16 v[0:15], a[48:51], a[224:227], v[0:15]
	ds_read_b128 a[224:227], v192 offset:32768
	v_rcp_f32_e32 v208, v208
	v_mul_f32_e32 v207, v207, v155
	v_mfma_f32_32x32x16_f16 v[16:31], a[48:51], a[228:231], v[16:31]
	ds_read_b128 a[228:231], v192 offset:33792
	v_rcp_f32_e32 v209, v209
	v_fmamk_f32 v208, v208, 0xc0b8aa3b, v198
	v_mfma_f32_32x32x16_f16 v[0:15], a[52:55], a[232:235], v[0:15]
	ds_read_b128 a[232:235], v192 offset:34816
	v_rcp_f32_e32 v210, v210
	v_fmamk_f32 v209, v209, 0xc0b8aa3b, v198
	v_fma_f32 v152, v200, v208, v204
	v_mfma_f32_32x32x16_f16 v[16:31], a[52:55], a[236:239], v[16:31]
	ds_read_b128 a[236:239], v192 offset:35840
	global_load_lds_dwordx4 v253, s[34:35] offset:3072 sc1
	v_rcp_f32_e32 v211, v211
	v_fmamk_f32 v210, v210, 0xc0b8aa3b, v198
	v_fma_f32 v153, v201, v209, v205
	v_mfma_f32_32x32x16_f16 v[0:15], a[56:59], a[240:243], v[0:15]
	ds_read_b128 a[240:243], v192 offset:36864
	v_rcp_f32_e32 v212, v212
	v_fmamk_f32 v211, v211, 0xc0b8aa3b, v198
	v_fma_f32 v154, v202, v210, v206
	v_mfma_f32_32x32x16_f16 v[16:31], a[56:59], a[244:247], v[16:31]
	ds_read_b128 a[244:247], v192 offset:37888
	v_rcp_f32_e32 v213, v213
	v_fma_f32 v155, v203, v211, v207
	s_waitcnt lgkmcnt(2)
	v_mfma_f32_32x32x16_f16 v[0:15], a[60:63], a[248:251], v[0:15]
	ds_read_b128 a[248:251], v192 offset:38912
	v_rcp_f32_e32 v214, v214
	s_mov_b32 m0, s58
	v_mfma_f32_32x32x16_f16 v[16:31], a[60:63], a[252:255], v[16:31]
	ds_read_b128 a[252:255], v192 offset:39936
	global_load_lds_dwordx4 v254, s[34:35] sc1
	v_rcp_f32_e32 v215, v215
	v_mfma_f32_32x32x16_f16 v[0:15], a[64:67], a[224:227], v[0:15]
	ds_read_b128 a[224:227], v192 offset:40960
	v_exp_f32_e32 v200, v152
	v_mfma_f32_32x32x16_f16 v[16:31], a[64:67], a[228:231], v[16:31]
	ds_read_b128 a[228:231], v192 offset:41984
	v_exp_f32_e32 v201, v153
	v_add_f32_e32 v200, 1.0, v200
	v_mfma_f32_32x32x16_f16 v[0:15], a[68:71], a[232:235], v[0:15]
	ds_read_b128 a[232:235], v192 offset:43008
	v_exp_f32_e32 v202, v154
	v_add_f32_e32 v201, 1.0, v201
	v_mfma_f32_32x32x16_f16 v[16:31], a[68:71], a[236:239], v[16:31]
	ds_read_b128 a[236:239], v192 offset:44032
	global_load_lds_dwordx4 v254, s[34:35] offset:1024 sc1
	v_exp_f32_e32 v203, v155
	v_add_f32_e32 v202, 1.0, v202
	s_waitcnt lgkmcnt(2)
	v_mfma_f32_32x32x16_f16 v[0:15], a[72:75], a[240:243], v[0:15]
	ds_read_b128 a[240:243], v192 offset:45056
	v_add_f32_e32 v203, 1.0, v203
	v_rcp_f32_e32 v200, v200
	v_mfma_f32_32x32x16_f16 v[16:31], a[72:75], a[244:247], v[16:31]
	ds_read_b128 a[244:247], v192 offset:46080
	v_rcp_f32_e32 v201, v201
	v_fma_f32 v200, v200, 2.0, -1.0
	v_mfma_f32_32x32x16_f16 v[0:15], a[76:79], a[248:251], v[0:15]
	ds_read_b128 a[248:251], v192 offset:47104
	v_rcp_f32_e32 v202, v202
	v_fma_f32 v201, v201, 2.0, -1.0
	v_mul_f32_e32 v216, v212, v200
	v_mfma_f32_32x32x16_f16 v[16:31], a[76:79], a[252:255], v[16:31]
	ds_read_b128 a[252:255], v192 offset:48128
	global_load_lds_dwordx4 v254, s[34:35] offset:2048 sc1
	v_rcp_f32_e32 v203, v203
	v_fma_f32 v202, v202, 2.0, -1.0
	v_mul_f32_e32 v217, v213, v201
	v_mfma_f32_32x32x16_f16 v[0:15], a[80:83], a[224:227], v[0:15]
	ds_read_b128 a[224:227], v192 offset:49152
	v_fma_f32 v203, v203, 2.0, -1.0
	v_mul_f32_e32 v218, v214, v202
	v_exp_f32_e32 v200, v112
	v_mfma_f32_32x32x16_f16 v[16:31], a[80:83], a[228:231], v[16:31]
	ds_read_b128 a[228:231], v192 offset:50176
	v_mul_f32_e32 v219, v215, v203
	v_cvt_pk_f16_f32 v220, v216, v217
	v_exp_f32_e32 v201, v113
	s_waitcnt lgkmcnt(2)
	v_mfma_f32_32x32x16_f16 v[0:15], a[84:87], a[232:235], v[0:15]
	ds_read_b128 a[232:235], v192 offset:51200
	v_cvt_pk_f16_f32 v221, v218, v219
	v_exp_f32_e32 v202, v114
	v_add_f32_e32 v200, 1.0, v200
	v_mfma_f32_32x32x16_f16 v[16:31], a[84:87], a[236:239], v[16:31]
	ds_read_b128 a[236:239], v192 offset:52224
	global_load_lds_dwordx4 v254, s[34:35] offset:3072 sc1
	v_exp_f32_e32 v203, v115
	v_add_f32_e32 v201, 1.0, v201
	v_add_f32_e32 v202, 1.0, v202
	v_mfma_f32_32x32x16_f16 v[0:15], a[88:91], a[240:243], v[0:15]
	ds_read_b128 a[240:243], v192 offset:53248
	v_exp_f32_e32 v204, v116
	v_add_f32_e32 v203, 1.0, v203
	v_mfma_f32_32x32x16_f16 v[16:31], a[88:91], a[244:247], v[16:31]
	ds_read_b128 a[244:247], v192 offset:54272
	v_exp_f32_e32 v205, v117
	v_add_f32_e32 v204, 1.0, v204
	v_mfma_f32_32x32x16_f16 v[0:15], a[92:95], a[248:251], v[0:15]
	ds_read_b128 a[248:251], v192 offset:55296
	v_exp_f32_e32 v206, v118
	v_add_f32_e32 v205, 1.0, v205
	s_mov_b32 m0, s59
	v_mfma_f32_32x32x16_f16 v[16:31], a[92:95], a[252:255], v[16:31]
	ds_read_b128 a[252:255], v192 offset:56320
	global_load_lds_dwordx4 v255, s[34:35] sc1
	v_exp_f32_e32 v207, v119
	v_add_f32_e32 v206, 1.0, v206
	s_waitcnt lgkmcnt(2)
	v_mfma_f32_32x32x16_f16 v[0:15], a[96:99], a[224:227], v[0:15]
	ds_read_b128 a[224:227], v192 offset:57344
	v_exp_f32_e32 v208, v120
	v_add_f32_e32 v207, 1.0, v207
	v_mfma_f32_32x32x16_f16 v[16:31], a[96:99], a[228:231], v[16:31]
	ds_read_b128 a[228:231], v192 offset:58368
	v_exp_f32_e32 v209, v121
	v_add_f32_e32 v208, 1.0, v208
	v_mfma_f32_32x32x16_f16 v[0:15], a[100:103], a[232:235], v[0:15]
	ds_read_b128 a[232:235], v192 offset:59392
	v_exp_f32_e32 v210, v122
	v_add_f32_e32 v209, 1.0, v209
	v_mfma_f32_32x32x16_f16 v[16:31], a[100:103], a[236:239], v[16:31]
	ds_read_b128 a[236:239], v192 offset:60416
	global_load_lds_dwordx4 v255, s[34:35] offset:1024 sc1
	v_exp_f32_e32 v211, v123
	v_add_f32_e32 v210, 1.0, v210
	v_mfma_f32_32x32x16_f16 v[0:15], a[104:107], a[240:243], v[0:15]
	ds_read_b128 a[240:243], v192 offset:61440
	v_exp_f32_e32 v212, v124
	v_add_f32_e32 v211, 1.0, v211
	v_mfma_f32_32x32x16_f16 v[16:31], a[104:107], a[244:247], v[16:31]
	ds_read_b128 a[244:247], v192 offset:62464
	v_exp_f32_e32 v213, v125
	v_add_f32_e32 v212, 1.0, v212
	s_waitcnt lgkmcnt(2)
	v_mfma_f32_32x32x16_f16 v[0:15], a[108:111], a[248:251], v[0:15]
	ds_read_b128 a[248:251], v192 offset:63488
	v_exp_f32_e32 v214, v126
	v_add_f32_e32 v213, 1.0, v213
	v_mfma_f32_32x32x16_f16 v[16:31], a[108:111], a[252:255], v[16:31]
	ds_read_b128 a[252:255], v192 offset:64512
	global_load_lds_dwordx4 v255, s[34:35] offset:2048 sc1
	v_exp_f32_e32 v215, v127
	v_add_f32_e32 v214, 1.0, v214
	s_waitcnt vmcnt(7)
	s_barrier
	v_mfma_f32_32x32x16_f16 v[0:15], a[112:115], a[224:227], v[0:15]
	ds_read_b128 a[224:227], v193 offset:0
	v_add_f32_e32 v215, 1.0, v215
	v_rcp_f32_e32 v200, v200
	v_mfma_f32_32x32x16_f16 v[16:31], a[112:115], a[228:231], v[16:31]
	ds_read_b128 a[228:231], v193 offset:1024
	v_rcp_f32_e32 v201, v201
	v_mfma_f32_32x32x16_f16 v[0:15], a[116:119], a[232:235], v[0:15]
	ds_read_b128 a[232:235], v193 offset:2048
	v_rcp_f32_e32 v202, v202
	v_mfma_f32_32x32x16_f16 v[16:31], a[116:119], a[236:239], v[16:31]
	ds_read_b128 a[236:239], v193 offset:3072
	global_load_lds_dwordx4 v255, s[34:35] offset:3072 sc1
	v_rcp_f32_e32 v203, v203
	s_waitcnt lgkmcnt(2)
	v_mfma_f32_32x32x16_f16 v[0:15], a[120:123], a[240:243], v[0:15]
	ds_read_b128 a[240:243], v193 offset:4096
	v_rcp_f32_e32 v204, v204
	v_mfma_f32_32x32x16_f16 v[16:31], a[120:123], a[244:247], v[16:31]
	ds_read_b128 a[244:247], v193 offset:5120
	v_rcp_f32_e32 v205, v205
	v_mul_f32_e32 v204, v204, v156
	v_mfma_f32_32x32x2_f32 v[64:79], v248, v228, v[232:247]
	v_mfma_f32_32x32x16_f16 v[0:15], a[124:127], a[248:251], v[0:15]
	ds_read_b128 a[248:251], v193 offset:6144
	v_rcp_f32_e32 v206, v206
	v_mul_f32_e32 v205, v205, v157
	v_mfma_f32_32x32x2_f32 v[80:95], v248, v229, v[232:247]
	s_mov_b32 m0, s52
	v_mfma_f32_32x32x16_f16 v[16:31], a[124:127], a[252:255], v[16:31]
	ds_read_b128 a[252:255], v193 offset:7168
	v_cmp_gt_u32_e32 vcc, 2, v251
	s_cbranch_vccnz .LE_tpoll21
.LE_tok20:
	s_add_u32 s34, s34, 0x20000
	s_addc_u32 s35, s35, 0
	global_load_lds_dwordx4 v224, s[34:35] sc1
	v_rcp_f32_e32 v207, v207
	v_mul_f32_e32 v206, v206, v158
	v_mfma_f32_32x32x16_f16 v[0:15], a[128:131], a[224:227], v[0:15]
	ds_read_b128 a[224:227], v193 offset:8192
	v_rcp_f32_e32 v208, v208
	v_mul_f32_e32 v207, v207, v159
	v_mfma_f32_32x32x16_f16 v[16:31], a[128:131], a[228:231], v[16:31]
	ds_read_b128 a[228:231], v193 offset:9216
	v_rcp_f32_e32 v209, v209
	v_fmamk_f32 v208, v208, 0xc0b8aa3b, v198
	s_waitcnt lgkmcnt(2)
	v_mfma_f32_32x32x16_f16 v[0:15], a[132:135], a[232:235], v[0:15]
	ds_read_b128 a[232:235], v193 offset:10240
	v_rcp_f32_e32 v210, v210
	v_fmamk_f32 v209, v209, 0xc0b8aa3b, v198
	v_fma_f32 v156, v200, v208, v204
	v_mfma_f32_32x32x16_f16 v[16:31], a[132:135], a[236:239], v[16:31]
	ds_read_b128 a[236:239], v193 offset:11264
	global_load_lds_dwordx4 v224, s[34:35] offset:1024 sc1
	v_rcp_f32_e32 v211, v211
	v_fmamk_f32 v210, v210, 0xc0b8aa3b, v198
	v_fma_f32 v157, v201, v209, v205
	v_mfma_f32_32x32x16_f16 v[0:15], a[136:139], a[240:243], v[0:15]
	ds_read_b128 a[240:243], v193 offset:12288
	v_rcp_f32_e32 v212, v212
	v_fmamk_f32 v211, v211, 0xc0b8aa3b, v198
	v_fma_f32 v158, v202, v210, v206
	v_mfma_f32_32x32x16_f16 v[16:31], a[136:139], a[244:247], v[16:31]
	ds_read_b128 a[244:247], v193 offset:13312
	v_rcp_f32_e32 v213, v213
	v_fma_f32 v159, v203, v211, v207
	v_mfma_f32_32x32x16_f16 v[0:15], a[140:143], a[248:251], v[0:15]
	ds_read_b128 a[248:251], v193 offset:14336
	v_rcp_f32_e32 v214, v214
	v_mfma_f32_32x32x16_f16 v[16:31], a[140:143], a[252:255], v[16:31]
	ds_read_b128 a[252:255], v193 offset:15360
	global_load_lds_dwordx4 v224, s[34:35] offset:2048 sc1
	v_rcp_f32_e32 v215, v215
	s_waitcnt lgkmcnt(2)
	v_mfma_f32_32x32x16_f16 v[0:15], a[144:147], a[224:227], v[0:15]
	ds_read_b128 a[224:227], v193 offset:16384
	v_exp_f32_e32 v200, v156
	v_mfma_f32_32x32x16_f16 v[16:31], a[144:147], a[228:231], v[16:31]
	ds_read_b128 a[228:231], v193 offset:17408
	v_exp_f32_e32 v201, v157
	v_add_f32_e32 v200, 1.0, v200
	v_mfma_f32_32x32x16_f16 v[0:15], a[148:151], a[232:235], v[0:15]
	ds_read_b128 a[232:235], v193 offset:18432
	v_exp_f32_e32 v202, v158
	v_add_f32_e32 v201, 1.0, v201
	v_mfma_f32_32x32x16_f16 v[16:31], a[148:151], a[236:239], v[16:31]
	ds_read_b128 a[236:239], v193 offset:19456
	global_load_lds_dwordx4 v224, s[34:35] offset:3072 sc1
	v_exp_f32_e32 v203, v159
	v_add_f32_e32 v202, 1.0, v202
	v_mfma_f32_32x32x16_f16 v[0:15], a[152:155], a[240:243], v[0:15]
	ds_read_b128 a[240:243], v193 offset:20480
	v_add_f32_e32 v203, 1.0, v203
	v_rcp_f32_e32 v200, v200
	v_mfma_f32_32x32x16_f16 v[16:31], a[152:155], a[244:247], v[16:31]
	ds_read_b128 a[244:247], v193 offset:21504
	v_rcp_f32_e32 v201, v201
	v_fma_f32 v200, v200, 2.0, -1.0
	s_waitcnt lgkmcnt(2)
	v_mfma_f32_32x32x16_f16 v[0:15], a[156:159], a[248:251], v[0:15]
	ds_read_b128 a[248:251], v193 offset:22528
	v_rcp_f32_e32 v202, v202
	v_fma_f32 v201, v201, 2.0, -1.0
	v_mul_f32_e32 v216, v212, v200
	s_mov_b32 m0, s53
	v_mfma_f32_32x32x16_f16 v[16:31], a[156:159], a[252:255], v[16:31]
	ds_read_b128 a[252:255], v193 offset:23552
	global_load_lds_dwordx4 v225, s[34:35] sc1
	v_rcp_f32_e32 v203, v203
	v_fma_f32 v202, v202, 2.0, -1.0
	v_mul_f32_e32 v217, v213, v201
	v_mfma_f32_32x32x16_f16 v[0:15], a[160:163], a[224:227], v[0:15]
	ds_read_b128 a[224:227], v193 offset:24576
	v_fma_f32 v203, v203, 2.0, -1.0
	v_mul_f32_e32 v218, v214, v202
	v_mfma_f32_32x32x16_f16 v[16:31], a[160:163], a[228:231], v[16:31]
	ds_read_b128 a[228:231], v193 offset:25600
	v_mul_f32_e32 v219, v215, v203
	v_cvt_pk_f16_f32 v222, v216, v217
	v_mfma_f32_32x32x16_f16 v[0:15], a[164:167], a[232:235], v[0:15]
	ds_read_b128 a[232:235], v193 offset:26624
	v_cvt_pk_f16_f32 v223, v218, v219
	v_mfma_f32_32x32x16_f16 v[16:31], a[164:167], a[236:239], v[16:31]
	ds_read_b128 a[236:239], v193 offset:27648
	global_load_lds_dwordx4 v225, s[34:35] offset:1024 sc1
	s_nop 1
	v_permlane32_swap_b32_e32 v220, v222
	v_permlane32_swap_b32_e32 v221, v223
	s_cmp_eq_u32 s31, 0
	s_cbranch_scc1 .LE_slow22
	global_store_dwordx4 v195, v[220:223], s[36:37] offset:0
.LE_join23:
	s_waitcnt lgkmcnt(2)
	v_mfma_f32_32x32x16_f16 v[0:15], a[168:171], a[240:243], v[0:15]
	ds_read_b128 a[240:243], v193 offset:28672
	v_mfma_f32_32x32x16_f16 v[16:31], a[168:171], a[244:247], v[16:31]
	ds_read_b128 a[244:247], v193 offset:29696
	v_mfma_f32_32x32x16_f16 v[0:15], a[172:175], a[248:251], v[0:15]
	ds_read_b128 a[248:251], v193 offset:30720
	v_mfma_f32_32x32x16_f16 v[16:31], a[172:175], a[252:255], v[16:31]
	ds_read_b128 a[252:255], v193 offset:31744
	global_load_lds_dwordx4 v225, s[34:35] offset:2048 sc1
	s_waitcnt vmcnt(8)
	s_barrier
	v_mfma_f32_32x32x16_f16 v[0:15], a[176:179], a[224:227], v[0:15]
	ds_read_b128 a[224:227], v193 offset:32768
	v_mfma_f32_32x32x16_f16 v[16:31], a[176:179], a[228:231], v[16:31]
	ds_read_b128 a[228:231], v193 offset:33792
	s_waitcnt lgkmcnt(2)
	v_mfma_f32_32x32x16_f16 v[0:15], a[180:183], a[232:235], v[0:15]
	ds_read_b128 a[232:235], v193 offset:34816
	v_mfma_f32_32x32x16_f16 v[16:31], a[180:183], a[236:239], v[16:31]
	ds_read_b128 a[236:239], v193 offset:35840
	global_load_lds_dwordx4 v225, s[34:35] offset:3072 sc1
	v_mfma_f32_32x32x16_f16 v[0:15], a[184:187], a[240:243], v[0:15]
	ds_read_b128 a[240:243], v193 offset:36864
	v_mfma_f32_32x32x16_f16 v[16:31], a[184:187], a[244:247], v[16:31]
	ds_read_b128 a[244:247], v193 offset:37888
	v_mfma_f32_32x32x16_f16 v[0:15], a[188:191], a[248:251], v[0:15]
	ds_read_b128 a[248:251], v193 offset:38912
	s_mov_b32 m0, s54
	v_mfma_f32_32x32x16_f16 v[16:31], a[188:191], a[252:255], v[16:31]
	ds_read_b128 a[252:255], v193 offset:39936
	global_load_lds_dwordx4 v226, s[34:35] sc1
	s_waitcnt lgkmcnt(2)
	v_mfma_f32_32x32x16_f16 v[0:15], a[192:195], a[224:227], v[0:15]
	ds_read_b128 a[224:227], v193 offset:40960
	s_waitcnt vmcnt(3)
	s_barrier
	v_mov_b32_e32 v199, 4
	s_cmp_eq_u32 s31, 0
	s_cbranch_scc1 .LE_slow24
	global_store_dword v197, v199, s[40:41]
.LE_join25:
	v_mfma_f32_32x32x16_f16 v[16:31], a[192:195], a[228:231], v[16:31]
	ds_read_b128 a[228:231], v193 offset:41984
	v_mfma_f32_32x32x16_f16 v[0:15], a[196:199], a[232:235], v[0:15]
	ds_read_b128 a[232:235], v193 offset:43008
	v_mfma_f32_32x32x16_f16 v[16:31], a[196:199], a[236:239], v[16:31]
	ds_read_b128 a[236:239], v193 offset:44032
	global_load_lds_dwordx4 v226, s[34:35] offset:1024 sc1
	v_mfma_f32_32x32x16_f16 v[0:15], a[200:203], a[240:243], v[0:15]
	ds_read_b128 a[240:243], v193 offset:45056
	s_and_b32 s64, s33, 1
	s_lshl_b32 s64, s64, 22
	s_add_u32 s64, s64, s50
	s_add_u32 s36, s6, s64
	s_addc_u32 s37, s7, 0
	s_lshl_b32 s64, s33, 3
	s_add_u32 s64, s64, s29
	s_lshl_b32 s64, s64, 5
	s_add_u32 s64, s64, s30
	s_lshl_b32 s64, s64, 2
	s_add_u32 s40, s8, s64
	s_addc_u32 s41, s9, 0
	s_lshl_b32 s64, s33, 11
	s_lshl_b32 s65, s29, 8
	s_add_u32 s64, s64, s65
	s_add_u32 s64, s64, 192
	s_lshl_b32 s64, s64, 3
	s_add_u32 s42, s12, s64
	s_addc_u32 s43, s13, 0
	v_mfma_f32_32x32x16_f16 v[16:31], a[200:203], a[244:247], v[16:31]
	ds_read_b128 a[244:247], v193 offset:46080
	s_waitcnt lgkmcnt(2)
	v_mfma_f32_32x32x16_f16 v[0:15], a[204:207], a[248:251], v[0:15]
	ds_read_b128 a[248:251], v193 offset:47104
	v_mfma_f32_32x32x16_f16 v[16:31], a[204:207], a[252:255], v[16:31]
	ds_read_b128 a[252:255], v193 offset:48128
	global_load_lds_dwordx4 v226, s[34:35] offset:2048 sc1
	v_mfma_f32_32x32x16_f16 v[0:15], a[208:211], a[224:227], v[0:15]
	ds_read_b128 a[224:227], v193 offset:49152
	v_mfma_f32_32x32x16_f16 v[16:31], a[208:211], a[228:231], v[16:31]
	ds_read_b128 a[228:231], v193 offset:50176
	v_mfma_f32_32x32x16_f16 v[0:15], a[212:215], a[232:235], v[0:15]
	ds_read_b128 a[232:235], v193 offset:51200
	v_mfma_f32_32x32x16_f16 v[16:31], a[212:215], a[236:239], v[16:31]
	ds_read_b128 a[236:239], v193 offset:52224
	global_load_lds_dwordx4 v226, s[34:35] offset:3072 sc1
	s_waitcnt lgkmcnt(2)
	v_mfma_f32_32x32x16_f16 v[0:15], a[216:219], a[240:243], v[0:15]
	ds_read_b128 a[240:243], v193 offset:53248
	v_mfma_f32_32x32x16_f16 v[16:31], a[216:219], a[244:247], v[16:31]
	ds_read_b128 a[244:247], v193 offset:54272
	v_mfma_f32_32x32x16_f16 v[0:15], a[220:223], a[248:251], v[0:15]
	ds_read_b128 a[248:251], v193 offset:55296
	s_mov_b32 m0, s55
	v_mfma_f32_32x32x16_f16 v[16:31], a[220:223], a[252:255], v[16:31]
	ds_read_b128 a[252:255], v193 offset:56320
	global_load_lds_dwordx4 v227, s[34:35] sc1
	v_mfma_f32_32x32x16_f16 v[0:15], v[160:163], a[224:227], v[0:15]
	ds_read_b128 a[224:227], v193 offset:57344
	v_mfma_f32_32x32x16_f16 v[16:31], v[160:163], a[228:231], v[16:31]
	ds_read_b128 a[228:231], v193 offset:58368
	s_waitcnt lgkmcnt(2)
	v_mfma_f32_32x32x16_f16 v[0:15], v[164:167], a[232:235], v[0:15]
	ds_read_b128 a[232:235], v193 offset:59392
	v_mfma_f32_32x32x16_f16 v[16:31], v[164:167], a[236:239], v[16:31]
	ds_read_b128 a[236:239], v193 offset:60416
	global_load_lds_dwordx4 v227, s[34:35] offset:1024 sc1
	v_mfma_f32_32x32x16_f16 v[0:15], v[168:171], a[240:243], v[0:15]
	ds_read_b128 a[240:243], v193 offset:61440
	v_mfma_f32_32x32x16_f16 v[16:31], v[168:171], a[244:247], v[16:31]
	ds_read_b128 a[244:247], v193 offset:62464
	v_mfma_f32_32x32x16_f16 v[0:15], v[172:175], a[248:251], v[0:15]
	ds_read_b128 a[248:251], v193 offset:63488
	v_mfma_f32_32x32x16_f16 v[16:31], v[172:175], a[252:255], v[16:31]
	ds_read_b128 a[252:255], v193 offset:64512
	global_load_lds_dwordx4 v227, s[34:35] offset:2048 sc1
	s_waitcnt vmcnt(8)
	s_barrier
	s_waitcnt lgkmcnt(2)
	v_mfma_f32_32x32x16_f16 v[0:15], v[176:179], a[224:227], v[0:15]
	ds_read_b128 a[224:227], v192 offset:0
	v_mfma_f32_32x32x16_f16 v[16:31], v[176:179], a[228:231], v[16:31]
	ds_read_b128 a[228:231], v192 offset:1024
	v_mfma_f32_32x32x16_f16 v[0:15], v[180:183], a[232:235], v[0:15]
	ds_read_b128 a[232:235], v192 offset:2048
	v_mfma_f32_32x32x16_f16 v[16:31], v[180:183], a[236:239], v[16:31]
	ds_read_b128 a[236:239], v192 offset:3072
	global_load_lds_dwordx4 v227, s[34:35] offset:3072 sc1
	v_mfma_f32_32x32x16_f16 v[0:15], v[184:187], a[240:243], v[0:15]
	ds_read_b128 a[240:243], v192 offset:4096
	v_mfma_f32_32x32x16_f16 v[16:31], v[184:187], a[244:247], v[16:31]
	ds_read_b128 a[244:247], v192 offset:5120
	s_waitcnt lgkmcnt(2)
	v_mfma_f32_32x32x16_f16 v[0:15], v[188:191], a[248:251], v[0:15]
	ds_read_b128 a[248:251], v192 offset:6144
	s_mov_b32 m0, s56
	v_mfma_f32_32x32x16_f16 v[16:31], v[188:191], a[252:255], v[16:31]
	ds_read_b128 a[252:255], v192 offset:7168
	global_load_lds_dwordx4 v252, s[34:35] sc1
	s_nop 5
	global_load_dword v228, v249, s[42:43] offset:0
	global_load_dword v229, v249, s[42:43] offset:256
	s_waitcnt lgkmcnt(2)
	v_mfma_f32_32x32x16_f16 v[32:47], a[0:3], a[224:227], v[32:47]
	ds_read_b128 a[224:227], v192 offset:8192
	v_exp_f32_e32 v200, v0
	v_mfma_f32_32x32x16_f16 v[48:63], a[0:3], a[228:231], v[48:63]
	ds_read_b128 a[228:231], v192 offset:9216
	global_load_dword v251, v196, s[38:39] sc1
	v_exp_f32_e32 v201, v1
	v_add_f32_e32 v200, 1.0, v200
	v_mfma_f32_32x32x16_f16 v[32:47], a[4:7], a[232:235], v[32:47]
	ds_read_b128 a[232:235], v192 offset:10240
	v_exp_f32_e32 v202, v2
	v_add_f32_e32 v201, 1.0, v201
	v_mfma_f32_32x32x16_f16 v[48:63], a[4:7], a[236:239], v[48:63]
	ds_read_b128 a[236:239], v192 offset:11264
	global_load_lds_dwordx4 v252, s[34:35] offset:1024 sc1
	v_exp_f32_e32 v203, v3
	v_add_f32_e32 v202, 1.0, v202
	v_mfma_f32_32x32x16_f16 v[32:47], a[8:11], a[240:243], v[32:47]
	ds_read_b128 a[240:243], v192 offset:12288
	v_exp_f32_e32 v204, v4
	v_add_f32_e32 v203, 1.0, v203
	v_mfma_f32_32x32x16_f16 v[48:63], a[8:11], a[244:247], v[48:63]
	ds_read_b128 a[244:247], v192 offset:13312
	v_exp_f32_e32 v205, v5
	v_add_f32_e32 v204, 1.0, v204
	s_waitcnt lgkmcnt(2)
	v_mfma_f32_32x32x16_f16 v[32:47], a[12:15], a[248:251], v[32:47]
	ds_read_b128 a[248:251], v192 offset:14336
	v_exp_f32_e32 v206, v6
	v_add_f32_e32 v205, 1.0, v205
	v_mfma_f32_32x32x16_f16 v[48:63], a[12:15], a[252:255], v[48:63]
	ds_read_b128 a[252:255], v192 offset:15360
	global_load_lds_dwordx4 v252, s[34:35] offset:2048 sc1
	v_exp_f32_e32 v207, v7
	v_add_f32_e32 v206, 1.0, v206
	v_mfma_f32_32x32x16_f16 v[32:47], a[16:19], a[224:227], v[32:47]
	ds_read_b128 a[224:227], v192 offset:16384
	v_exp_f32_e32 v208, v8
	v_add_f32_e32 v207, 1.0, v207
	v_mfma_f32_32x32x16_f16 v[48:63], a[16:19], a[228:231], v[48:63]
	ds_read_b128 a[228:231], v192 offset:17408
	v_exp_f32_e32 v209, v9
	v_add_f32_e32 v208, 1.0, v208
	v_mfma_f32_32x32x16_f16 v[32:47], a[20:23], a[232:235], v[32:47]
	ds_read_b128 a[232:235], v192 offset:18432
	v_exp_f32_e32 v210, v10
	v_add_f32_e32 v209, 1.0, v209
	v_mfma_f32_32x32x16_f16 v[48:63], a[20:23], a[236:239], v[48:63]
	ds_read_b128 a[236:239], v192 offset:19456
	global_load_lds_dwordx4 v252, s[34:35] offset:3072 sc1
	v_exp_f32_e32 v211, v11
	v_add_f32_e32 v210, 1.0, v210
	s_waitcnt lgkmcnt(2)
	v_mfma_f32_32x32x16_f16 v[32:47], a[24:27], a[240:243], v[32:47]
	ds_read_b128 a[240:243], v192 offset:20480
	v_exp_f32_e32 v212, v12
	v_add_f32_e32 v211, 1.0, v211
	v_mfma_f32_32x32x16_f16 v[48:63], a[24:27], a[244:247], v[48:63]
	ds_read_b128 a[244:247], v192 offset:21504
	v_exp_f32_e32 v213, v13
	v_add_f32_e32 v212, 1.0, v212
	v_mfma_f32_32x32x16_f16 v[32:47], a[28:31], a[248:251], v[32:47]
	ds_read_b128 a[248:251], v192 offset:22528
	v_exp_f32_e32 v214, v14
	v_add_f32_e32 v213, 1.0, v213
	s_mov_b32 m0, s57
	v_mfma_f32_32x32x16_f16 v[48:63], a[28:31], a[252:255], v[48:63]
	ds_read_b128 a[252:255], v192 offset:23552
	global_load_lds_dwordx4 v253, s[34:35] sc1
	v_exp_f32_e32 v215, v15
	v_add_f32_e32 v214, 1.0, v214
	v_mfma_f32_32x32x16_f16 v[32:47], a[32:35], a[224:227], v[32:47]
	ds_read_b128 a[224:227], v192 offset:24576
	v_add_f32_e32 v215, 1.0, v215
	v_rcp_f32_e32 v200, v200
	v_mfma_f32_32x32x16_f16 v[48:63], a[32:35], a[228:231], v[48:63]
	ds_read_b128 a[228:231], v192 offset:25600
	v_rcp_f32_e32 v201, v201
	s_waitcnt lgkmcnt(2)
	v_mfma_f32_32x32x16_f16 v[32:47], a[36:39], a[232:235], v[32:47]
	ds_read_b128 a[232:235], v192 offset:26624
	v_rcp_f32_e32 v202, v202
	v_mfma_f32_32x32x16_f16 v[48:63], a[36:39], a[236:239], v[48:63]
	ds_read_b128 a[236:239], v192 offset:27648
	global_load_lds_dwordx4 v253, s[34:35] offset:1024 sc1
	v_rcp_f32_e32 v203, v203
	v_mfma_f32_32x32x16_f16 v[32:47], a[40:43], a[240:243], v[32:47]
	ds_read_b128 a[240:243], v192 offset:28672
	v_rcp_f32_e32 v204, v204
	v_mfma_f32_32x32x16_f16 v[48:63], a[40:43], a[244:247], v[48:63]
	ds_read_b128 a[244:247], v192 offset:29696
	v_rcp_f32_e32 v205, v205
	v_mul_f32_e32 v204, v204, v128
	v_mfma_f32_32x32x16_f16 v[32:47], a[44:47], a[248:251], v[32:47]
	ds_read_b128 a[248:251], v192 offset:30720
	v_rcp_f32_e32 v206, v206
	v_mul_f32_e32 v205, v205, v129
	v_mfma_f32_32x32x16_f16 v[48:63], a[44:47], a[252:255], v[48:63]
	ds_read_b128 a[252:255], v192 offset:31744
	global_load_lds_dwordx4 v253, s[34:35] offset:2048 sc1
	v_rcp_f32_e32 v207, v207
	v_mul_f32_e32 v206, v206, v130
	s_waitcnt vmcnt(10)
	s_barrier
	s_waitcnt lgkmcnt(2)
	v_mfma_f32_32x32x16_f16 v[32:47], a[48:51], a[224:227], v[32:47]
	ds_read_b128 a[224:227], v192 offset:32768
	v_rcp_f32_e32 v208, v208
	v_mul_f32_e32 v207, v207, v131
	v_mfma_f32_32x32x16_f16 v[48:63], a[48:51], a[228:231], v[48:63]
	ds_read_b128 a[228:231], v192 offset:33792
	v_rcp_f32_e32 v209, v209
	v_fmamk_f32 v208, v208, 0xc0b8aa3b, v198
	v_mfma_f32_32x32x16_f16 v[32:47], a[52:55], a[232:235], v[32:47]
	ds_read_b128 a[232:235], v192 offset:34816
	v_rcp_f32_e32 v210, v210
	v_fmamk_f32 v209, v209, 0xc0b8aa3b, v198
	v_fma_f32 v128, v200, v208, v204
	v_mfma_f32_32x32x16_f16 v[48:63], a[52:55], a[236:239], v[48:63]
	ds_read_b128 a[236:239], v192 offset:35840
	global_load_lds_dwordx4 v253, s[34:35] offset:3072 sc1
	v_rcp_f32_e32 v211, v211
	v_fmamk_f32 v210, v210, 0xc0b8aa3b, v198
	v_fma_f32 v129, v201, v209, v205
	v_mfma_f32_32x32x16_f16 v[32:47], a[56:59], a[240:243], v[32:47]
	ds_read_b128 a[240:243], v192 offset:36864
	v_rcp_f32_e32 v212, v212
	v_fmamk_f32 v211, v211, 0xc0b8aa3b, v198
	v_fma_f32 v130, v202, v210, v206
	v_mfma_f32_32x32x16_f16 v[48:63], a[56:59], a[244:247], v[48:63]
	ds_read_b128 a[244:247], v192 offset:37888
	v_rcp_f32_e32 v213, v213
	v_fma_f32 v131, v203, v211, v207
	s_waitcnt lgkmcnt(2)
	v_mfma_f32_32x32x16_f16 v[32:47], a[60:63], a[248:251], v[32:47]
	ds_read_b128 a[248:251], v192 offset:38912
	v_rcp_f32_e32 v214, v214
	s_mov_b32 m0, s58
	v_mfma_f32_32x32x16_f16 v[48:63], a[60:63], a[252:255], v[48:63]
	ds_read_b128 a[252:255], v192 offset:39936
	global_load_lds_dwordx4 v254, s[34:35] sc1
	v_rcp_f32_e32 v215, v215
	v_mfma_f32_32x32x16_f16 v[32:47], a[64:67], a[224:227], v[32:47]
	ds_read_b128 a[224:227], v192 offset:40960
	v_exp_f32_e32 v200, v128
	v_mfma_f32_32x32x16_f16 v[48:63], a[64:67], a[228:231], v[48:63]
	ds_read_b128 a[228:231], v192 offset:41984
	v_exp_f32_e32 v201, v129
	v_add_f32_e32 v200, 1.0, v200
	v_mfma_f32_32x32x16_f16 v[32:47], a[68:71], a[232:235], v[32:47]
	ds_read_b128 a[232:235], v192 offset:43008
	v_exp_f32_e32 v202, v130
	v_add_f32_e32 v201, 1.0, v201
	v_mfma_f32_32x32x16_f16 v[48:63], a[68:71], a[236:239], v[48:63]
	ds_read_b128 a[236:239], v192 offset:44032
	global_load_lds_dwordx4 v254, s[34:35] offset:1024 sc1
	v_exp_f32_e32 v203, v131
	v_add_f32_e32 v202, 1.0, v202
	s_waitcnt lgkmcnt(2)
	v_mfma_f32_32x32x16_f16 v[32:47], a[72:75], a[240:243], v[32:47]
	ds_read_b128 a[240:243], v192 offset:45056
	v_add_f32_e32 v203, 1.0, v203
	v_rcp_f32_e32 v200, v200
	v_mfma_f32_32x32x16_f16 v[48:63], a[72:75], a[244:247], v[48:63]
	ds_read_b128 a[244:247], v192 offset:46080
	v_rcp_f32_e32 v201, v201
	v_fma_f32 v200, v200, 2.0, -1.0
	v_mfma_f32_32x32x16_f16 v[32:47], a[76:79], a[248:251], v[32:47]
	ds_read_b128 a[248:251], v192 offset:47104
	v_rcp_f32_e32 v202, v202
	v_fma_f32 v201, v201, 2.0, -1.0
	v_mul_f32_e32 v216, v212, v200
	v_mfma_f32_32x32x16_f16 v[48:63], a[76:79], a[252:255], v[48:63]
	ds_read_b128 a[252:255], v192 offset:48128
	global_load_lds_dwordx4 v254, s[34:35] offset:2048 sc1
	v_rcp_f32_e32 v203, v203
	v_fma_f32 v202, v202, 2.0, -1.0
	v_mul_f32_e32 v217, v213, v201
	v_mfma_f32_32x32x16_f16 v[32:47], a[80:83], a[224:227], v[32:47]
	ds_read_b128 a[224:227], v192 offset:49152
	v_fma_f32 v203, v203, 2.0, -1.0
	v_mul_f32_e32 v218, v214, v202
	v_exp_f32_e32 v200, v16
	v_mfma_f32_32x32x16_f16 v[48:63], a[80:83], a[228:231], v[48:63]
	ds_read_b128 a[228:231], v192 offset:50176
	v_mul_f32_e32 v219, v215, v203
	v_cvt_pk_f16_f32 v220, v216, v217
	v_exp_f32_e32 v201, v17
	s_waitcnt lgkmcnt(2)
	v_mfma_f32_32x32x16_f16 v[32:47], a[84:87], a[232:235], v[32:47]
	ds_read_b128 a[232:235], v192 offset:51200
	v_cvt_pk_f16_f32 v221, v218, v219
	v_exp_f32_e32 v202, v18
	v_add_f32_e32 v200, 1.0, v200
	v_mfma_f32_32x32x16_f16 v[48:63], a[84:87], a[236:239], v[48:63]
	ds_read_b128 a[236:239], v192 offset:52224
	global_load_lds_dwordx4 v254, s[34:35] offset:3072 sc1
	s_cmp_eq_u32 s33, s60
	s_cbranch_scc1 .LE_ht26
.LE_htb27:
	v_exp_f32_e32 v203, v19
	v_mfma_f32_32x32x16_f16 v[32:47], a[88:91], a[240:243], v[32:47]
	ds_read_b128 a[240:243], v192 offset:53248
	v_exp_f32_e32 v204, v20
	v_add_f32_e32 v201, 1.0, v201
	v_add_f32_e32 v202, 1.0, v202
	v_mfma_f32_32x32x16_f16 v[48:63], a[88:91], a[244:247], v[48:63]
	ds_read_b128 a[244:247], v192 offset:54272
	v_exp_f32_e32 v205, v21
	v_add_f32_e32 v203, 1.0, v203
	v_add_f32_e32 v204, 1.0, v204
	v_mfma_f32_32x32x16_f16 v[32:47], a[92:95], a[248:251], v[32:47]
	ds_read_b128 a[248:251], v192 offset:55296
	v_exp_f32_e32 v206, v22
	v_add_f32_e32 v205, 1.0, v205
	s_mov_b32 m0, s59
	v_mfma_f32_32x32x16_f16 v[48:63], a[92:95], a[252:255], v[48:63]
	ds_read_b128 a[252:255], v192 offset:56320
	global_load_lds_dwordx4 v255, s[34:35] sc1
	v_exp_f32_e32 v207, v23
	v_add_f32_e32 v206, 1.0, v206
	s_waitcnt lgkmcnt(2)
	v_mfma_f32_32x32x16_f16 v[32:47], a[96:99], a[224:227], v[32:47]
	ds_read_b128 a[224:227], v192 offset:57344
	v_exp_f32_e32 v208, v24
	v_add_f32_e32 v207, 1.0, v207
	v_mfma_f32_32x32x16_f16 v[48:63], a[96:99], a[228:231], v[48:63]
	ds_read_b128 a[228:231], v192 offset:58368
	v_exp_f32_e32 v209, v25
	v_add_f32_e32 v208, 1.0, v208
	v_mfma_f32_32x32x16_f16 v[32:47], a[100:103], a[232:235], v[32:47]
	ds_read_b128 a[232:235], v192 offset:59392
	v_exp_f32_e32 v210, v26
	v_add_f32_e32 v209, 1.0, v209
	v_mfma_f32_32x32x16_f16 v[48:63], a[100:103], a[236:239], v[48:63]
	ds_read_b128 a[236:239], v192 offset:60416
	global_load_lds_dwordx4 v255, s[34:35] offset:1024 sc1
	v_exp_f32_e32 v211, v27
	v_add_f32_e32 v210, 1.0, v210
	v_mfma_f32_32x32x16_f16 v[32:47], a[104:107], a[240:243], v[32:47]
	ds_read_b128 a[240:243], v192 offset:61440
	v_exp_f32_e32 v212, v28
	v_add_f32_e32 v211, 1.0, v211
	v_mfma_f32_32x32x16_f16 v[48:63], a[104:107], a[244:247], v[48:63]
	ds_read_b128 a[244:247], v192 offset:62464
	v_exp_f32_e32 v213, v29
	v_add_f32_e32 v212, 1.0, v212
	s_waitcnt lgkmcnt(2)
	v_mfma_f32_32x32x16_f16 v[32:47], a[108:111], a[248:251], v[32:47]
	ds_read_b128 a[248:251], v192 offset:63488
	v_exp_f32_e32 v214, v30
	v_add_f32_e32 v213, 1.0, v213
	v_mfma_f32_32x32x16_f16 v[48:63], a[108:111], a[252:255], v[48:63]
	ds_read_b128 a[252:255], v192 offset:64512
	global_load_lds_dwordx4 v255, s[34:35] offset:2048 sc1
	v_exp_f32_e32 v215, v31
	v_add_f32_e32 v214, 1.0, v214
	s_waitcnt vmcnt(7)
	s_barrier
	v_mfma_f32_32x32x16_f16 v[32:47], a[112:115], a[224:227], v[32:47]
	ds_read_b128 a[224:227], v193 offset:0
	v_add_f32_e32 v215, 1.0, v215
	v_rcp_f32_e32 v200, v200
	v_mfma_f32_32x32x16_f16 v[48:63], a[112:115], a[228:231], v[48:63]
	ds_read_b128 a[228:231], v193 offset:1024
	v_rcp_f32_e32 v201, v201
	v_mfma_f32_32x32x16_f16 v[32:47], a[116:119], a[232:235], v[32:47]
	ds_read_b128 a[232:235], v193 offset:2048
	v_rcp_f32_e32 v202, v202
	v_mfma_f32_32x32x16_f16 v[48:63], a[116:119], a[236:239], v[48:63]
	ds_read_b128 a[236:239], v193 offset:3072
	global_load_lds_dwordx4 v255, s[34:35] offset:3072 sc1
	v_rcp_f32_e32 v203, v203
	s_waitcnt lgkmcnt(2)
	v_mfma_f32_32x32x16_f16 v[32:47], a[120:123], a[240:243], v[32:47]
	ds_read_b128 a[240:243], v193 offset:4096
	v_rcp_f32_e32 v204, v204
	v_mfma_f32_32x32x16_f16 v[48:63], a[120:123], a[244:247], v[48:63]
	ds_read_b128 a[244:247], v193 offset:5120
	v_rcp_f32_e32 v205, v205
	v_mul_f32_e32 v204, v204, v132
	v_mfma_f32_32x32x2_f32 v[96:111], v248, v228, v[232:247]
	v_mfma_f32_32x32x16_f16 v[32:47], a[124:127], a[248:251], v[32:47]
	ds_read_b128 a[248:251], v193 offset:6144
	v_rcp_f32_e32 v206, v206
	v_mul_f32_e32 v205, v205, v133
	v_mfma_f32_32x32x2_f32 v[112:127], v248, v229, v[232:247]
	s_mov_b32 m0, s52
	v_mfma_f32_32x32x16_f16 v[48:63], a[124:127], a[252:255], v[48:63]
	ds_read_b128 a[252:255], v193 offset:7168
	v_cmp_gt_u32_e32 vcc, 3, v251
	s_cbranch_vccnz .LE_tpoll29
.LE_tok28:
	s_add_u32 s34, s34, 0x20000
	s_addc_u32 s35, s35, 0
	global_load_lds_dwordx4 v224, s[34:35] sc1
	v_rcp_f32_e32 v207, v207
	v_mul_f32_e32 v206, v206, v134
	v_mfma_f32_32x32x16_f16 v[32:47], a[128:131], a[224:227], v[32:47]
	ds_read_b128 a[224:227], v193 offset:8192
	v_rcp_f32_e32 v208, v208
	v_mul_f32_e32 v207, v207, v135
	v_mfma_f32_32x32x16_f16 v[48:63], a[128:131], a[228:231], v[48:63]
	ds_read_b128 a[228:231], v193 offset:9216
	v_rcp_f32_e32 v209, v209
	v_fmamk_f32 v208, v208, 0xc0b8aa3b, v198
	s_waitcnt lgkmcnt(2)
	v_mfma_f32_32x32x16_f16 v[32:47], a[132:135], a[232:235], v[32:47]
	ds_read_b128 a[232:235], v193 offset:10240
	v_rcp_f32_e32 v210, v210
	v_fmamk_f32 v209, v209, 0xc0b8aa3b, v198
	v_fma_f32 v132, v200, v208, v204
	v_mfma_f32_32x32x16_f16 v[48:63], a[132:135], a[236:239], v[48:63]
	ds_read_b128 a[236:239], v193 offset:11264
	global_load_lds_dwordx4 v224, s[34:35] offset:1024 sc1
	v_rcp_f32_e32 v211, v211
	v_fmamk_f32 v210, v210, 0xc0b8aa3b, v198
	v_fma_f32 v133, v201, v209, v205
	v_mfma_f32_32x32x16_f16 v[32:47], a[136:139], a[240:243], v[32:47]
	ds_read_b128 a[240:243], v193 offset:12288
	v_rcp_f32_e32 v212, v212
	v_fmamk_f32 v211, v211, 0xc0b8aa3b, v198
	v_fma_f32 v134, v202, v210, v206
	v_mfma_f32_32x32x16_f16 v[48:63], a[136:139], a[244:247], v[48:63]
	ds_read_b128 a[244:247], v193 offset:13312
	v_rcp_f32_e32 v213, v213
	v_fma_f32 v135, v203, v211, v207
	v_mfma_f32_32x32x16_f16 v[32:47], a[140:143], a[248:251], v[32:47]
	ds_read_b128 a[248:251], v193 offset:14336
	v_rcp_f32_e32 v214, v214
	v_mfma_f32_32x32x16_f16 v[48:63], a[140:143], a[252:255], v[48:63]
	ds_read_b128 a[252:255], v193 offset:15360
	global_load_lds_dwordx4 v224, s[34:35] offset:2048 sc1
	v_rcp_f32_e32 v215, v215
	s_waitcnt lgkmcnt(2)
	v_mfma_f32_32x32x16_f16 v[32:47], a[144:147], a[224:227], v[32:47]
	ds_read_b128 a[224:227], v193 offset:16384
	v_exp_f32_e32 v200, v132
	v_mfma_f32_32x32x16_f16 v[48:63], a[144:147], a[228:231], v[48:63]
	ds_read_b128 a[228:231], v193 offset:17408
	v_exp_f32_e32 v201, v133
	v_add_f32_e32 v200, 1.0, v200
	v_mfma_f32_32x32x16_f16 v[32:47], a[148:151], a[232:235], v[32:47]
	ds_read_b128 a[232:235], v193 offset:18432
	v_exp_f32_e32 v202, v134
	v_add_f32_e32 v201, 1.0, v201
	v_mfma_f32_32x32x16_f16 v[48:63], a[148:151], a[236:239], v[48:63]
	ds_read_b128 a[236:239], v193 offset:19456
	global_load_lds_dwordx4 v224, s[34:35] offset:3072 sc1
	v_exp_f32_e32 v203, v135
	v_add_f32_e32 v202, 1.0, v202
	v_mfma_f32_32x32x16_f16 v[32:47], a[152:155], a[240:243], v[32:47]
	ds_read_b128 a[240:243], v193 offset:20480
	v_add_f32_e32 v203, 1.0, v203
	v_rcp_f32_e32 v200, v200
	v_mfma_f32_32x32x16_f16 v[48:63], a[152:155], a[244:247], v[48:63]
	ds_read_b128 a[244:247], v193 offset:21504
	v_rcp_f32_e32 v201, v201
	v_fma_f32 v200, v200, 2.0, -1.0
	s_waitcnt lgkmcnt(2)
	v_mfma_f32_32x32x16_f16 v[32:47], a[156:159], a[248:251], v[32:47]
	ds_read_b128 a[248:251], v193 offset:22528
	v_rcp_f32_e32 v202, v202
	v_fma_f32 v201, v201, 2.0, -1.0
	v_mul_f32_e32 v216, v212, v200
	s_mov_b32 m0, s53
	v_mfma_f32_32x32x16_f16 v[48:63], a[156:159], a[252:255], v[48:63]
	ds_read_b128 a[252:255], v193 offset:23552
	global_load_lds_dwordx4 v225, s[34:35] sc1
	v_rcp_f32_e32 v203, v203
	v_fma_f32 v202, v202, 2.0, -1.0
	v_mul_f32_e32 v217, v213, v201
	v_mfma_f32_32x32x16_f16 v[32:47], a[160:163], a[224:227], v[32:47]
	ds_read_b128 a[224:227], v193 offset:24576
	v_fma_f32 v203, v203, 2.0, -1.0
	v_mul_f32_e32 v218, v214, v202
	v_mfma_f32_32x32x16_f16 v[48:63], a[160:163], a[228:231], v[48:63]
	ds_read_b128 a[228:231], v193 offset:25600
	v_mul_f32_e32 v219, v215, v203
	v_cvt_pk_f16_f32 v222, v216, v217
	v_mfma_f32_32x32x16_f16 v[32:47], a[164:167], a[232:235], v[32:47]
	ds_read_b128 a[232:235], v193 offset:26624
	v_cvt_pk_f16_f32 v223, v218, v219
	v_mfma_f32_32x32x16_f16 v[48:63], a[164:167], a[236:239], v[48:63]
	ds_read_b128 a[236:239], v193 offset:27648
	global_load_lds_dwordx4 v225, s[34:35] offset:1024 sc1
	s_cmp_eq_u32 s33, s60
	s_cbranch_scc1 .LE_ht30
.LE_htb31:
	s_waitcnt lgkmcnt(2)
	v_mfma_f32_32x32x16_f16 v[32:47], a[168:171], a[240:243], v[32:47]
	ds_read_b128 a[240:243], v193 offset:28672
	s_nop 1
	v_permlane32_swap_b32_e32 v220, v222
	v_permlane32_swap_b32_e32 v221, v223
	s_cmp_eq_u32 s31, 0
	s_cbranch_scc1 .LE_slow32
	global_store_dwordx4 v195, v[220:223], s[36:37] offset:0
.LE_join33:
	v_mfma_f32_32x32x16_f16 v[48:63], a[168:171], a[244:247], v[48:63]
	ds_read_b128 a[244:247], v193 offset:29696
	v_mfma_f32_32x32x16_f16 v[32:47], a[172:175], a[248:251], v[32:47]
	ds_read_b128 a[248:251], v193 offset:30720
	v_mfma_f32_32x32x16_f16 v[48:63], a[172:175], a[252:255], v[48:63]
	ds_read_b128 a[252:255], v193 offset:31744
	global_load_lds_dwordx4 v225, s[34:35] offset:2048 sc1
	s_waitcnt vmcnt(8)
	s_barrier
	v_mfma_f32_32x32x16_f16 v[32:47], a[176:179], a[224:227], v[32:47]
	ds_read_b128 a[224:227], v193 offset:32768
	v_mfma_f32_32x32x16_f16 v[48:63], a[176:179], a[228:231], v[48:63]
	ds_read_b128 a[228:231], v193 offset:33792
	s_waitcnt lgkmcnt(2)
	v_mfma_f32_32x32x16_f16 v[32:47], a[180:183], a[232:235], v[32:47]
	ds_read_b128 a[232:235], v193 offset:34816
	v_mfma_f32_32x32x16_f16 v[48:63], a[180:183], a[236:239], v[48:63]
	ds_read_b128 a[236:239], v193 offset:35840
	global_load_lds_dwordx4 v225, s[34:35] offset:3072 sc1
	v_mfma_f32_32x32x16_f16 v[32:47], a[184:187], a[240:243], v[32:47]
	ds_read_b128 a[240:243], v193 offset:36864
	v_mfma_f32_32x32x16_f16 v[48:63], a[184:187], a[244:247], v[48:63]
	ds_read_b128 a[244:247], v193 offset:37888
	v_mfma_f32_32x32x16_f16 v[32:47], a[188:191], a[248:251], v[32:47]
	ds_read_b128 a[248:251], v193 offset:38912
	s_mov_b32 m0, s54
	v_mfma_f32_32x32x16_f16 v[48:63], a[188:191], a[252:255], v[48:63]
	ds_read_b128 a[252:255], v193 offset:39936
	global_load_lds_dwordx4 v226, s[34:35] sc1
	s_waitcnt lgkmcnt(2)
	v_mfma_f32_32x32x16_f16 v[32:47], a[192:195], a[224:227], v[32:47]
	ds_read_b128 a[224:227], v193 offset:40960
	v_mfma_f32_32x32x16_f16 v[48:63], a[192:195], a[228:231], v[48:63]
	ds_read_b128 a[228:231], v193 offset:41984
	s_waitcnt vmcnt(3)
	s_barrier
	v_mov_b32_e32 v199, 1
	s_cmp_eq_u32 s31, 0
	s_cbranch_scc1 .LE_slow34
	global_store_dword v197, v199, s[40:41]
.LE_join35:
	v_mfma_f32_32x32x16_f16 v[32:47], a[196:199], a[232:235], v[32:47]
	ds_read_b128 a[232:235], v193 offset:43008
	v_mfma_f32_32x32x16_f16 v[48:63], a[196:199], a[236:239], v[48:63]
	ds_read_b128 a[236:239], v193 offset:44032
	global_load_lds_dwordx4 v226, s[34:35] offset:1024 sc1
	v_mfma_f32_32x32x16_f16 v[32:47], a[200:203], a[240:243], v[32:47]
	ds_read_b128 a[240:243], v193 offset:45056
	v_mfma_f32_32x32x16_f16 v[48:63], a[200:203], a[244:247], v[48:63]
	ds_read_b128 a[244:247], v193 offset:46080
	s_and_b32 s64, s33, 1
	s_lshl_b32 s64, s64, 22
	s_add_u32 s64, s64, s50
	s_add_u32 s64, s64, 0x20000
	s_add_u32 s36, s6, s64
	s_addc_u32 s37, s7, 0
	s_lshl_b32 s64, s33, 3
	s_add_u32 s64, s64, s29
	s_lshl_b32 s64, s64, 5
	s_add_u32 s64, s64, s30
	s_lshl_b32 s64, s64, 2
	s_add_u32 s40, s8, s64
	s_addc_u32 s41, s9, 0
	s_lshl_b32 s64, s61, 11
	s_lshl_b32 s65, s29, 8
	s_add_u32 s64, s64, s65
	s_lshl_b32 s64, s64, 3
	s_add_u32 s42, s12, s64
	s_addc_u32 s43, s13, 0
	s_waitcnt lgkmcnt(2)
	v_mfma_f32_32x32x16_f16 v[32:47], a[204:207], a[248:251], v[32:47]
	ds_read_b128 a[248:251], v193 offset:47104
	v_mfma_f32_32x32x16_f16 v[48:63], a[204:207], a[252:255], v[48:63]
	ds_read_b128 a[252:255], v193 offset:48128
	global_load_lds_dwordx4 v226, s[34:35] offset:2048 sc1
	v_mfma_f32_32x32x16_f16 v[32:47], a[208:211], a[224:227], v[32:47]
	ds_read_b128 a[224:227], v193 offset:49152
	v_mfma_f32_32x32x16_f16 v[48:63], a[208:211], a[228:231], v[48:63]
	ds_read_b128 a[228:231], v193 offset:50176
	v_mfma_f32_32x32x16_f16 v[32:47], a[212:215], a[232:235], v[32:47]
	ds_read_b128 a[232:235], v193 offset:51200
	v_mfma_f32_32x32x16_f16 v[48:63], a[212:215], a[236:239], v[48:63]
	ds_read_b128 a[236:239], v193 offset:52224
	global_load_lds_dwordx4 v226, s[34:35] offset:3072 sc1
	s_waitcnt lgkmcnt(2)
	v_mfma_f32_32x32x16_f16 v[32:47], a[216:219], a[240:243], v[32:47]
	ds_read_b128 a[240:243], v193 offset:53248
	v_mfma_f32_32x32x16_f16 v[48:63], a[216:219], a[244:247], v[48:63]
	ds_read_b128 a[244:247], v193 offset:54272
	v_mfma_f32_32x32x16_f16 v[32:47], a[220:223], a[248:251], v[32:47]
	ds_read_b128 a[248:251], v193 offset:55296
	s_mov_b32 m0, s55
	v_mfma_f32_32x32x16_f16 v[48:63], a[220:223], a[252:255], v[48:63]
	ds_read_b128 a[252:255], v193 offset:56320
	global_load_lds_dwordx4 v227, s[34:35] sc1
	v_mfma_f32_32x32x16_f16 v[32:47], v[160:163], a[224:227], v[32:47]
	ds_read_b128 a[224:227], v193 offset:57344
	v_mfma_f32_32x32x16_f16 v[48:63], v[160:163], a[228:231], v[48:63]
	ds_read_b128 a[228:231], v193 offset:58368
	s_waitcnt lgkmcnt(2)
	v_mfma_f32_32x32x16_f16 v[32:47], v[164:167], a[232:235], v[32:47]
	ds_read_b128 a[232:235], v193 offset:59392
	v_mfma_f32_32x32x16_f16 v[48:63], v[164:167], a[236:239], v[48:63]
	ds_read_b128 a[236:239], v193 offset:60416
	global_load_lds_dwordx4 v227, s[34:35] offset:1024 sc1
	v_mfma_f32_32x32x16_f16 v[32:47], v[168:171], a[240:243], v[32:47]
	ds_read_b128 a[240:243], v193 offset:61440
	v_mfma_f32_32x32x16_f16 v[48:63], v[168:171], a[244:247], v[48:63]
	ds_read_b128 a[244:247], v193 offset:62464
	v_mfma_f32_32x32x16_f16 v[32:47], v[172:175], a[248:251], v[32:47]
	ds_read_b128 a[248:251], v193 offset:63488
	v_mfma_f32_32x32x16_f16 v[48:63], v[172:175], a[252:255], v[48:63]
	ds_read_b128 a[252:255], v193 offset:64512
	global_load_lds_dwordx4 v227, s[34:35] offset:2048 sc1
	s_waitcnt vmcnt(8)
	s_barrier
	s_waitcnt lgkmcnt(2)
	v_mfma_f32_32x32x16_f16 v[32:47], v[176:179], a[224:227], v[32:47]
	ds_read_b128 a[224:227], v192 offset:0
	v_mfma_f32_32x32x16_f16 v[48:63], v[176:179], a[228:231], v[48:63]
	ds_read_b128 a[228:231], v192 offset:1024
	v_mfma_f32_32x32x16_f16 v[32:47], v[180:183], a[232:235], v[32:47]
	ds_read_b128 a[232:235], v192 offset:2048
	v_mfma_f32_32x32x16_f16 v[48:63], v[180:183], a[236:239], v[48:63]
	ds_read_b128 a[236:239], v192 offset:3072
	global_load_lds_dwordx4 v227, s[34:35] offset:3072 sc1
	v_mfma_f32_32x32x16_f16 v[32:47], v[184:187], a[240:243], v[32:47]
	ds_read_b128 a[240:243], v192 offset:4096
	v_mfma_f32_32x32x16_f16 v[48:63], v[184:187], a[244:247], v[48:63]
	ds_read_b128 a[244:247], v192 offset:5120
	s_waitcnt lgkmcnt(2)
	v_mfma_f32_32x32x16_f16 v[32:47], v[188:191], a[248:251], v[32:47]
	ds_read_b128 a[248:251], v192 offset:6144
	s_mov_b32 m0, s56
	v_mfma_f32_32x32x16_f16 v[48:63], v[188:191], a[252:255], v[48:63]
	ds_read_b128 a[252:255], v192 offset:7168
	global_load_lds_dwordx4 v252, s[34:35] sc1
	s_nop 5
	global_load_dword v228, v249, s[42:43] offset:0
	global_load_dword v229, v249, s[42:43] offset:256
	s_waitcnt lgkmcnt(2)
	v_mfma_f32_32x32x16_f16 v[64:79], a[0:3], a[224:227], v[64:79]
	ds_read_b128 a[224:227], v192 offset:8192
	v_exp_f32_e32 v200, v32
	v_mfma_f32_32x32x16_f16 v[80:95], a[0:3], a[228:231], v[80:95]
	ds_read_b128 a[228:231], v192 offset:9216
	global_load_dword v251, v196, s[38:39] sc1
	v_exp_f32_e32 v201, v33
	v_add_f32_e32 v200, 1.0, v200
	v_mfma_f32_32x32x16_f16 v[64:79], a[4:7], a[232:235], v[64:79]
	ds_read_b128 a[232:235], v192 offset:10240
	v_exp_f32_e32 v202, v34
	v_add_f32_e32 v201, 1.0, v201
	v_mfma_f32_32x32x16_f16 v[80:95], a[4:7], a[236:239], v[80:95]
	ds_read_b128 a[236:239], v192 offset:11264
	global_load_lds_dwordx4 v252, s[34:35] offset:1024 sc1
	v_exp_f32_e32 v203, v35
	v_add_f32_e32 v202, 1.0, v202
	v_mfma_f32_32x32x16_f16 v[64:79], a[8:11], a[240:243], v[64:79]
	ds_read_b128 a[240:243], v192 offset:12288
	v_exp_f32_e32 v204, v36
	v_add_f32_e32 v203, 1.0, v203
	v_mfma_f32_32x32x16_f16 v[80:95], a[8:11], a[244:247], v[80:95]
	ds_read_b128 a[244:247], v192 offset:13312
	v_exp_f32_e32 v205, v37
	v_add_f32_e32 v204, 1.0, v204
	s_waitcnt lgkmcnt(2)
	v_mfma_f32_32x32x16_f16 v[64:79], a[12:15], a[248:251], v[64:79]
	ds_read_b128 a[248:251], v192 offset:14336
	v_exp_f32_e32 v206, v38
	v_add_f32_e32 v205, 1.0, v205
	v_mfma_f32_32x32x16_f16 v[80:95], a[12:15], a[252:255], v[80:95]
	ds_read_b128 a[252:255], v192 offset:15360
	global_load_lds_dwordx4 v252, s[34:35] offset:2048 sc1
	v_exp_f32_e32 v207, v39
	v_add_f32_e32 v206, 1.0, v206
	v_mfma_f32_32x32x16_f16 v[64:79], a[16:19], a[224:227], v[64:79]
	ds_read_b128 a[224:227], v192 offset:16384
	v_exp_f32_e32 v208, v40
	v_add_f32_e32 v207, 1.0, v207
	v_mfma_f32_32x32x16_f16 v[80:95], a[16:19], a[228:231], v[80:95]
	ds_read_b128 a[228:231], v192 offset:17408
	v_exp_f32_e32 v209, v41
	v_add_f32_e32 v208, 1.0, v208
	v_mfma_f32_32x32x16_f16 v[64:79], a[20:23], a[232:235], v[64:79]
	ds_read_b128 a[232:235], v192 offset:18432
	v_exp_f32_e32 v210, v42
	v_add_f32_e32 v209, 1.0, v209
	v_mfma_f32_32x32x16_f16 v[80:95], a[20:23], a[236:239], v[80:95]
	ds_read_b128 a[236:239], v192 offset:19456
	global_load_lds_dwordx4 v252, s[34:35] offset:3072 sc1
	v_exp_f32_e32 v211, v43
	v_add_f32_e32 v210, 1.0, v210
	s_waitcnt lgkmcnt(2)
	v_mfma_f32_32x32x16_f16 v[64:79], a[24:27], a[240:243], v[64:79]
	ds_read_b128 a[240:243], v192 offset:20480
	v_exp_f32_e32 v212, v44
	v_add_f32_e32 v211, 1.0, v211
	v_mfma_f32_32x32x16_f16 v[80:95], a[24:27], a[244:247], v[80:95]
	ds_read_b128 a[244:247], v192 offset:21504
	v_exp_f32_e32 v213, v45
	v_add_f32_e32 v212, 1.0, v212
	v_mfma_f32_32x32x16_f16 v[64:79], a[28:31], a[248:251], v[64:79]
	ds_read_b128 a[248:251], v192 offset:22528
	v_exp_f32_e32 v214, v46
	v_add_f32_e32 v213, 1.0, v213
	s_mov_b32 m0, s57
	v_mfma_f32_32x32x16_f16 v[80:95], a[28:31], a[252:255], v[80:95]
	ds_read_b128 a[252:255], v192 offset:23552
	global_load_lds_dwordx4 v253, s[34:35] sc1
	v_exp_f32_e32 v215, v47
	v_add_f32_e32 v214, 1.0, v214
	v_mfma_f32_32x32x16_f16 v[64:79], a[32:35], a[224:227], v[64:79]
	ds_read_b128 a[224:227], v192 offset:24576
	v_add_f32_e32 v215, 1.0, v215
	v_rcp_f32_e32 v200, v200
	v_mfma_f32_32x32x16_f16 v[80:95], a[32:35], a[228:231], v[80:95]
	ds_read_b128 a[228:231], v192 offset:25600
	v_rcp_f32_e32 v201, v201
	s_waitcnt lgkmcnt(2)
	v_mfma_f32_32x32x16_f16 v[64:79], a[36:39], a[232:235], v[64:79]
	ds_read_b128 a[232:235], v192 offset:26624
	v_rcp_f32_e32 v202, v202
	v_mfma_f32_32x32x16_f16 v[80:95], a[36:39], a[236:239], v[80:95]
	ds_read_b128 a[236:239], v192 offset:27648
	global_load_lds_dwordx4 v253, s[34:35] offset:1024 sc1
	v_rcp_f32_e32 v203, v203
	v_mfma_f32_32x32x16_f16 v[64:79], a[40:43], a[240:243], v[64:79]
	ds_read_b128 a[240:243], v192 offset:28672
	v_rcp_f32_e32 v204, v204
	v_mfma_f32_32x32x16_f16 v[80:95], a[40:43], a[244:247], v[80:95]
	ds_read_b128 a[244:247], v192 offset:29696
	v_rcp_f32_e32 v205, v205
	v_mul_f32_e32 v204, v204, v136
	v_mfma_f32_32x32x16_f16 v[64:79], a[44:47], a[248:251], v[64:79]
	ds_read_b128 a[248:251], v192 offset:30720
	v_rcp_f32_e32 v206, v206
	v_mul_f32_e32 v205, v205, v137
	v_mfma_f32_32x32x16_f16 v[80:95], a[44:47], a[252:255], v[80:95]
	ds_read_b128 a[252:255], v192 offset:31744
	global_load_lds_dwordx4 v253, s[34:35] offset:2048 sc1
	v_rcp_f32_e32 v207, v207
	v_mul_f32_e32 v206, v206, v138
	s_waitcnt vmcnt(10)
	s_barrier
	s_waitcnt lgkmcnt(2)
	v_mfma_f32_32x32x16_f16 v[64:79], a[48:51], a[224:227], v[64:79]
	ds_read_b128 a[224:227], v192 offset:32768
	v_rcp_f32_e32 v208, v208
	v_mul_f32_e32 v207, v207, v139
	v_mfma_f32_32x32x16_f16 v[80:95], a[48:51], a[228:231], v[80:95]
	ds_read_b128 a[228:231], v192 offset:33792
	v_rcp_f32_e32 v209, v209
	v_fmamk_f32 v208, v208, 0xc0b8aa3b, v198
	v_mfma_f32_32x32x16_f16 v[64:79], a[52:55], a[232:235], v[64:79]
	ds_read_b128 a[232:235], v192 offset:34816
	v_rcp_f32_e32 v210, v210
	v_fmamk_f32 v209, v209, 0xc0b8aa3b, v198
	v_fma_f32 v136, v200, v208, v204
	v_mfma_f32_32x32x16_f16 v[80:95], a[52:55], a[236:239], v[80:95]
	ds_read_b128 a[236:239], v192 offset:35840
	global_load_lds_dwordx4 v253, s[34:35] offset:3072 sc1
	v_rcp_f32_e32 v211, v211
	v_fmamk_f32 v210, v210, 0xc0b8aa3b, v198
	v_fma_f32 v137, v201, v209, v205
	v_mfma_f32_32x32x16_f16 v[64:79], a[56:59], a[240:243], v[64:79]
	ds_read_b128 a[240:243], v192 offset:36864
	v_rcp_f32_e32 v212, v212
	v_fmamk_f32 v211, v211, 0xc0b8aa3b, v198
	v_fma_f32 v138, v202, v210, v206
	v_mfma_f32_32x32x16_f16 v[80:95], a[56:59], a[244:247], v[80:95]
	ds_read_b128 a[244:247], v192 offset:37888
	v_rcp_f32_e32 v213, v213
	v_fma_f32 v139, v203, v211, v207
	s_waitcnt lgkmcnt(2)
	v_mfma_f32_32x32x16_f16 v[64:79], a[60:63], a[248:251], v[64:79]
	ds_read_b128 a[248:251], v192 offset:38912
	v_rcp_f32_e32 v214, v214
	s_mov_b32 m0, s58
	v_mfma_f32_32x32x16_f16 v[80:95], a[60:63], a[252:255], v[80:95]
	ds_read_b128 a[252:255], v192 offset:39936
	global_load_lds_dwordx4 v254, s[34:35] sc1
	v_rcp_f32_e32 v215, v215
	v_mfma_f32_32x32x16_f16 v[64:79], a[64:67], a[224:227], v[64:79]
	ds_read_b128 a[224:227], v192 offset:40960
	v_exp_f32_e32 v200, v136
	v_mfma_f32_32x32x16_f16 v[80:95], a[64:67], a[228:231], v[80:95]
	ds_read_b128 a[228:231], v192 offset:41984
	v_exp_f32_e32 v201, v137
	v_add_f32_e32 v200, 1.0, v200
	v_mfma_f32_32x32x16_f16 v[64:79], a[68:71], a[232:235], v[64:79]
	ds_read_b128 a[232:235], v192 offset:43008
	v_exp_f32_e32 v202, v138
	v_add_f32_e32 v201, 1.0, v201
	v_mfma_f32_32x32x16_f16 v[80:95], a[68:71], a[236:239], v[80:95]
	ds_read_b128 a[236:239], v192 offset:44032
	global_load_lds_dwordx4 v254, s[34:35] offset:1024 sc1
	v_exp_f32_e32 v203, v139
	v_add_f32_e32 v202, 1.0, v202
	s_waitcnt lgkmcnt(2)
	v_mfma_f32_32x32x16_f16 v[64:79], a[72:75], a[240:243], v[64:79]
	ds_read_b128 a[240:243], v192 offset:45056
	v_add_f32_e32 v203, 1.0, v203
	v_rcp_f32_e32 v200, v200
	v_mfma_f32_32x32x16_f16 v[80:95], a[72:75], a[244:247], v[80:95]
	ds_read_b128 a[244:247], v192 offset:46080
	v_rcp_f32_e32 v201, v201
	v_fma_f32 v200, v200, 2.0, -1.0
	v_mfma_f32_32x32x16_f16 v[64:79], a[76:79], a[248:251], v[64:79]
	ds_read_b128 a[248:251], v192 offset:47104
	v_rcp_f32_e32 v202, v202
	v_fma_f32 v201, v201, 2.0, -1.0
	v_mul_f32_e32 v216, v212, v200
	v_mfma_f32_32x32x16_f16 v[80:95], a[76:79], a[252:255], v[80:95]
	ds_read_b128 a[252:255], v192 offset:48128
	global_load_lds_dwordx4 v254, s[34:35] offset:2048 sc1
	v_rcp_f32_e32 v203, v203
	v_fma_f32 v202, v202, 2.0, -1.0
	v_mul_f32_e32 v217, v213, v201
	v_mfma_f32_32x32x16_f16 v[64:79], a[80:83], a[224:227], v[64:79]
	ds_read_b128 a[224:227], v192 offset:49152
	v_fma_f32 v203, v203, 2.0, -1.0
	v_mul_f32_e32 v218, v214, v202
	v_exp_f32_e32 v200, v48
	v_mfma_f32_32x32x16_f16 v[80:95], a[80:83], a[228:231], v[80:95]
	ds_read_b128 a[228:231], v192 offset:50176
	v_mul_f32_e32 v219, v215, v203
	v_cvt_pk_f16_f32 v220, v216, v217
	v_exp_f32_e32 v201, v49
	s_waitcnt lgkmcnt(2)
	v_mfma_f32_32x32x16_f16 v[64:79], a[84:87], a[232:235], v[64:79]
	ds_read_b128 a[232:235], v192 offset:51200
	v_cvt_pk_f16_f32 v221, v218, v219
	v_exp_f32_e32 v202, v50
	v_add_f32_e32 v200, 1.0, v200
	v_mfma_f32_32x32x16_f16 v[80:95], a[84:87], a[236:239], v[80:95]
	ds_read_b128 a[236:239], v192 offset:52224
	global_load_lds_dwordx4 v254, s[34:35] offset:3072 sc1
	s_cmp_eq_u32 s33, s60
	s_cbranch_scc1 .LE_ht36
.LE_htb37:
	v_exp_f32_e32 v203, v51
	v_mfma_f32_32x32x16_f16 v[64:79], a[88:91], a[240:243], v[64:79]
	ds_read_b128 a[240:243], v192 offset:53248
	v_exp_f32_e32 v204, v52
	v_add_f32_e32 v201, 1.0, v201
	v_add_f32_e32 v202, 1.0, v202
	v_mfma_f32_32x32x16_f16 v[80:95], a[88:91], a[244:247], v[80:95]
	ds_read_b128 a[244:247], v192 offset:54272
	v_exp_f32_e32 v205, v53
	v_add_f32_e32 v203, 1.0, v203
	v_add_f32_e32 v204, 1.0, v204
	v_mfma_f32_32x32x16_f16 v[64:79], a[92:95], a[248:251], v[64:79]
	ds_read_b128 a[248:251], v192 offset:55296
	v_exp_f32_e32 v206, v54
	v_add_f32_e32 v205, 1.0, v205
	s_mov_b32 m0, s59
	v_mfma_f32_32x32x16_f16 v[80:95], a[92:95], a[252:255], v[80:95]
	ds_read_b128 a[252:255], v192 offset:56320
	global_load_lds_dwordx4 v255, s[34:35] sc1
	v_exp_f32_e32 v207, v55
	v_add_f32_e32 v206, 1.0, v206
	s_waitcnt lgkmcnt(2)
	v_mfma_f32_32x32x16_f16 v[64:79], a[96:99], a[224:227], v[64:79]
	ds_read_b128 a[224:227], v192 offset:57344
	v_exp_f32_e32 v208, v56
	v_add_f32_e32 v207, 1.0, v207
	v_mfma_f32_32x32x16_f16 v[80:95], a[96:99], a[228:231], v[80:95]
	ds_read_b128 a[228:231], v192 offset:58368
	v_exp_f32_e32 v209, v57
	v_add_f32_e32 v208, 1.0, v208
	v_mfma_f32_32x32x16_f16 v[64:79], a[100:103], a[232:235], v[64:79]
	ds_read_b128 a[232:235], v192 offset:59392
	v_exp_f32_e32 v210, v58
	v_add_f32_e32 v209, 1.0, v209
	v_mfma_f32_32x32x16_f16 v[80:95], a[100:103], a[236:239], v[80:95]
	ds_read_b128 a[236:239], v192 offset:60416
	global_load_lds_dwordx4 v255, s[34:35] offset:1024 sc1
	v_exp_f32_e32 v211, v59
	v_add_f32_e32 v210, 1.0, v210
	v_mfma_f32_32x32x16_f16 v[64:79], a[104:107], a[240:243], v[64:79]
	ds_read_b128 a[240:243], v192 offset:61440
	v_exp_f32_e32 v212, v60
	v_add_f32_e32 v211, 1.0, v211
	v_mfma_f32_32x32x16_f16 v[80:95], a[104:107], a[244:247], v[80:95]
	ds_read_b128 a[244:247], v192 offset:62464
	v_exp_f32_e32 v213, v61
	v_add_f32_e32 v212, 1.0, v212
	s_waitcnt lgkmcnt(2)
	v_mfma_f32_32x32x16_f16 v[64:79], a[108:111], a[248:251], v[64:79]
	ds_read_b128 a[248:251], v192 offset:63488
	v_exp_f32_e32 v214, v62
	v_add_f32_e32 v213, 1.0, v213
	v_mfma_f32_32x32x16_f16 v[80:95], a[108:111], a[252:255], v[80:95]
	ds_read_b128 a[252:255], v192 offset:64512
	global_load_lds_dwordx4 v255, s[34:35] offset:2048 sc1
	v_exp_f32_e32 v215, v63
	v_add_f32_e32 v214, 1.0, v214
	s_waitcnt vmcnt(7)
	s_barrier
	v_mfma_f32_32x32x16_f16 v[64:79], a[112:115], a[224:227], v[64:79]
	ds_read_b128 a[224:227], v193 offset:0
	v_add_f32_e32 v215, 1.0, v215
	v_rcp_f32_e32 v200, v200
	v_mfma_f32_32x32x16_f16 v[80:95], a[112:115], a[228:231], v[80:95]
	ds_read_b128 a[228:231], v193 offset:1024
	v_rcp_f32_e32 v201, v201
	v_mfma_f32_32x32x16_f16 v[64:79], a[116:119], a[232:235], v[64:79]
	ds_read_b128 a[232:235], v193 offset:2048
	v_rcp_f32_e32 v202, v202
	v_mfma_f32_32x32x16_f16 v[80:95], a[116:119], a[236:239], v[80:95]
	ds_read_b128 a[236:239], v193 offset:3072
	global_load_lds_dwordx4 v255, s[34:35] offset:3072 sc1
	v_rcp_f32_e32 v203, v203
	s_waitcnt lgkmcnt(2)
	v_mfma_f32_32x32x16_f16 v[64:79], a[120:123], a[240:243], v[64:79]
	ds_read_b128 a[240:243], v193 offset:4096
	v_rcp_f32_e32 v204, v204
	v_mfma_f32_32x32x16_f16 v[80:95], a[120:123], a[244:247], v[80:95]
	ds_read_b128 a[244:247], v193 offset:5120
	v_rcp_f32_e32 v205, v205
	v_mul_f32_e32 v204, v204, v140
	v_mfma_f32_32x32x2_f32 v[0:15], v248, v228, v[232:247]
	v_mfma_f32_32x32x16_f16 v[64:79], a[124:127], a[248:251], v[64:79]
	ds_read_b128 a[248:251], v193 offset:6144
	v_rcp_f32_e32 v206, v206
	v_mul_f32_e32 v205, v205, v141
	v_mfma_f32_32x32x2_f32 v[16:31], v248, v229, v[232:247]
	s_mov_b32 m0, s52
	v_mfma_f32_32x32x16_f16 v[80:95], a[124:127], a[252:255], v[80:95]
	ds_read_b128 a[252:255], v193 offset:7168
	v_cmp_gt_u32_e32 vcc, 4, v251
	s_cbranch_vccnz .LE_tpoll39
.LE_tok38:
	s_add_u32 s34, s34, 0x20000
	s_addc_u32 s35, s35, 0
	global_load_lds_dwordx4 v224, s[34:35] sc1
	v_rcp_f32_e32 v207, v207
	v_mul_f32_e32 v206, v206, v142
	v_mfma_f32_32x32x16_f16 v[64:79], a[128:131], a[224:227], v[64:79]
	ds_read_b128 a[224:227], v193 offset:8192
	v_rcp_f32_e32 v208, v208
	v_mul_f32_e32 v207, v207, v143
	v_mfma_f32_32x32x16_f16 v[80:95], a[128:131], a[228:231], v[80:95]
	ds_read_b128 a[228:231], v193 offset:9216
	v_rcp_f32_e32 v209, v209
	v_fmamk_f32 v208, v208, 0xc0b8aa3b, v198
	s_waitcnt lgkmcnt(2)
	v_mfma_f32_32x32x16_f16 v[64:79], a[132:135], a[232:235], v[64:79]
	ds_read_b128 a[232:235], v193 offset:10240
	v_rcp_f32_e32 v210, v210
	v_fmamk_f32 v209, v209, 0xc0b8aa3b, v198
	v_fma_f32 v140, v200, v208, v204
	v_mfma_f32_32x32x16_f16 v[80:95], a[132:135], a[236:239], v[80:95]
	ds_read_b128 a[236:239], v193 offset:11264
	global_load_lds_dwordx4 v224, s[34:35] offset:1024 sc1
	v_rcp_f32_e32 v211, v211
	v_fmamk_f32 v210, v210, 0xc0b8aa3b, v198
	v_fma_f32 v141, v201, v209, v205
	v_mfma_f32_32x32x16_f16 v[64:79], a[136:139], a[240:243], v[64:79]
	ds_read_b128 a[240:243], v193 offset:12288
	v_rcp_f32_e32 v212, v212
	v_fmamk_f32 v211, v211, 0xc0b8aa3b, v198
	v_fma_f32 v142, v202, v210, v206
	v_mfma_f32_32x32x16_f16 v[80:95], a[136:139], a[244:247], v[80:95]
	ds_read_b128 a[244:247], v193 offset:13312
	v_rcp_f32_e32 v213, v213
	v_fma_f32 v143, v203, v211, v207
	v_mfma_f32_32x32x16_f16 v[64:79], a[140:143], a[248:251], v[64:79]
	ds_read_b128 a[248:251], v193 offset:14336
	v_rcp_f32_e32 v214, v214
	v_mfma_f32_32x32x16_f16 v[80:95], a[140:143], a[252:255], v[80:95]
	ds_read_b128 a[252:255], v193 offset:15360
	global_load_lds_dwordx4 v224, s[34:35] offset:2048 sc1
	v_rcp_f32_e32 v215, v215
	s_waitcnt lgkmcnt(2)
	v_mfma_f32_32x32x16_f16 v[64:79], a[144:147], a[224:227], v[64:79]
	ds_read_b128 a[224:227], v193 offset:16384
	v_exp_f32_e32 v200, v140
	v_mfma_f32_32x32x16_f16 v[80:95], a[144:147], a[228:231], v[80:95]
	ds_read_b128 a[228:231], v193 offset:17408
	v_exp_f32_e32 v201, v141
	v_add_f32_e32 v200, 1.0, v200
	v_mfma_f32_32x32x16_f16 v[64:79], a[148:151], a[232:235], v[64:79]
	ds_read_b128 a[232:235], v193 offset:18432
	v_exp_f32_e32 v202, v142
	v_add_f32_e32 v201, 1.0, v201
	v_mfma_f32_32x32x16_f16 v[80:95], a[148:151], a[236:239], v[80:95]
	ds_read_b128 a[236:239], v193 offset:19456
	global_load_lds_dwordx4 v224, s[34:35] offset:3072 sc1
	v_exp_f32_e32 v203, v143
	v_add_f32_e32 v202, 1.0, v202
	v_mfma_f32_32x32x16_f16 v[64:79], a[152:155], a[240:243], v[64:79]
	ds_read_b128 a[240:243], v193 offset:20480
	v_add_f32_e32 v203, 1.0, v203
	v_rcp_f32_e32 v200, v200
	v_mfma_f32_32x32x16_f16 v[80:95], a[152:155], a[244:247], v[80:95]
	ds_read_b128 a[244:247], v193 offset:21504
	v_rcp_f32_e32 v201, v201
	v_fma_f32 v200, v200, 2.0, -1.0
	s_waitcnt lgkmcnt(2)
	v_mfma_f32_32x32x16_f16 v[64:79], a[156:159], a[248:251], v[64:79]
	ds_read_b128 a[248:251], v193 offset:22528
	v_rcp_f32_e32 v202, v202
	v_fma_f32 v201, v201, 2.0, -1.0
	v_mul_f32_e32 v216, v212, v200
	s_mov_b32 m0, s53
	v_mfma_f32_32x32x16_f16 v[80:95], a[156:159], a[252:255], v[80:95]
	ds_read_b128 a[252:255], v193 offset:23552
	global_load_lds_dwordx4 v225, s[34:35] sc1
	v_rcp_f32_e32 v203, v203
	v_fma_f32 v202, v202, 2.0, -1.0
	v_mul_f32_e32 v217, v213, v201
	v_mfma_f32_32x32x16_f16 v[64:79], a[160:163], a[224:227], v[64:79]
	ds_read_b128 a[224:227], v193 offset:24576
	v_fma_f32 v203, v203, 2.0, -1.0
	v_mul_f32_e32 v218, v214, v202
	v_mfma_f32_32x32x16_f16 v[80:95], a[160:163], a[228:231], v[80:95]
	ds_read_b128 a[228:231], v193 offset:25600
	v_mul_f32_e32 v219, v215, v203
	v_cvt_pk_f16_f32 v222, v216, v217
	v_mfma_f32_32x32x16_f16 v[64:79], a[164:167], a[232:235], v[64:79]
	ds_read_b128 a[232:235], v193 offset:26624
	v_cvt_pk_f16_f32 v223, v218, v219
	v_mfma_f32_32x32x16_f16 v[80:95], a[164:167], a[236:239], v[80:95]
	ds_read_b128 a[236:239], v193 offset:27648
	global_load_lds_dwordx4 v225, s[34:35] offset:1024 sc1
	s_cmp_eq_u32 s33, s60
	s_cbranch_scc1 .LE_ht40
.LE_htb41:
	s_waitcnt lgkmcnt(2)
	v_mfma_f32_32x32x16_f16 v[64:79], a[168:171], a[240:243], v[64:79]
	ds_read_b128 a[240:243], v193 offset:28672
	s_nop 1
	v_permlane32_swap_b32_e32 v220, v222
	v_permlane32_swap_b32_e32 v221, v223
	s_cmp_eq_u32 s31, 0
	s_cbranch_scc1 .LE_slow42
	global_store_dwordx4 v195, v[220:223], s[36:37] offset:0
.LE_join43:
	v_mfma_f32_32x32x16_f16 v[80:95], a[168:171], a[244:247], v[80:95]
	ds_read_b128 a[244:247], v193 offset:29696
	v_mfma_f32_32x32x16_f16 v[64:79], a[172:175], a[248:251], v[64:79]
	ds_read_b128 a[248:251], v193 offset:30720
	v_mfma_f32_32x32x16_f16 v[80:95], a[172:175], a[252:255], v[80:95]
	ds_read_b128 a[252:255], v193 offset:31744
	global_load_lds_dwordx4 v225, s[34:35] offset:2048 sc1
	s_waitcnt vmcnt(8)
	s_barrier
	v_mfma_f32_32x32x16_f16 v[64:79], a[176:179], a[224:227], v[64:79]
	ds_read_b128 a[224:227], v193 offset:32768
	v_mfma_f32_32x32x16_f16 v[80:95], a[176:179], a[228:231], v[80:95]
	ds_read_b128 a[228:231], v193 offset:33792
	s_waitcnt lgkmcnt(2)
	v_mfma_f32_32x32x16_f16 v[64:79], a[180:183], a[232:235], v[64:79]
	ds_read_b128 a[232:235], v193 offset:34816
	v_mfma_f32_32x32x16_f16 v[80:95], a[180:183], a[236:239], v[80:95]
	ds_read_b128 a[236:239], v193 offset:35840
	global_load_lds_dwordx4 v225, s[34:35] offset:3072 sc1
	v_mfma_f32_32x32x16_f16 v[64:79], a[184:187], a[240:243], v[64:79]
	ds_read_b128 a[240:243], v193 offset:36864
	v_mfma_f32_32x32x16_f16 v[80:95], a[184:187], a[244:247], v[80:95]
	ds_read_b128 a[244:247], v193 offset:37888
	v_mfma_f32_32x32x16_f16 v[64:79], a[188:191], a[248:251], v[64:79]
	ds_read_b128 a[248:251], v193 offset:38912
	s_mov_b32 m0, s54
	v_mfma_f32_32x32x16_f16 v[80:95], a[188:191], a[252:255], v[80:95]
	ds_read_b128 a[252:255], v193 offset:39936
	global_load_lds_dwordx4 v226, s[34:35] sc1
	s_waitcnt lgkmcnt(2)
	v_mfma_f32_32x32x16_f16 v[64:79], a[192:195], a[224:227], v[64:79]
	ds_read_b128 a[224:227], v193 offset:40960
	v_mfma_f32_32x32x16_f16 v[80:95], a[192:195], a[228:231], v[80:95]
	ds_read_b128 a[228:231], v193 offset:41984
	s_waitcnt vmcnt(3)
	s_barrier
	v_mov_b32_e32 v199, 2
	s_cmp_eq_u32 s31, 0
	s_cbranch_scc1 .LE_slow44
	global_store_dword v197, v199, s[40:41]
.LE_join45:
	v_mfma_f32_32x32x16_f16 v[64:79], a[196:199], a[232:235], v[64:79]
	ds_read_b128 a[232:235], v193 offset:43008
	v_mfma_f32_32x32x16_f16 v[80:95], a[196:199], a[236:239], v[80:95]
	ds_read_b128 a[236:239], v193 offset:44032
	global_load_lds_dwordx4 v226, s[34:35] offset:1024 sc1
	v_mfma_f32_32x32x16_f16 v[64:79], a[200:203], a[240:243], v[64:79]
	ds_read_b128 a[240:243], v193 offset:45056
	v_mfma_f32_32x32x16_f16 v[80:95], a[200:203], a[244:247], v[80:95]
	ds_read_b128 a[244:247], v193 offset:46080
	s_and_b32 s64, s33, 1
	s_lshl_b32 s64, s64, 22
	s_add_u32 s64, s64, s50
	s_add_u32 s64, s64, 0x40000
	s_add_u32 s36, s6, s64
	s_addc_u32 s37, s7, 0
	s_lshl_b32 s64, s33, 3
	s_add_u32 s64, s64, s29
	s_lshl_b32 s64, s64, 5
	s_add_u32 s64, s64, s30
	s_lshl_b32 s64, s64, 2
	s_add_u32 s40, s8, s64
	s_addc_u32 s41, s9, 0
	s_lshl_b32 s64, s61, 11
	s_lshl_b32 s65, s29, 8
	s_add_u32 s64, s64, s65
	s_add_u32 s64, s64, 64
	s_lshl_b32 s64, s64, 3
	s_add_u32 s42, s12, s64
	s_addc_u32 s43, s13, 0
	s_waitcnt lgkmcnt(2)
	v_mfma_f32_32x32x16_f16 v[64:79], a[204:207], a[248:251], v[64:79]
	ds_read_b128 a[248:251], v193 offset:47104
	v_mfma_f32_32x32x16_f16 v[80:95], a[204:207], a[252:255], v[80:95]
	ds_read_b128 a[252:255], v193 offset:48128
	global_load_lds_dwordx4 v226, s[34:35] offset:2048 sc1
	v_mfma_f32_32x32x16_f16 v[64:79], a[208:211], a[224:227], v[64:79]
	ds_read_b128 a[224:227], v193 offset:49152
	v_mfma_f32_32x32x16_f16 v[80:95], a[208:211], a[228:231], v[80:95]
	ds_read_b128 a[228:231], v193 offset:50176
	v_mfma_f32_32x32x16_f16 v[64:79], a[212:215], a[232:235], v[64:79]
	ds_read_b128 a[232:235], v193 offset:51200
	v_mfma_f32_32x32x16_f16 v[80:95], a[212:215], a[236:239], v[80:95]
	ds_read_b128 a[236:239], v193 offset:52224
	global_load_lds_dwordx4 v226, s[34:35] offset:3072 sc1
	s_waitcnt lgkmcnt(2)
	v_mfma_f32_32x32x16_f16 v[64:79], a[216:219], a[240:243], v[64:79]
	ds_read_b128 a[240:243], v193 offset:53248
	v_mfma_f32_32x32x16_f16 v[80:95], a[216:219], a[244:247], v[80:95]
	ds_read_b128 a[244:247], v193 offset:54272
	v_mfma_f32_32x32x16_f16 v[64:79], a[220:223], a[248:251], v[64:79]
	ds_read_b128 a[248:251], v193 offset:55296
	s_mov_b32 m0, s55
	v_mfma_f32_32x32x16_f16 v[80:95], a[220:223], a[252:255], v[80:95]
	ds_read_b128 a[252:255], v193 offset:56320
	global_load_lds_dwordx4 v227, s[34:35] sc1
	v_mfma_f32_32x32x16_f16 v[64:79], v[160:163], a[224:227], v[64:79]
	ds_read_b128 a[224:227], v193 offset:57344
	v_mfma_f32_32x32x16_f16 v[80:95], v[160:163], a[228:231], v[80:95]
	ds_read_b128 a[228:231], v193 offset:58368
	s_waitcnt lgkmcnt(2)
	v_mfma_f32_32x32x16_f16 v[64:79], v[164:167], a[232:235], v[64:79]
	ds_read_b128 a[232:235], v193 offset:59392
	v_mfma_f32_32x32x16_f16 v[80:95], v[164:167], a[236:239], v[80:95]
	ds_read_b128 a[236:239], v193 offset:60416
	global_load_lds_dwordx4 v227, s[34:35] offset:1024 sc1
	v_mfma_f32_32x32x16_f16 v[64:79], v[168:171], a[240:243], v[64:79]
	ds_read_b128 a[240:243], v193 offset:61440
	v_mfma_f32_32x32x16_f16 v[80:95], v[168:171], a[244:247], v[80:95]
	ds_read_b128 a[244:247], v193 offset:62464
	v_mfma_f32_32x32x16_f16 v[64:79], v[172:175], a[248:251], v[64:79]
	ds_read_b128 a[248:251], v193 offset:63488
	v_mfma_f32_32x32x16_f16 v[80:95], v[172:175], a[252:255], v[80:95]
	ds_read_b128 a[252:255], v193 offset:64512
	global_load_lds_dwordx4 v227, s[34:35] offset:2048 sc1
	s_waitcnt vmcnt(8)
	s_barrier
	s_waitcnt lgkmcnt(2)
	v_mfma_f32_32x32x16_f16 v[64:79], v[176:179], a[224:227], v[64:79]
	ds_read_b128 a[224:227], v192 offset:0
	v_mfma_f32_32x32x16_f16 v[80:95], v[176:179], a[228:231], v[80:95]
	ds_read_b128 a[228:231], v192 offset:1024
	v_mfma_f32_32x32x16_f16 v[64:79], v[180:183], a[232:235], v[64:79]
	ds_read_b128 a[232:235], v192 offset:2048
	v_mfma_f32_32x32x16_f16 v[80:95], v[180:183], a[236:239], v[80:95]
	ds_read_b128 a[236:239], v192 offset:3072
	global_load_lds_dwordx4 v227, s[34:35] offset:3072 sc1
	v_mfma_f32_32x32x16_f16 v[64:79], v[184:187], a[240:243], v[64:79]
	ds_read_b128 a[240:243], v192 offset:4096
	v_mfma_f32_32x32x16_f16 v[80:95], v[184:187], a[244:247], v[80:95]
	ds_read_b128 a[244:247], v192 offset:5120
	s_waitcnt lgkmcnt(2)
	v_mfma_f32_32x32x16_f16 v[64:79], v[188:191], a[248:251], v[64:79]
	ds_read_b128 a[248:251], v192 offset:6144
	s_mov_b32 m0, s56
	v_mfma_f32_32x32x16_f16 v[80:95], v[188:191], a[252:255], v[80:95]
	ds_read_b128 a[252:255], v192 offset:7168
	global_load_lds_dwordx4 v252, s[34:35] sc1
	s_nop 5
	global_load_dword v228, v249, s[42:43] offset:0
	global_load_dword v229, v249, s[42:43] offset:256
	s_waitcnt lgkmcnt(2)
	v_mfma_f32_32x32x16_f16 v[96:111], a[0:3], a[224:227], v[96:111]
	ds_read_b128 a[224:227], v192 offset:8192
	v_exp_f32_e32 v200, v64
	v_mfma_f32_32x32x16_f16 v[112:127], a[0:3], a[228:231], v[112:127]
	ds_read_b128 a[228:231], v192 offset:9216
	s_lshl_b32 s64, s33, 3
	s_add_u32 s64, s64, s29
	s_lshl_b32 s64, s64, 7
	s_add_u32 s38, s8, s64
	s_addc_u32 s39, s9, 0
	global_load_dword v251, v196, s[38:39] sc1
	v_exp_f32_e32 v201, v65
	v_add_f32_e32 v200, 1.0, v200
	v_mfma_f32_32x32x16_f16 v[96:111], a[4:7], a[232:235], v[96:111]
	ds_read_b128 a[232:235], v192 offset:10240
	v_exp_f32_e32 v202, v66
	v_add_f32_e32 v201, 1.0, v201
	v_mfma_f32_32x32x16_f16 v[112:127], a[4:7], a[236:239], v[112:127]
	ds_read_b128 a[236:239], v192 offset:11264
	global_load_lds_dwordx4 v252, s[34:35] offset:1024 sc1
	v_exp_f32_e32 v203, v67
	v_add_f32_e32 v202, 1.0, v202
	v_mfma_f32_32x32x16_f16 v[96:111], a[8:11], a[240:243], v[96:111]
	ds_read_b128 a[240:243], v192 offset:12288
	v_exp_f32_e32 v204, v68
	v_add_f32_e32 v203, 1.0, v203
	v_mfma_f32_32x32x16_f16 v[112:127], a[8:11], a[244:247], v[112:127]
	ds_read_b128 a[244:247], v192 offset:13312
	v_exp_f32_e32 v205, v69
	v_add_f32_e32 v204, 1.0, v204
	s_waitcnt lgkmcnt(2)
	v_mfma_f32_32x32x16_f16 v[96:111], a[12:15], a[248:251], v[96:111]
	ds_read_b128 a[248:251], v192 offset:14336
	v_exp_f32_e32 v206, v70
	v_add_f32_e32 v205, 1.0, v205
	v_mfma_f32_32x32x16_f16 v[112:127], a[12:15], a[252:255], v[112:127]
	ds_read_b128 a[252:255], v192 offset:15360
	global_load_lds_dwordx4 v252, s[34:35] offset:2048 sc1
	v_exp_f32_e32 v207, v71
	v_add_f32_e32 v206, 1.0, v206
	v_mfma_f32_32x32x16_f16 v[96:111], a[16:19], a[224:227], v[96:111]
	ds_read_b128 a[224:227], v192 offset:16384
	v_exp_f32_e32 v208, v72
	v_add_f32_e32 v207, 1.0, v207
	v_mfma_f32_32x32x16_f16 v[112:127], a[16:19], a[228:231], v[112:127]
	ds_read_b128 a[228:231], v192 offset:17408
	v_exp_f32_e32 v209, v73
	v_add_f32_e32 v208, 1.0, v208
	v_mfma_f32_32x32x16_f16 v[96:111], a[20:23], a[232:235], v[96:111]
	ds_read_b128 a[232:235], v192 offset:18432
	v_exp_f32_e32 v210, v74
	v_add_f32_e32 v209, 1.0, v209
	v_mfma_f32_32x32x16_f16 v[112:127], a[20:23], a[236:239], v[112:127]
	ds_read_b128 a[236:239], v192 offset:19456
	global_load_lds_dwordx4 v252, s[34:35] offset:3072 sc1
	v_exp_f32_e32 v211, v75
	v_add_f32_e32 v210, 1.0, v210
	s_waitcnt lgkmcnt(2)
	v_mfma_f32_32x32x16_f16 v[96:111], a[24:27], a[240:243], v[96:111]
	ds_read_b128 a[240:243], v192 offset:20480
	v_exp_f32_e32 v212, v76
	v_add_f32_e32 v211, 1.0, v211
	v_mfma_f32_32x32x16_f16 v[112:127], a[24:27], a[244:247], v[112:127]
	ds_read_b128 a[244:247], v192 offset:21504
	v_exp_f32_e32 v213, v77
	v_add_f32_e32 v212, 1.0, v212
	v_mfma_f32_32x32x16_f16 v[96:111], a[28:31], a[248:251], v[96:111]
	ds_read_b128 a[248:251], v192 offset:22528
	v_exp_f32_e32 v214, v78
	v_add_f32_e32 v213, 1.0, v213
	s_mov_b32 m0, s57
	v_mfma_f32_32x32x16_f16 v[112:127], a[28:31], a[252:255], v[112:127]
	ds_read_b128 a[252:255], v192 offset:23552
	global_load_lds_dwordx4 v253, s[34:35] sc1
	v_exp_f32_e32 v215, v79
	v_add_f32_e32 v214, 1.0, v214
	v_mfma_f32_32x32x16_f16 v[96:111], a[32:35], a[224:227], v[96:111]
	ds_read_b128 a[224:227], v192 offset:24576
	v_add_f32_e32 v215, 1.0, v215
	v_rcp_f32_e32 v200, v200
	v_mfma_f32_32x32x16_f16 v[112:127], a[32:35], a[228:231], v[112:127]
	ds_read_b128 a[228:231], v192 offset:25600
	v_rcp_f32_e32 v201, v201
	s_waitcnt lgkmcnt(2)
	v_mfma_f32_32x32x16_f16 v[96:111], a[36:39], a[232:235], v[96:111]
	ds_read_b128 a[232:235], v192 offset:26624
	v_rcp_f32_e32 v202, v202
	v_mfma_f32_32x32x16_f16 v[112:127], a[36:39], a[236:239], v[112:127]
	ds_read_b128 a[236:239], v192 offset:27648
	global_load_lds_dwordx4 v253, s[34:35] offset:1024 sc1
	v_rcp_f32_e32 v203, v203
	v_mfma_f32_32x32x16_f16 v[96:111], a[40:43], a[240:243], v[96:111]
	ds_read_b128 a[240:243], v192 offset:28672
	v_rcp_f32_e32 v204, v204
	v_mfma_f32_32x32x16_f16 v[112:127], a[40:43], a[244:247], v[112:127]
	ds_read_b128 a[244:247], v192 offset:29696
	v_rcp_f32_e32 v205, v205
	v_mul_f32_e32 v204, v204, v144
	v_mfma_f32_32x32x16_f16 v[96:111], a[44:47], a[248:251], v[96:111]
	ds_read_b128 a[248:251], v192 offset:30720
	v_rcp_f32_e32 v206, v206
	v_mul_f32_e32 v205, v205, v145
	v_mfma_f32_32x32x16_f16 v[112:127], a[44:47], a[252:255], v[112:127]
	ds_read_b128 a[252:255], v192 offset:31744
	global_load_lds_dwordx4 v253, s[34:35] offset:2048 sc1
	v_rcp_f32_e32 v207, v207
	v_mul_f32_e32 v206, v206, v146
	s_waitcnt vmcnt(10)
	s_barrier
	s_waitcnt lgkmcnt(2)
	v_mfma_f32_32x32x16_f16 v[96:111], a[48:51], a[224:227], v[96:111]
	ds_read_b128 a[224:227], v192 offset:32768
	v_rcp_f32_e32 v208, v208
	v_mul_f32_e32 v207, v207, v147
	v_mfma_f32_32x32x16_f16 v[112:127], a[48:51], a[228:231], v[112:127]
	ds_read_b128 a[228:231], v192 offset:33792
	v_rcp_f32_e32 v209, v209
	v_fmamk_f32 v208, v208, 0xc0b8aa3b, v198
	v_mfma_f32_32x32x16_f16 v[96:111], a[52:55], a[232:235], v[96:111]
	ds_read_b128 a[232:235], v192 offset:34816
	v_rcp_f32_e32 v210, v210
	v_fmamk_f32 v209, v209, 0xc0b8aa3b, v198
	v_fma_f32 v144, v200, v208, v204
	v_mfma_f32_32x32x16_f16 v[112:127], a[52:55], a[236:239], v[112:127]
	ds_read_b128 a[236:239], v192 offset:35840
	global_load_lds_dwordx4 v253, s[34:35] offset:3072 sc1
	v_rcp_f32_e32 v211, v211
	v_fmamk_f32 v210, v210, 0xc0b8aa3b, v198
	v_fma_f32 v145, v201, v209, v205
	v_mfma_f32_32x32x16_f16 v[96:111], a[56:59], a[240:243], v[96:111]
	ds_read_b128 a[240:243], v192 offset:36864
	v_rcp_f32_e32 v212, v212
	v_fmamk_f32 v211, v211, 0xc0b8aa3b, v198
	v_fma_f32 v146, v202, v210, v206
	v_mfma_f32_32x32x16_f16 v[112:127], a[56:59], a[244:247], v[112:127]
	ds_read_b128 a[244:247], v192 offset:37888
	v_rcp_f32_e32 v213, v213
	v_fma_f32 v147, v203, v211, v207
	s_waitcnt lgkmcnt(2)
	v_mfma_f32_32x32x16_f16 v[96:111], a[60:63], a[248:251], v[96:111]
	ds_read_b128 a[248:251], v192 offset:38912
	v_rcp_f32_e32 v214, v214
	s_mov_b32 m0, s58
	v_mfma_f32_32x32x16_f16 v[112:127], a[60:63], a[252:255], v[112:127]
	ds_read_b128 a[252:255], v192 offset:39936
	global_load_lds_dwordx4 v254, s[34:35] sc1
	v_rcp_f32_e32 v215, v215
	v_mfma_f32_32x32x16_f16 v[96:111], a[64:67], a[224:227], v[96:111]
	ds_read_b128 a[224:227], v192 offset:40960
	v_exp_f32_e32 v200, v144
	v_mfma_f32_32x32x16_f16 v[112:127], a[64:67], a[228:231], v[112:127]
	ds_read_b128 a[228:231], v192 offset:41984
	v_exp_f32_e32 v201, v145
	v_add_f32_e32 v200, 1.0, v200
	v_mfma_f32_32x32x16_f16 v[96:111], a[68:71], a[232:235], v[96:111]
	ds_read_b128 a[232:235], v192 offset:43008
	v_exp_f32_e32 v202, v146
	v_add_f32_e32 v201, 1.0, v201
	v_mfma_f32_32x32x16_f16 v[112:127], a[68:71], a[236:239], v[112:127]
	ds_read_b128 a[236:239], v192 offset:44032
	global_load_lds_dwordx4 v254, s[34:35] offset:1024 sc1
	v_exp_f32_e32 v203, v147
	v_add_f32_e32 v202, 1.0, v202
	s_waitcnt lgkmcnt(2)
	v_mfma_f32_32x32x16_f16 v[96:111], a[72:75], a[240:243], v[96:111]
	ds_read_b128 a[240:243], v192 offset:45056
	v_add_f32_e32 v203, 1.0, v203
	v_rcp_f32_e32 v200, v200
	v_mfma_f32_32x32x16_f16 v[112:127], a[72:75], a[244:247], v[112:127]
	ds_read_b128 a[244:247], v192 offset:46080
	v_rcp_f32_e32 v201, v201
	v_fma_f32 v200, v200, 2.0, -1.0
	v_mfma_f32_32x32x16_f16 v[96:111], a[76:79], a[248:251], v[96:111]
	ds_read_b128 a[248:251], v192 offset:47104
	v_rcp_f32_e32 v202, v202
	v_fma_f32 v201, v201, 2.0, -1.0
	v_mul_f32_e32 v216, v212, v200
	v_mfma_f32_32x32x16_f16 v[112:127], a[76:79], a[252:255], v[112:127]
	ds_read_b128 a[252:255], v192 offset:48128
	global_load_lds_dwordx4 v254, s[34:35] offset:2048 sc1
	v_rcp_f32_e32 v203, v203
	v_fma_f32 v202, v202, 2.0, -1.0
	v_mul_f32_e32 v217, v213, v201
	v_mfma_f32_32x32x16_f16 v[96:111], a[80:83], a[224:227], v[96:111]
	ds_read_b128 a[224:227], v192 offset:49152
	v_fma_f32 v203, v203, 2.0, -1.0
	v_mul_f32_e32 v218, v214, v202
	v_exp_f32_e32 v200, v80
	v_mfma_f32_32x32x16_f16 v[112:127], a[80:83], a[228:231], v[112:127]
	ds_read_b128 a[228:231], v192 offset:50176
	v_mul_f32_e32 v219, v215, v203
	v_cvt_pk_f16_f32 v220, v216, v217
	v_exp_f32_e32 v201, v81
	s_waitcnt lgkmcnt(2)
	v_mfma_f32_32x32x16_f16 v[96:111], a[84:87], a[232:235], v[96:111]
	ds_read_b128 a[232:235], v192 offset:51200
	v_cvt_pk_f16_f32 v221, v218, v219
	v_exp_f32_e32 v202, v82
	v_add_f32_e32 v200, 1.0, v200
	v_mfma_f32_32x32x16_f16 v[112:127], a[84:87], a[236:239], v[112:127]
	ds_read_b128 a[236:239], v192 offset:52224
	global_load_lds_dwordx4 v254, s[34:35] offset:3072 sc1
	s_cmp_eq_u32 s33, s60
	s_cbranch_scc1 .LE_ht46
.LE_htb47:
	v_exp_f32_e32 v203, v83
	v_mfma_f32_32x32x16_f16 v[96:111], a[88:91], a[240:243], v[96:111]
	ds_read_b128 a[240:243], v192 offset:53248
	v_exp_f32_e32 v204, v84
	v_add_f32_e32 v201, 1.0, v201
	v_add_f32_e32 v202, 1.0, v202
	v_mfma_f32_32x32x16_f16 v[112:127], a[88:91], a[244:247], v[112:127]
	ds_read_b128 a[244:247], v192 offset:54272
	v_exp_f32_e32 v205, v85
	v_add_f32_e32 v203, 1.0, v203
	v_add_f32_e32 v204, 1.0, v204
	v_mfma_f32_32x32x16_f16 v[96:111], a[92:95], a[248:251], v[96:111]
	ds_read_b128 a[248:251], v192 offset:55296
	v_exp_f32_e32 v206, v86
	v_add_f32_e32 v205, 1.0, v205
	s_mov_b32 m0, s59
	v_mfma_f32_32x32x16_f16 v[112:127], a[92:95], a[252:255], v[112:127]
	ds_read_b128 a[252:255], v192 offset:56320
	global_load_lds_dwordx4 v255, s[34:35] sc1
	v_exp_f32_e32 v207, v87
	v_add_f32_e32 v206, 1.0, v206
	s_waitcnt lgkmcnt(2)
	v_mfma_f32_32x32x16_f16 v[96:111], a[96:99], a[224:227], v[96:111]
	ds_read_b128 a[224:227], v192 offset:57344
	v_exp_f32_e32 v208, v88
	v_add_f32_e32 v207, 1.0, v207
	v_mfma_f32_32x32x16_f16 v[112:127], a[96:99], a[228:231], v[112:127]
	ds_read_b128 a[228:231], v192 offset:58368
	v_exp_f32_e32 v209, v89
	v_add_f32_e32 v208, 1.0, v208
	v_mfma_f32_32x32x16_f16 v[96:111], a[100:103], a[232:235], v[96:111]
	ds_read_b128 a[232:235], v192 offset:59392
	v_exp_f32_e32 v210, v90
	v_add_f32_e32 v209, 1.0, v209
	v_mfma_f32_32x32x16_f16 v[112:127], a[100:103], a[236:239], v[112:127]
	ds_read_b128 a[236:239], v192 offset:60416
	global_load_lds_dwordx4 v255, s[34:35] offset:1024 sc1
	v_exp_f32_e32 v211, v91
	v_add_f32_e32 v210, 1.0, v210
	v_mfma_f32_32x32x16_f16 v[96:111], a[104:107], a[240:243], v[96:111]
	ds_read_b128 a[240:243], v192 offset:61440
	v_exp_f32_e32 v212, v92
	v_add_f32_e32 v211, 1.0, v211
	v_mfma_f32_32x32x16_f16 v[112:127], a[104:107], a[244:247], v[112:127]
	ds_read_b128 a[244:247], v192 offset:62464
	v_exp_f32_e32 v213, v93
	v_add_f32_e32 v212, 1.0, v212
	s_waitcnt lgkmcnt(2)
	v_mfma_f32_32x32x16_f16 v[96:111], a[108:111], a[248:251], v[96:111]
	ds_read_b128 a[248:251], v192 offset:63488
	v_exp_f32_e32 v214, v94
	v_add_f32_e32 v213, 1.0, v213
	v_mfma_f32_32x32x16_f16 v[112:127], a[108:111], a[252:255], v[112:127]
	ds_read_b128 a[252:255], v192 offset:64512
	global_load_lds_dwordx4 v255, s[34:35] offset:2048 sc1
	v_exp_f32_e32 v215, v95
	v_add_f32_e32 v214, 1.0, v214
	s_waitcnt vmcnt(7)
	s_barrier
	v_mfma_f32_32x32x16_f16 v[96:111], a[112:115], a[224:227], v[96:111]
	ds_read_b128 a[224:227], v193 offset:0
	v_add_f32_e32 v215, 1.0, v215
	v_rcp_f32_e32 v200, v200
	v_mfma_f32_32x32x16_f16 v[112:127], a[112:115], a[228:231], v[112:127]
	ds_read_b128 a[228:231], v193 offset:1024
	v_rcp_f32_e32 v201, v201
	v_mfma_f32_32x32x16_f16 v[96:111], a[116:119], a[232:235], v[96:111]
	ds_read_b128 a[232:235], v193 offset:2048
	v_rcp_f32_e32 v202, v202
	v_mfma_f32_32x32x16_f16 v[112:127], a[116:119], a[236:239], v[112:127]
	ds_read_b128 a[236:239], v193 offset:3072
	global_load_lds_dwordx4 v255, s[34:35] offset:3072 sc1
	v_rcp_f32_e32 v203, v203
	s_waitcnt lgkmcnt(2)
	v_mfma_f32_32x32x16_f16 v[96:111], a[120:123], a[240:243], v[96:111]
	ds_read_b128 a[240:243], v193 offset:4096
	v_rcp_f32_e32 v204, v204
	v_mfma_f32_32x32x16_f16 v[112:127], a[120:123], a[244:247], v[112:127]
	ds_read_b128 a[244:247], v193 offset:5120
	v_rcp_f32_e32 v205, v205
	v_mul_f32_e32 v204, v204, v148
	v_mfma_f32_32x32x2_f32 v[32:47], v248, v228, v[232:247]
	v_mfma_f32_32x32x16_f16 v[96:111], a[124:127], a[248:251], v[96:111]
	ds_read_b128 a[248:251], v193 offset:6144
	v_rcp_f32_e32 v206, v206
	v_mul_f32_e32 v205, v205, v149
	v_mfma_f32_32x32x2_f32 v[48:63], v248, v229, v[232:247]
	s_mov_b32 m0, s52
	v_mfma_f32_32x32x16_f16 v[112:127], a[124:127], a[252:255], v[112:127]
	ds_read_b128 a[252:255], v193 offset:7168
	v_cmp_gt_u32_e32 vcc, 1, v251
	s_cbranch_vccnz .LE_tpoll49
.LE_tok48:
	s_and_b32 s64, s33, 1
	s_lshl_b32 s64, s64, 22
	s_add_u32 s64, s64, s49
	s_add_u32 s34, s6, s64
	s_addc_u32 s35, s7, 0
	global_load_lds_dwordx4 v224, s[34:35] sc1
	v_rcp_f32_e32 v207, v207
	v_mul_f32_e32 v206, v206, v150
	v_mfma_f32_32x32x16_f16 v[96:111], a[128:131], a[224:227], v[96:111]
	ds_read_b128 a[224:227], v193 offset:8192
	v_rcp_f32_e32 v208, v208
	v_mul_f32_e32 v207, v207, v151
	v_mfma_f32_32x32x16_f16 v[112:127], a[128:131], a[228:231], v[112:127]
	ds_read_b128 a[228:231], v193 offset:9216
	v_rcp_f32_e32 v209, v209
	v_fmamk_f32 v208, v208, 0xc0b8aa3b, v198
	s_waitcnt lgkmcnt(2)
	v_mfma_f32_32x32x16_f16 v[96:111], a[132:135], a[232:235], v[96:111]
	ds_read_b128 a[232:235], v193 offset:10240
	v_rcp_f32_e32 v210, v210
	v_fmamk_f32 v209, v209, 0xc0b8aa3b, v198
	v_fma_f32 v148, v200, v208, v204
	v_mfma_f32_32x32x16_f16 v[112:127], a[132:135], a[236:239], v[112:127]
	ds_read_b128 a[236:239], v193 offset:11264
	global_load_lds_dwordx4 v224, s[34:35] offset:1024 sc1
	v_rcp_f32_e32 v211, v211
	v_fmamk_f32 v210, v210, 0xc0b8aa3b, v198
	v_fma_f32 v149, v201, v209, v205
	v_mfma_f32_32x32x16_f16 v[96:111], a[136:139], a[240:243], v[96:111]
	ds_read_b128 a[240:243], v193 offset:12288
	v_rcp_f32_e32 v212, v212
	v_fmamk_f32 v211, v211, 0xc0b8aa3b, v198
	v_fma_f32 v150, v202, v210, v206
	v_mfma_f32_32x32x16_f16 v[112:127], a[136:139], a[244:247], v[112:127]
	ds_read_b128 a[244:247], v193 offset:13312
	v_rcp_f32_e32 v213, v213
	v_fma_f32 v151, v203, v211, v207
	v_mfma_f32_32x32x16_f16 v[96:111], a[140:143], a[248:251], v[96:111]
	ds_read_b128 a[248:251], v193 offset:14336
	v_rcp_f32_e32 v214, v214
	v_mfma_f32_32x32x16_f16 v[112:127], a[140:143], a[252:255], v[112:127]
	ds_read_b128 a[252:255], v193 offset:15360
	global_load_lds_dwordx4 v224, s[34:35] offset:2048 sc1
	v_rcp_f32_e32 v215, v215
	s_waitcnt lgkmcnt(2)
	v_mfma_f32_32x32x16_f16 v[96:111], a[144:147], a[224:227], v[96:111]
	ds_read_b128 a[224:227], v193 offset:16384
	v_exp_f32_e32 v200, v148
	v_mfma_f32_32x32x16_f16 v[112:127], a[144:147], a[228:231], v[112:127]
	ds_read_b128 a[228:231], v193 offset:17408
	v_exp_f32_e32 v201, v149
	v_add_f32_e32 v200, 1.0, v200
	v_mfma_f32_32x32x16_f16 v[96:111], a[148:151], a[232:235], v[96:111]
	ds_read_b128 a[232:235], v193 offset:18432
	v_exp_f32_e32 v202, v150
	v_add_f32_e32 v201, 1.0, v201
	v_mfma_f32_32x32x16_f16 v[112:127], a[148:151], a[236:239], v[112:127]
	ds_read_b128 a[236:239], v193 offset:19456
	global_load_lds_dwordx4 v224, s[34:35] offset:3072 sc1
	v_exp_f32_e32 v203, v151
	v_add_f32_e32 v202, 1.0, v202
	v_mfma_f32_32x32x16_f16 v[96:111], a[152:155], a[240:243], v[96:111]
	ds_read_b128 a[240:243], v193 offset:20480
	v_add_f32_e32 v203, 1.0, v203
	v_rcp_f32_e32 v200, v200
	v_mfma_f32_32x32x16_f16 v[112:127], a[152:155], a[244:247], v[112:127]
	ds_read_b128 a[244:247], v193 offset:21504
	v_rcp_f32_e32 v201, v201
	v_fma_f32 v200, v200, 2.0, -1.0
	s_waitcnt lgkmcnt(2)
	v_mfma_f32_32x32x16_f16 v[96:111], a[156:159], a[248:251], v[96:111]
	ds_read_b128 a[248:251], v193 offset:22528
	v_rcp_f32_e32 v202, v202
	v_fma_f32 v201, v201, 2.0, -1.0
	v_mul_f32_e32 v216, v212, v200
	s_mov_b32 m0, s53
	v_mfma_f32_32x32x16_f16 v[112:127], a[156:159], a[252:255], v[112:127]
	ds_read_b128 a[252:255], v193 offset:23552
	global_load_lds_dwordx4 v225, s[34:35] sc1
	v_rcp_f32_e32 v203, v203
	v_fma_f32 v202, v202, 2.0, -1.0
	v_mul_f32_e32 v217, v213, v201
	v_mfma_f32_32x32x16_f16 v[96:111], a[160:163], a[224:227], v[96:111]
	ds_read_b128 a[224:227], v193 offset:24576
	v_fma_f32 v203, v203, 2.0, -1.0
	v_mul_f32_e32 v218, v214, v202
	v_mfma_f32_32x32x16_f16 v[112:127], a[160:163], a[228:231], v[112:127]
	ds_read_b128 a[228:231], v193 offset:25600
	v_mul_f32_e32 v219, v215, v203
	v_cvt_pk_f16_f32 v222, v216, v217
	v_mfma_f32_32x32x16_f16 v[96:111], a[164:167], a[232:235], v[96:111]
	ds_read_b128 a[232:235], v193 offset:26624
	v_cvt_pk_f16_f32 v223, v218, v219
	v_mfma_f32_32x32x16_f16 v[112:127], a[164:167], a[236:239], v[112:127]
	ds_read_b128 a[236:239], v193 offset:27648
	global_load_lds_dwordx4 v225, s[34:35] offset:1024 sc1
	s_cmp_eq_u32 s33, s60
	s_cbranch_scc1 .LE_ht50
.LE_htb51:
	s_waitcnt lgkmcnt(2)
	v_mfma_f32_32x32x16_f16 v[96:111], a[168:171], a[240:243], v[96:111]
	ds_read_b128 a[240:243], v193 offset:28672
	s_nop 1
	v_permlane32_swap_b32_e32 v220, v222
	v_permlane32_swap_b32_e32 v221, v223
	s_cmp_eq_u32 s31, 0
	s_cbranch_scc1 .LE_slow52
	global_store_dwordx4 v195, v[220:223], s[36:37] offset:0
.LE_join53:
	v_mfma_f32_32x32x16_f16 v[112:127], a[168:171], a[244:247], v[112:127]
	ds_read_b128 a[244:247], v193 offset:29696
	v_mfma_f32_32x32x16_f16 v[96:111], a[172:175], a[248:251], v[96:111]
	ds_read_b128 a[248:251], v193 offset:30720
	v_mfma_f32_32x32x16_f16 v[112:127], a[172:175], a[252:255], v[112:127]
	ds_read_b128 a[252:255], v193 offset:31744
	global_load_lds_dwordx4 v225, s[34:35] offset:2048 sc1
	s_waitcnt vmcnt(8)
	s_barrier
	v_mfma_f32_32x32x16_f16 v[96:111], a[176:179], a[224:227], v[96:111]
	ds_read_b128 a[224:227], v193 offset:32768
	v_mfma_f32_32x32x16_f16 v[112:127], a[176:179], a[228:231], v[112:127]
	ds_read_b128 a[228:231], v193 offset:33792
	s_waitcnt lgkmcnt(2)
	v_mfma_f32_32x32x16_f16 v[96:111], a[180:183], a[232:235], v[96:111]
	ds_read_b128 a[232:235], v193 offset:34816
	v_mfma_f32_32x32x16_f16 v[112:127], a[180:183], a[236:239], v[112:127]
	ds_read_b128 a[236:239], v193 offset:35840
	global_load_lds_dwordx4 v225, s[34:35] offset:3072 sc1
	v_mfma_f32_32x32x16_f16 v[96:111], a[184:187], a[240:243], v[96:111]
	ds_read_b128 a[240:243], v193 offset:36864
	v_mfma_f32_32x32x16_f16 v[112:127], a[184:187], a[244:247], v[112:127]
	ds_read_b128 a[244:247], v193 offset:37888
	v_mfma_f32_32x32x16_f16 v[96:111], a[188:191], a[248:251], v[96:111]
	ds_read_b128 a[248:251], v193 offset:38912
	s_mov_b32 m0, s54
	v_mfma_f32_32x32x16_f16 v[112:127], a[188:191], a[252:255], v[112:127]
	ds_read_b128 a[252:255], v193 offset:39936
	global_load_lds_dwordx4 v226, s[34:35] sc1
	s_waitcnt lgkmcnt(2)
	v_mfma_f32_32x32x16_f16 v[96:111], a[192:195], a[224:227], v[96:111]
	ds_read_b128 a[224:227], v193 offset:40960
	v_mfma_f32_32x32x16_f16 v[112:127], a[192:195], a[228:231], v[112:127]
	ds_read_b128 a[228:231], v193 offset:41984
	s_waitcnt vmcnt(3)
	s_barrier
	v_mov_b32_e32 v199, 3
	s_cmp_eq_u32 s31, 0
	s_cbranch_scc1 .LE_slow54
	global_store_dword v197, v199, s[40:41]
.LE_join55:
	v_mfma_f32_32x32x16_f16 v[96:111], a[196:199], a[232:235], v[96:111]
	ds_read_b128 a[232:235], v193 offset:43008
	v_mfma_f32_32x32x16_f16 v[112:127], a[196:199], a[236:239], v[112:127]
	ds_read_b128 a[236:239], v193 offset:44032
	global_load_lds_dwordx4 v226, s[34:35] offset:1024 sc1
	v_mfma_f32_32x32x16_f16 v[96:111], a[200:203], a[240:243], v[96:111]
	ds_read_b128 a[240:243], v193 offset:45056
	v_mfma_f32_32x32x16_f16 v[112:127], a[200:203], a[244:247], v[112:127]
	ds_read_b128 a[244:247], v193 offset:46080
	s_waitcnt lgkmcnt(2)
	v_mfma_f32_32x32x16_f16 v[96:111], a[204:207], a[248:251], v[96:111]
	ds_read_b128 a[248:251], v193 offset:47104
	v_mfma_f32_32x32x16_f16 v[112:127], a[204:207], a[252:255], v[112:127]
	ds_read_b128 a[252:255], v193 offset:48128
	global_load_lds_dwordx4 v226, s[34:35] offset:2048 sc1
	v_mfma_f32_32x32x16_f16 v[96:111], a[208:211], a[224:227], v[96:111]
	ds_read_b128 a[224:227], v193 offset:49152
	v_mfma_f32_32x32x16_f16 v[112:127], a[208:211], a[228:231], v[112:127]
	ds_read_b128 a[228:231], v193 offset:50176
	v_mfma_f32_32x32x16_f16 v[96:111], a[212:215], a[232:235], v[96:111]
	ds_read_b128 a[232:235], v193 offset:51200
	v_mfma_f32_32x32x16_f16 v[112:127], a[212:215], a[236:239], v[112:127]
	ds_read_b128 a[236:239], v193 offset:52224
	global_load_lds_dwordx4 v226, s[34:35] offset:3072 sc1
	s_waitcnt lgkmcnt(2)
	v_mfma_f32_32x32x16_f16 v[96:111], a[216:219], a[240:243], v[96:111]
	ds_read_b128 a[240:243], v193 offset:53248
	v_mfma_f32_32x32x16_f16 v[112:127], a[216:219], a[244:247], v[112:127]
	ds_read_b128 a[244:247], v193 offset:54272
	v_mfma_f32_32x32x16_f16 v[96:111], a[220:223], a[248:251], v[96:111]
	ds_read_b128 a[248:251], v193 offset:55296
	s_mov_b32 m0, s55
	v_mfma_f32_32x32x16_f16 v[112:127], a[220:223], a[252:255], v[112:127]
	ds_read_b128 a[252:255], v193 offset:56320
	global_load_lds_dwordx4 v227, s[34:35] sc1
	v_mfma_f32_32x32x16_f16 v[96:111], v[160:163], a[224:227], v[96:111]
	ds_read_b128 a[224:227], v193 offset:57344
	v_mfma_f32_32x32x16_f16 v[112:127], v[160:163], a[228:231], v[112:127]
	ds_read_b128 a[228:231], v193 offset:58368
	s_waitcnt lgkmcnt(2)
	v_mfma_f32_32x32x16_f16 v[96:111], v[164:167], a[232:235], v[96:111]
	ds_read_b128 a[232:235], v193 offset:59392
	v_mfma_f32_32x32x16_f16 v[112:127], v[164:167], a[236:239], v[112:127]
	ds_read_b128 a[236:239], v193 offset:60416
	global_load_lds_dwordx4 v227, s[34:35] offset:1024 sc1
	v_mfma_f32_32x32x16_f16 v[96:111], v[168:171], a[240:243], v[96:111]
	ds_read_b128 a[240:243], v193 offset:61440
	v_mfma_f32_32x32x16_f16 v[112:127], v[168:171], a[244:247], v[112:127]
	ds_read_b128 a[244:247], v193 offset:62464
	v_mfma_f32_32x32x16_f16 v[96:111], v[172:175], a[248:251], v[96:111]
	ds_read_b128 a[248:251], v193 offset:63488
	v_mfma_f32_32x32x16_f16 v[112:127], v[172:175], a[252:255], v[112:127]
	ds_read_b128 a[252:255], v193 offset:64512
	global_load_lds_dwordx4 v227, s[34:35] offset:2048 sc1
	s_waitcnt vmcnt(8)
	s_barrier
	s_waitcnt lgkmcnt(2)
	v_mfma_f32_32x32x16_f16 v[96:111], v[176:179], a[224:227], v[96:111]
	ds_read_b128 a[224:227], v192 offset:0
	v_mfma_f32_32x32x16_f16 v[112:127], v[176:179], a[228:231], v[112:127]
	ds_read_b128 a[228:231], v192 offset:1024
	v_mfma_f32_32x32x16_f16 v[96:111], v[180:183], a[232:235], v[96:111]
	ds_read_b128 a[232:235], v192 offset:2048
	v_mfma_f32_32x32x16_f16 v[112:127], v[180:183], a[236:239], v[112:127]
	ds_read_b128 a[236:239], v192 offset:3072
	global_load_lds_dwordx4 v227, s[34:35] offset:3072 sc1
	v_mfma_f32_32x32x16_f16 v[96:111], v[184:187], a[240:243], v[96:111]
	ds_read_b128 a[240:243], v192 offset:4096
	v_mfma_f32_32x32x16_f16 v[112:127], v[184:187], a[244:247], v[112:127]
	ds_read_b128 a[244:247], v192 offset:5120
	s_waitcnt lgkmcnt(2)
	v_mfma_f32_32x32x16_f16 v[96:111], v[188:191], a[248:251], v[96:111]
	ds_read_b128 a[248:251], v192 offset:6144
	s_mov_b32 m0, s56
	v_mfma_f32_32x32x16_f16 v[112:127], v[188:191], a[252:255], v[112:127]
	ds_read_b128 a[252:255], v192 offset:7168
	global_load_lds_dwordx4 v252, s[34:35] sc1
	s_add_u32 s33, s33, 1
	s_cmp_lt_u32 s33, s28
	s_cbranch_scc1 .LE_loop16

.LD_cdone1:
	s_waitcnt lgkmcnt(0)
	s_barrier
	v_mov_b32_e32 v252, 0x22000
	ds_read_b32 v200, v252
	ds_read_b32 v201, v252 offset:4
	ds_read_b32 v202, v252 offset:8
	s_waitcnt lgkmcnt(0)
	s_nop 1
	v_readfirstlane_b32 s31, v200
	v_readfirstlane_b32 s29, v201
	v_readfirstlane_b32 s30, v202
	s_nop 3
	s_barrier
	s_lshl_b32 s49, s29, 19
	s_lshl_b32 s64, s32, 13
	s_add_u32 s49, s49, s64
	s_mov_b32 s51, s64
	s_add_u32 s52, s51, 0x0
	s_add_u32 s53, s51, 0x1000
	s_add_u32 s54, s51, 0x8000
	s_add_u32 s55, s51, 0x9000
	s_add_u32 s56, s51, 0x10000
	s_add_u32 s57, s51, 0x11000
	s_add_u32 s58, s51, 0x18000
	s_add_u32 s59, s51, 0x19000
	s_lshl_b32 s64, s29, 8
	s_lshl_b32 s65, s30, 1
	s_add_u32 s64, s64, s65
	s_lshr_b32 s65, s32, 1
	s_add_u32 s64, s64, s65
	s_lshl_b32 s64, s64, 11
	s_and_b32 s65, s32, 1
	s_lshl_b32 s65, s65, 9
	s_add_u32 s50, s64, s65
	s_sub_u32 s60, s28, 1
	s_lshl_b32 s64, s30, 2
	s_add_u32 s64, s64, s32
	s_lshl_b32 s64, s64, 16
	s_add_u32 s44, s4, s64
	s_addc_u32 s45, s5, 0
	global_load_dwordx4 a[0:3], v192, s[44:45] offset:0
	global_load_dwordx4 a[4:7], v192, s[44:45] offset:1024
	global_load_dwordx4 a[8:11], v192, s[44:45] offset:2048
	global_load_dwordx4 a[12:15], v192, s[44:45] offset:3072
	s_add_u32 s44, s44, 0x1000
	s_addc_u32 s45, s45, 0
	global_load_dwordx4 a[16:19], v192, s[44:45] offset:0
	global_load_dwordx4 a[20:23], v192, s[44:45] offset:1024
	global_load_dwordx4 a[24:27], v192, s[44:45] offset:2048
	global_load_dwordx4 a[28:31], v192, s[44:45] offset:3072
	s_add_u32 s44, s44, 0x1000
	s_addc_u32 s45, s45, 0
	global_load_dwordx4 a[32:35], v192, s[44:45] offset:0
	global_load_dwordx4 a[36:39], v192, s[44:45] offset:1024
	global_load_dwordx4 a[40:43], v192, s[44:45] offset:2048
	global_load_dwordx4 a[44:47], v192, s[44:45] offset:3072
	s_add_u32 s44, s44, 0x1000
	s_addc_u32 s45, s45, 0
	global_load_dwordx4 a[48:51], v192, s[44:45] offset:0
	global_load_dwordx4 a[52:55], v192, s[44:45] offset:1024
	global_load_dwordx4 a[56:59], v192, s[44:45] offset:2048
	global_load_dwordx4 a[60:63], v192, s[44:45] offset:3072
	s_add_u32 s44, s44, 0x1000
	s_addc_u32 s45, s45, 0
	global_load_dwordx4 a[64:67], v192, s[44:45] offset:0
	global_load_dwordx4 a[68:71], v192, s[44:45] offset:1024
	global_load_dwordx4 a[72:75], v192, s[44:45] offset:2048
	global_load_dwordx4 a[76:79], v192, s[44:45] offset:3072
	s_add_u32 s44, s44, 0x1000
	s_addc_u32 s45, s45, 0
	global_load_dwordx4 a[80:83], v192, s[44:45] offset:0
	global_load_dwordx4 a[84:87], v192, s[44:45] offset:1024
	global_load_dwordx4 a[88:91], v192, s[44:45] offset:2048
	global_load_dwordx4 a[92:95], v192, s[44:45] offset:3072
	s_add_u32 s44, s44, 0x1000
	s_addc_u32 s45, s45, 0
	global_load_dwordx4 a[96:99], v192, s[44:45] offset:0
	global_load_dwordx4 a[100:103], v192, s[44:45] offset:1024
	global_load_dwordx4 a[104:107], v192, s[44:45] offset:2048
	global_load_dwordx4 a[108:111], v192, s[44:45] offset:3072
	s_add_u32 s44, s44, 0x1000
	s_addc_u32 s45, s45, 0
	global_load_dwordx4 a[112:115], v192, s[44:45] offset:0
	global_load_dwordx4 a[116:119], v192, s[44:45] offset:1024
	global_load_dwordx4 a[120:123], v192, s[44:45] offset:2048
	global_load_dwordx4 a[124:127], v192, s[44:45] offset:3072
	s_add_u32 s44, s44, 0x1000
	s_addc_u32 s45, s45, 0
	s_waitcnt vmcnt(16)
	global_load_dwordx4 a[128:131], v192, s[44:45] offset:0
	global_load_dwordx4 a[132:135], v192, s[44:45] offset:1024
	global_load_dwordx4 a[136:139], v192, s[44:45] offset:2048
	global_load_dwordx4 a[140:143], v192, s[44:45] offset:3072
	s_add_u32 s44, s44, 0x1000
	s_addc_u32 s45, s45, 0
	global_load_dwordx4 a[144:147], v192, s[44:45] offset:0
	global_load_dwordx4 a[148:151], v192, s[44:45] offset:1024
	global_load_dwordx4 a[152:155], v192, s[44:45] offset:2048
	global_load_dwordx4 a[156:159], v192, s[44:45] offset:3072
	s_add_u32 s44, s44, 0x1000
	s_addc_u32 s45, s45, 0
	global_load_dwordx4 a[160:163], v192, s[44:45] offset:0
	global_load_dwordx4 a[164:167], v192, s[44:45] offset:1024
	global_load_dwordx4 a[168:171], v192, s[44:45] offset:2048
	global_load_dwordx4 a[172:175], v192, s[44:45] offset:3072
	s_add_u32 s44, s44, 0x1000
	s_addc_u32 s45, s45, 0
	global_load_dwordx4 a[176:179], v192, s[44:45] offset:0
	global_load_dwordx4 a[180:183], v192, s[44:45] offset:1024
	global_load_dwordx4 a[184:187], v192, s[44:45] offset:2048
	global_load_dwordx4 a[188:191], v192, s[44:45] offset:3072
	s_add_u32 s44, s44, 0x1000
	s_addc_u32 s45, s45, 0
	global_load_dwordx4 a[192:195], v192, s[44:45] offset:0
	global_load_dwordx4 a[196:199], v192, s[44:45] offset:1024
	global_load_dwordx4 a[200:203], v192, s[44:45] offset:2048
	global_load_dwordx4 a[204:207], v192, s[44:45] offset:3072
	s_add_u32 s44, s44, 0x1000
	s_addc_u32 s45, s45, 0
	global_load_dwordx4 a[208:211], v192, s[44:45] offset:0
	global_load_dwordx4 a[212:215], v192, s[44:45] offset:1024
	global_load_dwordx4 a[216:219], v192, s[44:45] offset:2048
	global_load_dwordx4 a[220:223], v192, s[44:45] offset:3072
	s_add_u32 s44, s44, 0x1000
	s_addc_u32 s45, s45, 0
	global_load_dwordx4 v[160:163], v192, s[44:45] offset:0
	global_load_dwordx4 v[164:167], v192, s[44:45] offset:1024
	global_load_dwordx4 v[168:171], v192, s[44:45] offset:2048
	global_load_dwordx4 v[172:175], v192, s[44:45] offset:3072
	s_add_u32 s44, s44, 0x1000
	s_addc_u32 s45, s45, 0
	global_load_dwordx4 v[176:179], v192, s[44:45] offset:0
	global_load_dwordx4 v[180:183], v192, s[44:45] offset:1024
	global_load_dwordx4 v[184:187], v192, s[44:45] offset:2048
	global_load_dwordx4 v[188:191], v192, s[44:45] offset:3072
	s_add_u32 s44, s44, 0x1000
	s_addc_u32 s45, s45, 0
	v_mov_b32_e32 v128, 0
	v_mov_b32_e32 v129, 0
	v_mov_b32_e32 v130, 0
	v_mov_b32_e32 v131, 0
	v_mov_b32_e32 v132, 0
	v_mov_b32_e32 v133, 0
	v_mov_b32_e32 v134, 0
	v_mov_b32_e32 v135, 0
	v_mov_b32_e32 v136, 0
	v_mov_b32_e32 v137, 0
	v_mov_b32_e32 v138, 0
	v_mov_b32_e32 v139, 0
	v_mov_b32_e32 v140, 0
	v_mov_b32_e32 v141, 0
	v_mov_b32_e32 v142, 0
	v_mov_b32_e32 v143, 0
	v_mov_b32_e32 v144, 0
	v_mov_b32_e32 v145, 0
	v_mov_b32_e32 v146, 0
	v_mov_b32_e32 v147, 0
	v_mov_b32_e32 v148, 0
	v_mov_b32_e32 v149, 0
	v_mov_b32_e32 v150, 0
	v_mov_b32_e32 v151, 0
	v_mov_b32_e32 v152, 0
	v_mov_b32_e32 v153, 0
	v_mov_b32_e32 v154, 0
	v_mov_b32_e32 v155, 0
	v_mov_b32_e32 v156, 0
	v_mov_b32_e32 v157, 0
	v_mov_b32_e32 v158, 0
	v_mov_b32_e32 v159, 0
	s_lshl_b32 s64, s30, 5
	s_lshl_b32 s65, s32, 3
	s_add_u32 s64, s64, s65
	v_lshlrev_b32_e32 v255, 2, v254
	v_add_u32_e32 v255, s64, v255
	v_lshlrev_b32_e32 v200, 2, v255
	global_load_dwordx4 v[228:231], v200, s[22:23]
	v_add_u32_e32 v201, 0x1000, v200
	global_load_dwordx4 v[232:235], v201, s[22:23]
	s_lshl_b32 s65, s32, 11
	v_lshl_add_u32 v248, v253, 3, s65
	v_add_u32_e32 v248, 0x20000, v248
	v_and_b32_e32 v250, 15, v194
	s_mul_i32 s65, s32, 128
	v_lshl_add_u32 v249, v250, 3, s65
	v_add_u32_e32 v249, 0x20000, v249
	v_lshlrev_b32_e32 v250, 3, v250
	s_lshl_b32 s65, s30, 11
	s_lshl_b32 s66, s29, 8
	s_add_u32 s65, s65, s66
	s_mul_i32 s66, s32, 16
	s_add_u32 s65, s65, s66
	s_lshl_b32 s65, s65, 3
	s_add_u32 s62, s24, s65
	s_addc_u32 s63, s25, 0
	s_lshl_b32 s65, s29, 5
	s_add_u32 s65, s65, s30
	s_lshl_b32 s65, s65, 2
	s_add_u32 s65, s65, s32
	s_lshl_b32 s65, s65, 15
	s_add_u32 s42, s18, s65
	s_addc_u32 s43, s19, 0
	s_waitcnt vmcnt(0)
	s_waitcnt vmcnt(0)
	v_add_u32_e32 v224, 0x0, v192
	v_add_u32_e32 v225, 0x1000, v192
	v_add_u32_e32 v226, 0x8000, v192
	v_add_u32_e32 v227, 0x9000, v192
	v_add_u32_e32 v242, 0x10000, v192
	v_add_u32_e32 v243, 0x11000, v192
	v_add_u32_e32 v244, 0x18000, v192
	v_add_u32_e32 v245, 0x19000, v192
	s_mov_b32 s33, 0
	s_add_u32 s46, s42, 0x0
	s_addc_u32 s47, s43, 0
	global_load_dwordx4 v[0:3], v192, s[46:47] offset:0
	global_load_dwordx4 v[4:7], v192, s[46:47] offset:1024
	global_load_dwordx4 v[8:11], v192, s[46:47] offset:2048
	global_load_dwordx4 v[12:15], v192, s[46:47] offset:3072
	s_add_u32 s46, s42, 0x1000
	s_addc_u32 s47, s43, 0
	global_load_dwordx4 v[16:19], v192, s[46:47] offset:0
	global_load_dwordx4 v[20:23], v192, s[46:47] offset:1024
	global_load_dwordx4 v[24:27], v192, s[46:47] offset:2048
	global_load_dwordx4 v[28:31], v192, s[46:47] offset:3072
	s_add_u32 s46, s42, 0x2000
	s_addc_u32 s47, s43, 0
	global_load_dwordx4 v[32:35], v192, s[46:47] offset:0
	global_load_dwordx4 v[36:39], v192, s[46:47] offset:1024
	global_load_dwordx4 v[40:43], v192, s[46:47] offset:2048
	global_load_dwordx4 v[44:47], v192, s[46:47] offset:3072
	s_add_u32 s46, s42, 0x3000
	s_addc_u32 s47, s43, 0
	global_load_dwordx4 v[48:51], v192, s[46:47] offset:0
	global_load_dwordx4 v[52:55], v192, s[46:47] offset:1024
	global_load_dwordx4 v[56:59], v192, s[46:47] offset:2048
	global_load_dwordx4 v[60:63], v192, s[46:47] offset:3072
	s_add_u32 s46, s42, 0x4000
	s_addc_u32 s47, s43, 0
	global_load_dwordx4 v[64:67], v192, s[46:47] offset:0
	global_load_dwordx4 v[68:71], v192, s[46:47] offset:1024
	global_load_dwordx4 v[72:75], v192, s[46:47] offset:2048
	global_load_dwordx4 v[76:79], v192, s[46:47] offset:3072
	s_add_u32 s46, s42, 0x5000
	s_addc_u32 s47, s43, 0
	global_load_dwordx4 v[80:83], v192, s[46:47] offset:0
	global_load_dwordx4 v[84:87], v192, s[46:47] offset:1024
	global_load_dwordx4 v[88:91], v192, s[46:47] offset:2048
	global_load_dwordx4 v[92:95], v192, s[46:47] offset:3072
	s_add_u32 s46, s42, 0x6000
	s_addc_u32 s47, s43, 0
	global_load_dwordx4 v[96:99], v192, s[46:47] offset:0
	global_load_dwordx4 v[100:103], v192, s[46:47] offset:1024
	global_load_dwordx4 v[104:107], v192, s[46:47] offset:2048
	global_load_dwordx4 v[108:111], v192, s[46:47] offset:3072
	s_add_u32 s46, s42, 0x7000
	s_addc_u32 s47, s43, 0
	global_load_dwordx4 v[112:115], v192, s[46:47] offset:0
	global_load_dwordx4 v[116:119], v192, s[46:47] offset:1024
	global_load_dwordx4 v[120:123], v192, s[46:47] offset:2048
	global_load_dwordx4 v[124:127], v192, s[46:47] offset:3072
	s_waitcnt vmcnt(0)
	s_waitcnt lgkmcnt(0)
	s_lshl_b32 s64, s33, 3
	s_add_u32 s64, s64, s29
	s_lshl_b32 s64, s64, 5
	s_add_u32 s64, s64, s30
	s_lshl_b32 s64, s64, 2
	s_add_u32 s40, s8, s64
	s_addc_u32 s41, s9, 0
	s_and_b32 s64, s33, 1
	s_lshl_b32 s64, s64, 22
	s_add_u32 s64, s64, s50
	s_add_u32 s36, s6, s64
	s_addc_u32 s37, s7, 0
	s_lshl_b32 s64, s33, 19
	s_add_u32 s72, s62, s64
	s_addc_u32 s73, s63, 0
	v_exp_f32_e32 v200, v0
	v_exp_f32_e32 v201, v1
	v_exp_f32_e32 v202, v2
	v_exp_f32_e32 v203, v3
	v_exp_f32_e32 v204, v4
	v_exp_f32_e32 v205, v5
	v_exp_f32_e32 v206, v6
	v_exp_f32_e32 v207, v7
	v_exp_f32_e32 v208, v8
	v_exp_f32_e32 v209, v9
	v_exp_f32_e32 v210, v10
	v_exp_f32_e32 v211, v11
	v_exp_f32_e32 v212, v12
	v_exp_f32_e32 v213, v13
	v_exp_f32_e32 v214, v14
	v_exp_f32_e32 v215, v15
	v_add_f32_e32 v200, 1.0, v200
	v_add_f32_e32 v201, 1.0, v201
	v_add_f32_e32 v202, 1.0, v202
	v_add_f32_e32 v203, 1.0, v203
	v_add_f32_e32 v204, 1.0, v204
	v_add_f32_e32 v205, 1.0, v205
	v_add_f32_e32 v206, 1.0, v206
	v_add_f32_e32 v207, 1.0, v207
	v_add_f32_e32 v208, 1.0, v208
	v_add_f32_e32 v209, 1.0, v209
	v_add_f32_e32 v210, 1.0, v210
	v_add_f32_e32 v211, 1.0, v211
	v_add_f32_e32 v212, 1.0, v212
	v_add_f32_e32 v213, 1.0, v213
	v_add_f32_e32 v214, 1.0, v214
	v_add_f32_e32 v215, 1.0, v215
	v_rcp_f32_e32 v200, v200
	v_rcp_f32_e32 v201, v201
	v_rcp_f32_e32 v202, v202
	v_rcp_f32_e32 v203, v203
	v_rcp_f32_e32 v204, v204
	v_rcp_f32_e32 v205, v205
	v_rcp_f32_e32 v206, v206
	v_rcp_f32_e32 v207, v207
	v_rcp_f32_e32 v208, v208
	v_rcp_f32_e32 v209, v209
	v_rcp_f32_e32 v210, v210
	v_rcp_f32_e32 v211, v211
	v_rcp_f32_e32 v212, v212
	v_rcp_f32_e32 v213, v213
	v_rcp_f32_e32 v214, v214
	v_rcp_f32_e32 v215, v215
	v_fmamk_f32 v208, v208, 0xc0b8aa3b, v198
	v_fmamk_f32 v209, v209, 0xc0b8aa3b, v198
	v_fmamk_f32 v210, v210, 0xc0b8aa3b, v198
	v_fmamk_f32 v211, v211, 0xc0b8aa3b, v198
	v_mul_f32_e32 v204, v204, v128
	v_mul_f32_e32 v205, v205, v129
	v_mul_f32_e32 v206, v206, v130
	v_mul_f32_e32 v207, v207, v131
	v_fma_f32 v128, v200, v208, v204
	v_fma_f32 v129, v201, v209, v205
	v_fma_f32 v130, v202, v210, v206
	v_fma_f32 v131, v203, v211, v207
	v_exp_f32_e32 v200, v128
	v_exp_f32_e32 v201, v129
	v_exp_f32_e32 v202, v130
	v_exp_f32_e32 v203, v131
	v_add_f32_e32 v200, 1.0, v200
	v_add_f32_e32 v201, 1.0, v201
	v_add_f32_e32 v202, 1.0, v202
	v_add_f32_e32 v203, 1.0, v203
	v_rcp_f32_e32 v200, v200
	v_rcp_f32_e32 v201, v201
	v_rcp_f32_e32 v202, v202
	v_rcp_f32_e32 v203, v203
	v_fma_f32 v200, v200, 2.0, -1.0
	v_fma_f32 v201, v201, 2.0, -1.0
	v_fma_f32 v202, v202, 2.0, -1.0
	v_fma_f32 v203, v203, 2.0, -1.0
	v_mul_f32_e32 v216, v212, v200
	v_mul_f32_e32 v217, v213, v201
	v_mul_f32_e32 v218, v214, v202
	v_mul_f32_e32 v219, v215, v203
	v_mul_f32_e32 v236, v216, v228
	v_mul_f32_e32 v237, v216, v232
	v_fmac_f32_e32 v236, v217, v229
	v_fmac_f32_e32 v237, v217, v233
	v_fmac_f32_e32 v236, v218, v230
	v_fmac_f32_e32 v237, v218, v234
	v_fmac_f32_e32 v236, v219, v231
	v_fmac_f32_e32 v237, v219, v235
	v_mov_b32_e32 v238, v236
	v_mov_b32_e32 v239, v236
	v_mov_b32_e32 v240, v237
	v_mov_b32_e32 v241, v237
	s_nop 1
	v_permlane32_swap_b32_e32 v238, v239
	v_permlane32_swap_b32_e32 v240, v241
	v_add_f32_e32 v238, v238, v239
	v_add_f32_e32 v239, v240, v241
	ds_write_b64 v248, v[238:239] offset:0
	v_cvt_pk_f16_f32 v220, v216, v217
	v_cvt_pk_f16_f32 v221, v218, v219
	v_exp_f32_e32 v200, v16
	v_exp_f32_e32 v201, v17
	v_exp_f32_e32 v202, v18
	v_exp_f32_e32 v203, v19
	v_exp_f32_e32 v204, v20
	v_exp_f32_e32 v205, v21
	v_exp_f32_e32 v206, v22
	v_exp_f32_e32 v207, v23
	v_exp_f32_e32 v208, v24
	v_exp_f32_e32 v209, v25
	v_exp_f32_e32 v210, v26
	v_exp_f32_e32 v211, v27
	v_exp_f32_e32 v212, v28
	v_exp_f32_e32 v213, v29
	v_exp_f32_e32 v214, v30
	v_exp_f32_e32 v215, v31
	v_add_f32_e32 v200, 1.0, v200
	v_add_f32_e32 v201, 1.0, v201
	v_add_f32_e32 v202, 1.0, v202
	v_add_f32_e32 v203, 1.0, v203
	v_add_f32_e32 v204, 1.0, v204
	v_add_f32_e32 v205, 1.0, v205
	v_add_f32_e32 v206, 1.0, v206
	v_add_f32_e32 v207, 1.0, v207
	v_add_f32_e32 v208, 1.0, v208
	v_add_f32_e32 v209, 1.0, v209
	v_add_f32_e32 v210, 1.0, v210
	v_add_f32_e32 v211, 1.0, v211
	v_add_f32_e32 v212, 1.0, v212
	v_add_f32_e32 v213, 1.0, v213
	v_add_f32_e32 v214, 1.0, v214
	v_add_f32_e32 v215, 1.0, v215
	v_rcp_f32_e32 v200, v200
	v_rcp_f32_e32 v201, v201
	v_rcp_f32_e32 v202, v202
	v_rcp_f32_e32 v203, v203
	v_rcp_f32_e32 v204, v204
	v_rcp_f32_e32 v205, v205
	v_rcp_f32_e32 v206, v206
	v_rcp_f32_e32 v207, v207
	v_rcp_f32_e32 v208, v208
	v_rcp_f32_e32 v209, v209
	v_rcp_f32_e32 v210, v210
	v_rcp_f32_e32 v211, v211
	v_rcp_f32_e32 v212, v212
	v_rcp_f32_e32 v213, v213
	v_rcp_f32_e32 v214, v214
	v_rcp_f32_e32 v215, v215
	v_fmamk_f32 v208, v208, 0xc0b8aa3b, v198
	v_fmamk_f32 v209, v209, 0xc0b8aa3b, v198
	v_fmamk_f32 v210, v210, 0xc0b8aa3b, v198
	v_fmamk_f32 v211, v211, 0xc0b8aa3b, v198
	v_mul_f32_e32 v204, v204, v132
	v_mul_f32_e32 v205, v205, v133
	v_mul_f32_e32 v206, v206, v134
	v_mul_f32_e32 v207, v207, v135
	v_fma_f32 v132, v200, v208, v204
	v_fma_f32 v133, v201, v209, v205
	v_fma_f32 v134, v202, v210, v206
	v_fma_f32 v135, v203, v211, v207
	v_exp_f32_e32 v200, v132
	v_exp_f32_e32 v201, v133
	v_exp_f32_e32 v202, v134
	v_exp_f32_e32 v203, v135
	v_add_f32_e32 v200, 1.0, v200
	v_add_f32_e32 v201, 1.0, v201
	v_add_f32_e32 v202, 1.0, v202
	v_add_f32_e32 v203, 1.0, v203
	v_rcp_f32_e32 v200, v200
	v_rcp_f32_e32 v201, v201
	v_rcp_f32_e32 v202, v202
	v_rcp_f32_e32 v203, v203
	v_fma_f32 v200, v200, 2.0, -1.0
	v_fma_f32 v201, v201, 2.0, -1.0
	v_fma_f32 v202, v202, 2.0, -1.0
	v_fma_f32 v203, v203, 2.0, -1.0
	v_mul_f32_e32 v216, v212, v200
	v_mul_f32_e32 v217, v213, v201
	v_mul_f32_e32 v218, v214, v202
	v_mul_f32_e32 v219, v215, v203
	v_mul_f32_e32 v236, v216, v228
	v_mul_f32_e32 v237, v216, v232
	v_fmac_f32_e32 v236, v217, v229
	v_fmac_f32_e32 v237, v217, v233
	v_fmac_f32_e32 v236, v218, v230
	v_fmac_f32_e32 v237, v218, v234
	v_fmac_f32_e32 v236, v219, v231
	v_fmac_f32_e32 v237, v219, v235
	v_mov_b32_e32 v238, v236
	v_mov_b32_e32 v239, v236
	v_mov_b32_e32 v240, v237
	v_mov_b32_e32 v241, v237
	s_nop 1
	v_permlane32_swap_b32_e32 v238, v239
	v_permlane32_swap_b32_e32 v240, v241
	v_add_f32_e32 v238, v238, v239
	v_add_f32_e32 v239, v240, v241
	ds_write_b64 v248, v[238:239] offset:256
	v_cvt_pk_f16_f32 v222, v216, v217
	v_cvt_pk_f16_f32 v223, v218, v219
	s_nop 1
	v_permlane32_swap_b32_e32 v220, v222
	v_permlane32_swap_b32_e32 v221, v223
	s_cmp_eq_u32 s31, 0
	s_cbranch_scc1 .LD_slow4
	global_store_dwordx4 v195, v[220:223], s[36:37] offset:0

.LD_pok19:
	s_waitcnt lgkmcnt(0)
	s_barrier
	s_mov_b32 m0, s52
	s_nop 0
	global_load_lds_dwordx4 v224, s[34:35] sc1
	global_load_lds_dwordx4 v224, s[34:35] offset:1024 sc1
	global_load_lds_dwordx4 v224, s[34:35] offset:2048 sc1
	global_load_lds_dwordx4 v224, s[34:35] offset:3072 sc1
	s_mov_b32 m0, s53
	s_nop 0
	global_load_lds_dwordx4 v225, s[34:35] sc1
	global_load_lds_dwordx4 v225, s[34:35] offset:1024 sc1
	global_load_lds_dwordx4 v225, s[34:35] offset:2048 sc1
	global_load_lds_dwordx4 v225, s[34:35] offset:3072 sc1
	s_mov_b32 m0, s54
	s_nop 0
	global_load_lds_dwordx4 v226, s[34:35] sc1
	global_load_lds_dwordx4 v226, s[34:35] offset:1024 sc1
	global_load_lds_dwordx4 v226, s[34:35] offset:2048 sc1
	global_load_lds_dwordx4 v226, s[34:35] offset:3072 sc1
	s_mov_b32 m0, s55
	s_nop 0
	global_load_lds_dwordx4 v227, s[34:35] sc1
	global_load_lds_dwordx4 v227, s[34:35] offset:1024 sc1
	global_load_lds_dwordx4 v227, s[34:35] offset:2048 sc1
	global_load_lds_dwordx4 v227, s[34:35] offset:3072 sc1
	s_waitcnt vmcnt(8)
	s_barrier
	s_mov_b32 m0, s56
	s_nop 0
	global_load_lds_dwordx4 v242, s[34:35] sc1
	ds_read_b128 a[224:227], v192 offset:0
	ds_read_b128 a[228:231], v192 offset:1024
	ds_read_b128 a[232:235], v192 offset:2048
	ds_read_b128 a[236:239], v192 offset:3072
	ds_read_b128 a[240:243], v192 offset:4096
	ds_read_b128 a[244:247], v192 offset:5120
	ds_read_b128 a[248:251], v192 offset:6144
	ds_read_b128 a[252:255], v192 offset:7168
.LD_loop16:
	s_sub_u32 s71, s33, 1
	s_add_u32 s61, s33, 1
	s_min_u32 s61, s61, s60
	s_and_b32 s64, s71, 1
	s_lshl_b32 s64, s64, 22
	s_add_u32 s64, s64, s50
	s_add_u32 s64, s64, 0x60000
	s_add_u32 s36, s6, s64
	s_addc_u32 s37, s7, 0
	s_lshl_b32 s64, s71, 3
	s_add_u32 s64, s64, s29
	s_lshl_b32 s64, s64, 5
	s_add_u32 s64, s64, s30
	s_lshl_b32 s64, s64, 2
	s_add_u32 s40, s8, s64
	s_addc_u32 s41, s9, 0
	s_lshl_b32 s64, s71, 19
	s_add_u32 s64, s64, 0x600
	s_add_u32 s72, s62, s64
	s_addc_u32 s73, s63, 0
	s_nop 5
	s_waitcnt lgkmcnt(2)
	v_mfma_f32_32x32x16_f16 v[0:15], a[0:3], a[224:227], v[0:15]
	ds_read_b128 a[224:227], v192 offset:8192
	v_exp_f32_e32 v200, v96
	v_mfma_f32_32x32x16_f16 v[16:31], a[0:3], a[228:231], v[16:31]
	ds_read_b128 a[228:231], v192 offset:9216
	global_load_dword v251, v196, s[38:39] sc1
	v_exp_f32_e32 v201, v97
	v_add_f32_e32 v200, 1.0, v200
	v_mfma_f32_32x32x16_f16 v[0:15], a[4:7], a[232:235], v[0:15]
	ds_read_b128 a[232:235], v192 offset:10240
	v_exp_f32_e32 v202, v98
	v_add_f32_e32 v201, 1.0, v201
	v_mfma_f32_32x32x16_f16 v[16:31], a[4:7], a[236:239], v[16:31]
	ds_read_b128 a[236:239], v192 offset:11264
	global_load_lds_dwordx4 v242, s[34:35] offset:1024 sc1
	v_exp_f32_e32 v203, v99
	v_add_f32_e32 v202, 1.0, v202
	v_mfma_f32_32x32x16_f16 v[0:15], a[8:11], a[240:243], v[0:15]
	ds_read_b128 a[240:243], v192 offset:12288
	v_exp_f32_e32 v204, v100
	v_add_f32_e32 v203, 1.0, v203
	v_mfma_f32_32x32x16_f16 v[16:31], a[8:11], a[244:247], v[16:31]
	ds_read_b128 a[244:247], v192 offset:13312
	v_exp_f32_e32 v205, v101
	v_add_f32_e32 v204, 1.0, v204
	s_waitcnt lgkmcnt(2)
	v_mfma_f32_32x32x16_f16 v[0:15], a[12:15], a[248:251], v[0:15]
	ds_read_b128 a[248:251], v192 offset:14336
	v_exp_f32_e32 v206, v102
	v_add_f32_e32 v205, 1.0, v205
	v_mfma_f32_32x32x16_f16 v[16:31], a[12:15], a[252:255], v[16:31]
	ds_read_b128 a[252:255], v192 offset:15360
	global_load_lds_dwordx4 v242, s[34:35] offset:2048 sc1
	v_exp_f32_e32 v207, v103
	v_add_f32_e32 v206, 1.0, v206
	v_mfma_f32_32x32x16_f16 v[0:15], a[16:19], a[224:227], v[0:15]
	ds_read_b128 a[224:227], v192 offset:16384
	v_exp_f32_e32 v208, v104
	v_add_f32_e32 v207, 1.0, v207
	v_mfma_f32_32x32x16_f16 v[16:31], a[16:19], a[228:231], v[16:31]
	ds_read_b128 a[228:231], v192 offset:17408
	v_exp_f32_e32 v209, v105
	v_add_f32_e32 v208, 1.0, v208
	v_mfma_f32_32x32x16_f16 v[0:15], a[20:23], a[232:235], v[0:15]
	ds_read_b128 a[232:235], v192 offset:18432
	v_exp_f32_e32 v210, v106
	v_add_f32_e32 v209, 1.0, v209
	v_mfma_f32_32x32x16_f16 v[16:31], a[20:23], a[236:239], v[16:31]
	ds_read_b128 a[236:239], v192 offset:19456
	global_load_lds_dwordx4 v242, s[34:35] offset:3072 sc1
	v_exp_f32_e32 v211, v107
	v_add_f32_e32 v210, 1.0, v210
	s_waitcnt lgkmcnt(2)
	v_mfma_f32_32x32x16_f16 v[0:15], a[24:27], a[240:243], v[0:15]
	ds_read_b128 a[240:243], v192 offset:20480
	v_exp_f32_e32 v212, v108
	v_add_f32_e32 v211, 1.0, v211
	v_mfma_f32_32x32x16_f16 v[16:31], a[24:27], a[244:247], v[16:31]
	ds_read_b128 a[244:247], v192 offset:21504
	v_exp_f32_e32 v213, v109
	v_add_f32_e32 v212, 1.0, v212
	v_mfma_f32_32x32x16_f16 v[0:15], a[28:31], a[248:251], v[0:15]
	ds_read_b128 a[248:251], v192 offset:22528
	v_exp_f32_e32 v214, v110
	v_add_f32_e32 v213, 1.0, v213
	s_mov_b32 m0, s57
	v_mfma_f32_32x32x16_f16 v[16:31], a[28:31], a[252:255], v[16:31]
	ds_read_b128 a[252:255], v192 offset:23552
	global_load_lds_dwordx4 v243, s[34:35] sc1
	v_exp_f32_e32 v215, v111
	v_add_f32_e32 v214, 1.0, v214
	v_mfma_f32_32x32x16_f16 v[0:15], a[32:35], a[224:227], v[0:15]
	ds_read_b128 a[224:227], v192 offset:24576
	v_add_f32_e32 v215, 1.0, v215
	v_rcp_f32_e32 v200, v200
	v_mfma_f32_32x32x16_f16 v[16:31], a[32:35], a[228:231], v[16:31]
	ds_read_b128 a[228:231], v192 offset:25600
	v_rcp_f32_e32 v201, v201
	s_waitcnt lgkmcnt(2)
	v_mfma_f32_32x32x16_f16 v[0:15], a[36:39], a[232:235], v[0:15]
	ds_read_b128 a[232:235], v192 offset:26624
	v_rcp_f32_e32 v202, v202
	v_mfma_f32_32x32x16_f16 v[16:31], a[36:39], a[236:239], v[16:31]
	ds_read_b128 a[236:239], v192 offset:27648
	global_load_lds_dwordx4 v243, s[34:35] offset:1024 sc1
	v_rcp_f32_e32 v203, v203
	v_mfma_f32_32x32x16_f16 v[0:15], a[40:43], a[240:243], v[0:15]
	ds_read_b128 a[240:243], v192 offset:28672
	v_rcp_f32_e32 v204, v204
	v_mfma_f32_32x32x16_f16 v[16:31], a[40:43], a[244:247], v[16:31]
	ds_read_b128 a[244:247], v192 offset:29696
	v_rcp_f32_e32 v205, v205
	v_mul_f32_e32 v204, v204, v152
	v_mfma_f32_32x32x16_f16 v[0:15], a[44:47], a[248:251], v[0:15]
	ds_read_b128 a[248:251], v192 offset:30720
	v_rcp_f32_e32 v206, v206
	v_mul_f32_e32 v205, v205, v153
	v_mfma_f32_32x32x16_f16 v[16:31], a[44:47], a[252:255], v[16:31]
	ds_read_b128 a[252:255], v192 offset:31744
	global_load_lds_dwordx4 v243, s[34:35] offset:2048 sc1
	v_rcp_f32_e32 v207, v207
	v_mul_f32_e32 v206, v206, v154
	s_waitcnt vmcnt(8)
	s_barrier
	s_waitcnt lgkmcnt(2)
	v_mfma_f32_32x32x16_f16 v[0:15], a[48:51], a[224:227], v[0:15]
	ds_read_b128 a[224:227], v192 offset:32768
	v_rcp_f32_e32 v208, v208
	v_mul_f32_e32 v207, v207, v155
	v_mfma_f32_32x32x16_f16 v[16:31], a[48:51], a[228:231], v[16:31]
	ds_read_b128 a[228:231], v192 offset:33792
	v_rcp_f32_e32 v209, v209
	v_fmamk_f32 v208, v208, 0xc0b8aa3b, v198
	v_mfma_f32_32x32x16_f16 v[0:15], a[52:55], a[232:235], v[0:15]
	ds_read_b128 a[232:235], v192 offset:34816
	v_rcp_f32_e32 v210, v210
	v_fmamk_f32 v209, v209, 0xc0b8aa3b, v198
	v_fma_f32 v152, v200, v208, v204
	v_mfma_f32_32x32x16_f16 v[16:31], a[52:55], a[236:239], v[16:31]
	ds_read_b128 a[236:239], v192 offset:35840
	global_load_lds_dwordx4 v243, s[34:35] offset:3072 sc1
	v_rcp_f32_e32 v211, v211
	v_fmamk_f32 v210, v210, 0xc0b8aa3b, v198
	v_fma_f32 v153, v201, v209, v205
	v_mfma_f32_32x32x16_f16 v[0:15], a[56:59], a[240:243], v[0:15]
	ds_read_b128 a[240:243], v192 offset:36864
	v_rcp_f32_e32 v212, v212
	v_fmamk_f32 v211, v211, 0xc0b8aa3b, v198
	v_fma_f32 v154, v202, v210, v206
	v_mfma_f32_32x32x16_f16 v[16:31], a[56:59], a[244:247], v[16:31]
	ds_read_b128 a[244:247], v192 offset:37888
	v_rcp_f32_e32 v213, v213
	v_fma_f32 v155, v203, v211, v207
	s_waitcnt lgkmcnt(2)
	v_mfma_f32_32x32x16_f16 v[0:15], a[60:63], a[248:251], v[0:15]
	ds_read_b128 a[248:251], v192 offset:38912
	v_rcp_f32_e32 v214, v214
	s_mov_b32 m0, s58
	v_mfma_f32_32x32x16_f16 v[16:31], a[60:63], a[252:255], v[16:31]
	ds_read_b128 a[252:255], v192 offset:39936
	global_load_lds_dwordx4 v244, s[34:35] sc1
	v_rcp_f32_e32 v215, v215
	v_mfma_f32_32x32x16_f16 v[0:15], a[64:67], a[224:227], v[0:15]
	ds_read_b128 a[224:227], v192 offset:40960
	v_exp_f32_e32 v200, v152
	v_mfma_f32_32x32x16_f16 v[16:31], a[64:67], a[228:231], v[16:31]
	ds_read_b128 a[228:231], v192 offset:41984
	v_exp_f32_e32 v201, v153
	v_add_f32_e32 v200, 1.0, v200
	v_mfma_f32_32x32x16_f16 v[0:15], a[68:71], a[232:235], v[0:15]
	ds_read_b128 a[232:235], v192 offset:43008
	v_exp_f32_e32 v202, v154
	v_add_f32_e32 v201, 1.0, v201
	v_mfma_f32_32x32x16_f16 v[16:31], a[68:71], a[236:239], v[16:31]
	ds_read_b128 a[236:239], v192 offset:44032
	global_load_lds_dwordx4 v244, s[34:35] offset:1024 sc1
	v_exp_f32_e32 v203, v155
	v_add_f32_e32 v202, 1.0, v202
	s_waitcnt lgkmcnt(2)
	v_mfma_f32_32x32x16_f16 v[0:15], a[72:75], a[240:243], v[0:15]
	ds_read_b128 a[240:243], v192 offset:45056
	v_add_f32_e32 v203, 1.0, v203
	v_rcp_f32_e32 v200, v200
	v_mfma_f32_32x32x16_f16 v[16:31], a[72:75], a[244:247], v[16:31]
	ds_read_b128 a[244:247], v192 offset:46080
	v_rcp_f32_e32 v201, v201
	v_fma_f32 v200, v200, 2.0, -1.0
	v_mfma_f32_32x32x16_f16 v[0:15], a[76:79], a[248:251], v[0:15]
	ds_read_b128 a[248:251], v192 offset:47104
	v_rcp_f32_e32 v202, v202
	v_fma_f32 v201, v201, 2.0, -1.0
	v_mul_f32_e32 v216, v212, v200
	v_mfma_f32_32x32x16_f16 v[16:31], a[76:79], a[252:255], v[16:31]
	ds_read_b128 a[252:255], v192 offset:48128
	global_load_lds_dwordx4 v244, s[34:35] offset:2048 sc1
	v_rcp_f32_e32 v203, v203
	v_fma_f32 v202, v202, 2.0, -1.0
	v_mul_f32_e32 v217, v213, v201
	v_mfma_f32_32x32x16_f16 v[0:15], a[80:83], a[224:227], v[0:15]
	ds_read_b128 a[224:227], v192 offset:49152
	v_fma_f32 v203, v203, 2.0, -1.0
	v_mul_f32_e32 v218, v214, v202
	v_exp_f32_e32 v200, v112
	v_mfma_f32_32x32x16_f16 v[16:31], a[80:83], a[228:231], v[16:31]
	ds_read_b128 a[228:231], v192 offset:50176
	v_mul_f32_e32 v219, v215, v203
	v_mul_f32_e32 v236, v216, v228
	v_exp_f32_e32 v201, v113
	s_waitcnt lgkmcnt(2)
	v_mfma_f32_32x32x16_f16 v[0:15], a[84:87], a[232:235], v[0:15]
	ds_read_b128 a[232:235], v192 offset:51200
	v_mul_f32_e32 v237, v216, v232
	v_fmac_f32_e32 v236, v217, v229
	v_exp_f32_e32 v202, v114
	v_mfma_f32_32x32x16_f16 v[16:31], a[84:87], a[236:239], v[16:31]
	ds_read_b128 a[236:239], v192 offset:52224
	global_load_lds_dwordx4 v244, s[34:35] offset:3072 sc1
	v_fmac_f32_e32 v237, v217, v233
	v_fmac_f32_e32 v236, v218, v230
	v_exp_f32_e32 v203, v115
	v_mfma_f32_32x32x16_f16 v[0:15], a[88:91], a[240:243], v[0:15]
	ds_read_b128 a[240:243], v192 offset:53248
	v_fmac_f32_e32 v237, v218, v234
	v_fmac_f32_e32 v236, v219, v231
	v_exp_f32_e32 v204, v116
	v_mfma_f32_32x32x16_f16 v[16:31], a[88:91], a[244:247], v[16:31]
	ds_read_b128 a[244:247], v192 offset:54272
	v_fmac_f32_e32 v237, v219, v235
	v_mov_b32_e32 v238, v236
	v_exp_f32_e32 v205, v117
	v_mfma_f32_32x32x16_f16 v[0:15], a[92:95], a[248:251], v[0:15]
	ds_read_b128 a[248:251], v192 offset:55296
	v_mov_b32_e32 v239, v236
	v_mov_b32_e32 v240, v237
	v_exp_f32_e32 v206, v118
	s_mov_b32 m0, s59
	v_mfma_f32_32x32x16_f16 v[16:31], a[92:95], a[252:255], v[16:31]
	ds_read_b128 a[252:255], v192 offset:56320
	global_load_lds_dwordx4 v245, s[34:35] sc1
	v_mov_b32_e32 v241, v237
	v_cvt_pk_f16_f32 v220, v216, v217
	v_exp_f32_e32 v207, v119
	s_waitcnt lgkmcnt(2)
	v_mfma_f32_32x32x16_f16 v[0:15], a[96:99], a[224:227], v[0:15]
	ds_read_b128 a[224:227], v192 offset:57344
	s_nop 1
	v_permlane32_swap_b32_e32 v238, v239
	v_permlane32_swap_b32_e32 v240, v241
	v_add_f32_e32 v238, v238, v239
	v_add_f32_e32 v239, v240, v241
	ds_write_b64 v248, v[238:239] offset:1536
	v_exp_f32_e32 v208, v120
	v_mfma_f32_32x32x16_f16 v[16:31], a[96:99], a[228:231], v[16:31]
	ds_read_b128 a[228:231], v192 offset:58368
	v_cvt_pk_f16_f32 v221, v218, v219
	v_exp_f32_e32 v209, v121
	v_add_f32_e32 v200, 1.0, v200
	v_mfma_f32_32x32x16_f16 v[0:15], a[100:103], a[232:235], v[0:15]
	ds_read_b128 a[232:235], v192 offset:59392
	v_exp_f32_e32 v210, v122
	v_add_f32_e32 v201, 1.0, v201
	v_add_f32_e32 v202, 1.0, v202
	v_mfma_f32_32x32x16_f16 v[16:31], a[100:103], a[236:239], v[16:31]
	ds_read_b128 a[236:239], v192 offset:60416
	global_load_lds_dwordx4 v245, s[34:35] offset:1024 sc1
	v_exp_f32_e32 v211, v123
	v_add_f32_e32 v203, 1.0, v203
	v_add_f32_e32 v204, 1.0, v204
	v_mfma_f32_32x32x16_f16 v[0:15], a[104:107], a[240:243], v[0:15]
	ds_read_b128 a[240:243], v192 offset:61440
	v_exp_f32_e32 v212, v124
	v_add_f32_e32 v205, 1.0, v205
	v_add_f32_e32 v206, 1.0, v206
	v_mfma_f32_32x32x16_f16 v[16:31], a[104:107], a[244:247], v[16:31]
	ds_read_b128 a[244:247], v192 offset:62464
	v_exp_f32_e32 v213, v125
	v_add_f32_e32 v207, 1.0, v207
	v_add_f32_e32 v208, 1.0, v208
	s_waitcnt lgkmcnt(2)
	v_mfma_f32_32x32x16_f16 v[0:15], a[108:111], a[248:251], v[0:15]
	ds_read_b128 a[248:251], v192 offset:63488
	v_exp_f32_e32 v214, v126
	v_add_f32_e32 v209, 1.0, v209
	v_add_f32_e32 v210, 1.0, v210
	v_mfma_f32_32x32x16_f16 v[16:31], a[108:111], a[252:255], v[16:31]
	ds_read_b128 a[252:255], v192 offset:64512
	global_load_lds_dwordx4 v245, s[34:35] offset:2048 sc1
	v_exp_f32_e32 v215, v127
	v_add_f32_e32 v211, 1.0, v211
	v_add_f32_e32 v212, 1.0, v212
	s_waitcnt vmcnt(7)
	s_barrier
	v_mfma_f32_32x32x16_f16 v[0:15], a[112:115], a[224:227], v[0:15]
	ds_read_b128 a[224:227], v193 offset:0
	v_add_f32_e32 v213, 1.0, v213
	v_add_f32_e32 v214, 1.0, v214
	v_rcp_f32_e32 v200, v200
	v_mfma_f32_32x32x16_f16 v[16:31], a[112:115], a[228:231], v[16:31]
	ds_read_b128 a[228:231], v193 offset:1024
	v_add_f32_e32 v215, 1.0, v215
	v_rcp_f32_e32 v201, v201
	v_mfma_f32_32x32x16_f16 v[0:15], a[116:119], a[232:235], v[0:15]
	ds_read_b128 a[232:235], v193 offset:2048
	v_rcp_f32_e32 v202, v202
	v_mfma_f32_32x32x16_f16 v[16:31], a[116:119], a[236:239], v[16:31]
	ds_read_b128 a[236:239], v193 offset:3072
	global_load_lds_dwordx4 v245, s[34:35] offset:3072 sc1
	v_rcp_f32_e32 v203, v203
	s_waitcnt lgkmcnt(2)
	v_mfma_f32_32x32x16_f16 v[0:15], a[120:123], a[240:243], v[0:15]
	ds_read_b128 a[240:243], v193 offset:4096
	v_rcp_f32_e32 v204, v204
	s_add_u32 s46, s42, 0x4000
	s_addc_u32 s47, s43, 0
	global_load_dwordx4 v[64:67], v192, s[46:47] offset:0
	v_mfma_f32_32x32x16_f16 v[16:31], a[120:123], a[244:247], v[16:31]
	ds_read_b128 a[244:247], v193 offset:5120
	v_rcp_f32_e32 v205, v205
	v_mul_f32_e32 v204, v204, v156
	global_load_dwordx4 v[68:71], v192, s[46:47] offset:1024
	global_load_dwordx4 v[72:75], v192, s[46:47] offset:2048
	v_mfma_f32_32x32x16_f16 v[0:15], a[124:127], a[248:251], v[0:15]
	ds_read_b128 a[248:251], v193 offset:6144
	v_rcp_f32_e32 v206, v206
	v_mul_f32_e32 v205, v205, v157
	global_load_dwordx4 v[76:79], v192, s[46:47] offset:3072
	s_add_u32 s46, s42, 0x5000
	s_addc_u32 s47, s43, 0
	s_mov_b32 m0, s52
	v_mfma_f32_32x32x16_f16 v[16:31], a[124:127], a[252:255], v[16:31]
	ds_read_b128 a[252:255], v193 offset:7168
	v_cmp_gt_u32_e32 vcc, 2, v251
	s_cbranch_vccnz .LD_tpoll21
.LD_tok20:
	s_add_u32 s34, s34, 0x20000
	s_addc_u32 s35, s35, 0
	global_load_lds_dwordx4 v224, s[34:35] sc1
	v_rcp_f32_e32 v207, v207
	v_mul_f32_e32 v206, v206, v158
	global_load_dwordx4 v[80:83], v192, s[46:47] offset:0
	global_load_dwordx4 v[84:87], v192, s[46:47] offset:1024
	v_mfma_f32_32x32x16_f16 v[0:15], a[128:131], a[224:227], v[0:15]
	ds_read_b128 a[224:227], v193 offset:8192
	v_rcp_f32_e32 v208, v208
	v_mul_f32_e32 v207, v207, v159
	global_load_dwordx4 v[88:91], v192, s[46:47] offset:2048
	global_load_dwordx4 v[92:95], v192, s[46:47] offset:3072
	v_mfma_f32_32x32x16_f16 v[16:31], a[128:131], a[228:231], v[16:31]
	ds_read_b128 a[228:231], v193 offset:9216
	v_rcp_f32_e32 v209, v209
	v_fmamk_f32 v208, v208, 0xc0b8aa3b, v198
	s_waitcnt lgkmcnt(2)
	v_mfma_f32_32x32x16_f16 v[0:15], a[132:135], a[232:235], v[0:15]
	ds_read_b128 a[232:235], v193 offset:10240
	v_rcp_f32_e32 v210, v210
	v_fmamk_f32 v209, v209, 0xc0b8aa3b, v198
	v_fma_f32 v156, v200, v208, v204
	v_mfma_f32_32x32x16_f16 v[16:31], a[132:135], a[236:239], v[16:31]
	ds_read_b128 a[236:239], v193 offset:11264
	global_load_lds_dwordx4 v224, s[34:35] offset:1024 sc1
	v_rcp_f32_e32 v211, v211
	v_fmamk_f32 v210, v210, 0xc0b8aa3b, v198
	v_fma_f32 v157, v201, v209, v205
	v_mfma_f32_32x32x16_f16 v[0:15], a[136:139], a[240:243], v[0:15]
	ds_read_b128 a[240:243], v193 offset:12288
	v_rcp_f32_e32 v212, v212
	v_fmamk_f32 v211, v211, 0xc0b8aa3b, v198
	v_fma_f32 v158, v202, v210, v206
	v_mfma_f32_32x32x16_f16 v[16:31], a[136:139], a[244:247], v[16:31]
	ds_read_b128 a[244:247], v193 offset:13312
	v_rcp_f32_e32 v213, v213
	v_fma_f32 v159, v203, v211, v207
	v_mfma_f32_32x32x16_f16 v[0:15], a[140:143], a[248:251], v[0:15]
	ds_read_b128 a[248:251], v193 offset:14336
	v_rcp_f32_e32 v214, v214
	v_mfma_f32_32x32x16_f16 v[16:31], a[140:143], a[252:255], v[16:31]
	ds_read_b128 a[252:255], v193 offset:15360
	global_load_lds_dwordx4 v224, s[34:35] offset:2048 sc1
	v_rcp_f32_e32 v215, v215
	s_waitcnt lgkmcnt(2)
	v_mfma_f32_32x32x16_f16 v[0:15], a[144:147], a[224:227], v[0:15]
	ds_read_b128 a[224:227], v193 offset:16384
	v_exp_f32_e32 v200, v156
	v_mfma_f32_32x32x16_f16 v[16:31], a[144:147], a[228:231], v[16:31]
	ds_read_b128 a[228:231], v193 offset:17408
	v_exp_f32_e32 v201, v157
	v_add_f32_e32 v200, 1.0, v200
	v_mfma_f32_32x32x16_f16 v[0:15], a[148:151], a[232:235], v[0:15]
	ds_read_b128 a[232:235], v193 offset:18432
	v_exp_f32_e32 v202, v158
	v_add_f32_e32 v201, 1.0, v201
	v_mfma_f32_32x32x16_f16 v[16:31], a[148:151], a[236:239], v[16:31]
	ds_read_b128 a[236:239], v193 offset:19456
	global_load_lds_dwordx4 v224, s[34:35] offset:3072 sc1
	v_exp_f32_e32 v203, v159
	v_add_f32_e32 v202, 1.0, v202
	v_mfma_f32_32x32x16_f16 v[0:15], a[152:155], a[240:243], v[0:15]
	ds_read_b128 a[240:243], v193 offset:20480
	v_add_f32_e32 v203, 1.0, v203
	v_rcp_f32_e32 v200, v200
	v_mfma_f32_32x32x16_f16 v[16:31], a[152:155], a[244:247], v[16:31]
	ds_read_b128 a[244:247], v193 offset:21504
	v_rcp_f32_e32 v201, v201
	v_fma_f32 v200, v200, 2.0, -1.0
	s_waitcnt lgkmcnt(2)
	v_mfma_f32_32x32x16_f16 v[0:15], a[156:159], a[248:251], v[0:15]
	ds_read_b128 a[248:251], v193 offset:22528
	v_rcp_f32_e32 v202, v202
	v_fma_f32 v201, v201, 2.0, -1.0
	v_mul_f32_e32 v216, v212, v200
	s_mov_b32 m0, s53
	v_mfma_f32_32x32x16_f16 v[16:31], a[156:159], a[252:255], v[16:31]
	ds_read_b128 a[252:255], v193 offset:23552
	global_load_lds_dwordx4 v225, s[34:35] sc1
	v_rcp_f32_e32 v203, v203
	v_fma_f32 v202, v202, 2.0, -1.0
	v_mul_f32_e32 v217, v213, v201
	v_mfma_f32_32x32x16_f16 v[0:15], a[160:163], a[224:227], v[0:15]
	ds_read_b128 a[224:227], v193 offset:24576
	v_fma_f32 v203, v203, 2.0, -1.0
	v_mul_f32_e32 v218, v214, v202
	v_mfma_f32_32x32x16_f16 v[16:31], a[160:163], a[228:231], v[16:31]
	ds_read_b128 a[228:231], v193 offset:25600
	v_mul_f32_e32 v219, v215, v203
	v_mul_f32_e32 v236, v216, v228
	v_mfma_f32_32x32x16_f16 v[0:15], a[164:167], a[232:235], v[0:15]
	ds_read_b128 a[232:235], v193 offset:26624
	v_mul_f32_e32 v237, v216, v232
	v_fmac_f32_e32 v236, v217, v229
	v_mfma_f32_32x32x16_f16 v[16:31], a[164:167], a[236:239], v[16:31]
	ds_read_b128 a[236:239], v193 offset:27648
	global_load_lds_dwordx4 v225, s[34:35] offset:1024 sc1
	v_fmac_f32_e32 v237, v217, v233
	v_fmac_f32_e32 v236, v218, v230
	s_waitcnt lgkmcnt(2)
	v_mfma_f32_32x32x16_f16 v[0:15], a[168:171], a[240:243], v[0:15]
	ds_read_b128 a[240:243], v193 offset:28672
	v_fmac_f32_e32 v237, v218, v234
	v_fmac_f32_e32 v236, v219, v231
	v_mfma_f32_32x32x16_f16 v[16:31], a[168:171], a[244:247], v[16:31]
	ds_read_b128 a[244:247], v193 offset:29696
	v_fmac_f32_e32 v237, v219, v235
	v_mov_b32_e32 v238, v236
	v_mfma_f32_32x32x16_f16 v[0:15], a[172:175], a[248:251], v[0:15]
	ds_read_b128 a[248:251], v193 offset:30720
	v_mov_b32_e32 v239, v236
	v_mov_b32_e32 v240, v237
	v_mfma_f32_32x32x16_f16 v[16:31], a[172:175], a[252:255], v[16:31]
	ds_read_b128 a[252:255], v193 offset:31744
	global_load_lds_dwordx4 v225, s[34:35] offset:2048 sc1
	v_mov_b32_e32 v241, v237
	v_cvt_pk_f16_f32 v222, v216, v217
	s_waitcnt vmcnt(15)
	s_barrier
	v_mfma_f32_32x32x16_f16 v[0:15], a[176:179], a[224:227], v[0:15]
	ds_read_b128 a[224:227], v193 offset:32768
	s_nop 1
	v_permlane32_swap_b32_e32 v238, v239
	v_permlane32_swap_b32_e32 v240, v241
	v_add_f32_e32 v238, v238, v239
	v_add_f32_e32 v239, v240, v241
	ds_write_b64 v248, v[238:239] offset:1792
	v_mfma_f32_32x32x16_f16 v[16:31], a[176:179], a[228:231], v[16:31]
	ds_read_b128 a[228:231], v193 offset:33792
	v_cvt_pk_f16_f32 v223, v218, v219
	s_waitcnt lgkmcnt(3)
	v_mfma_f32_32x32x16_f16 v[0:15], a[180:183], a[232:235], v[0:15]
	ds_read_b128 a[232:235], v193 offset:34816
	s_nop 1
	v_permlane32_swap_b32_e32 v220, v222
	v_permlane32_swap_b32_e32 v221, v223
	s_cmp_eq_u32 s31, 0
	s_cbranch_scc1 .LD_slow22
	global_store_dwordx4 v195, v[220:223], s[36:37] offset:0
.LD_join23:
	v_mfma_f32_32x32x16_f16 v[16:31], a[180:183], a[236:239], v[16:31]
	ds_read_b128 a[236:239], v193 offset:35840
	global_load_lds_dwordx4 v225, s[34:35] offset:3072 sc1
	v_mfma_f32_32x32x16_f16 v[0:15], a[184:187], a[240:243], v[0:15]
	ds_read_b128 a[240:243], v193 offset:36864
	v_mfma_f32_32x32x16_f16 v[16:31], a[184:187], a[244:247], v[16:31]
	ds_read_b128 a[244:247], v193 offset:37888
	v_mfma_f32_32x32x16_f16 v[0:15], a[188:191], a[248:251], v[0:15]
	ds_read_b128 a[248:251], v193 offset:38912
	s_mov_b32 m0, s54
	v_mfma_f32_32x32x16_f16 v[16:31], a[188:191], a[252:255], v[16:31]
	ds_read_b128 a[252:255], v193 offset:39936
	global_load_lds_dwordx4 v226, s[34:35] sc1
	s_waitcnt lgkmcnt(2)
	v_mfma_f32_32x32x16_f16 v[0:15], a[192:195], a[224:227], v[0:15]
	ds_read_b128 a[224:227], v193 offset:40960
	v_mfma_f32_32x32x16_f16 v[16:31], a[192:195], a[228:231], v[16:31]
	ds_read_b128 a[228:231], v193 offset:41984
	v_mfma_f32_32x32x16_f16 v[0:15], a[196:199], a[232:235], v[0:15]
	ds_read_b128 a[232:235], v193 offset:43008
	v_mfma_f32_32x32x16_f16 v[16:31], a[196:199], a[236:239], v[16:31]
	ds_read_b128 a[236:239], v193 offset:44032
	global_load_lds_dwordx4 v226, s[34:35] offset:1024 sc1
	v_mfma_f32_32x32x16_f16 v[0:15], a[200:203], a[240:243], v[0:15]
	ds_read_b128 a[240:243], v193 offset:45056
	v_mfma_f32_32x32x16_f16 v[16:31], a[200:203], a[244:247], v[16:31]
	ds_read_b128 a[244:247], v193 offset:46080
	s_waitcnt lgkmcnt(2)
	v_mfma_f32_32x32x16_f16 v[0:15], a[204:207], a[248:251], v[0:15]
	ds_read_b128 a[248:251], v193 offset:47104
	v_mfma_f32_32x32x16_f16 v[16:31], a[204:207], a[252:255], v[16:31]
	ds_read_b128 a[252:255], v193 offset:48128
	global_load_lds_dwordx4 v226, s[34:35] offset:2048 sc1
	s_waitcnt vmcnt(4)
	s_barrier
	v_mov_b32_e32 v199, 4
	s_cmp_eq_u32 s31, 0
	s_cbranch_scc1 .LD_slow24
	global_store_dword v197, v199, s[40:41]
.LD_join25:
	ds_read_b64 v[200:201], v249 offset:1536
	ds_read_b64 v[202:203], v249 offset:3584
	ds_read_b64 v[204:205], v249 offset:5632
	ds_read_b64 v[206:207], v249 offset:7680
	v_mfma_f32_32x32x16_f16 v[0:15], a[208:211], a[224:227], v[0:15]
	ds_read_b128 a[224:227], v193 offset:49152
	v_mfma_f32_32x32x16_f16 v[16:31], a[208:211], a[228:231], v[16:31]
	ds_read_b128 a[228:231], v193 offset:50176
	v_mfma_f32_32x32x16_f16 v[0:15], a[212:215], a[232:235], v[0:15]
	ds_read_b128 a[232:235], v193 offset:51200
	v_mfma_f32_32x32x16_f16 v[16:31], a[212:215], a[236:239], v[16:31]
	ds_read_b128 a[236:239], v193 offset:52224
	global_load_lds_dwordx4 v226, s[34:35] offset:3072 sc1
	s_waitcnt lgkmcnt(2)
	v_mfma_f32_32x32x16_f16 v[0:15], a[216:219], a[240:243], v[0:15]
	ds_read_b128 a[240:243], v193 offset:53248
	v_mfma_f32_32x32x16_f16 v[16:31], a[216:219], a[244:247], v[16:31]
	ds_read_b128 a[244:247], v193 offset:54272
	v_mfma_f32_32x32x16_f16 v[0:15], a[220:223], a[248:251], v[0:15]
	ds_read_b128 a[248:251], v193 offset:55296
	s_mov_b32 m0, s55
	v_mfma_f32_32x32x16_f16 v[16:31], a[220:223], a[252:255], v[16:31]
	ds_read_b128 a[252:255], v193 offset:56320
	global_load_lds_dwordx4 v227, s[34:35] sc1
	v_mfma_f32_32x32x16_f16 v[0:15], v[160:163], a[224:227], v[0:15]
	ds_read_b128 a[224:227], v193 offset:57344
	v_mfma_f32_32x32x16_f16 v[16:31], v[160:163], a[228:231], v[16:31]
	ds_read_b128 a[228:231], v193 offset:58368
	s_waitcnt lgkmcnt(2)
	v_mfma_f32_32x32x16_f16 v[0:15], v[164:167], a[232:235], v[0:15]
	ds_read_b128 a[232:235], v193 offset:59392
	v_mfma_f32_32x32x16_f16 v[16:31], v[164:167], a[236:239], v[16:31]
	ds_read_b128 a[236:239], v193 offset:60416
	global_load_lds_dwordx4 v227, s[34:35] offset:1024 sc1
	v_add_f32_e32 v200, v200, v202
	v_add_f32_e32 v201, v201, v203
	v_add_f32_e32 v200, v200, v204
	v_add_f32_e32 v201, v201, v205
	v_add_f32_e32 v200, v200, v206
	v_add_f32_e32 v201, v201, v207
	global_store_dwordx2 v250, v[200:201], s[72:73]
	v_mfma_f32_32x32x16_f16 v[0:15], v[168:171], a[240:243], v[0:15]
	ds_read_b128 a[240:243], v193 offset:61440
	v_mfma_f32_32x32x16_f16 v[16:31], v[168:171], a[244:247], v[16:31]
	ds_read_b128 a[244:247], v193 offset:62464
	v_mfma_f32_32x32x16_f16 v[0:15], v[172:175], a[248:251], v[0:15]
	ds_read_b128 a[248:251], v193 offset:63488
	v_mfma_f32_32x32x16_f16 v[16:31], v[172:175], a[252:255], v[16:31]
	ds_read_b128 a[252:255], v193 offset:64512
	global_load_lds_dwordx4 v227, s[34:35] offset:2048 sc1
	s_and_b32 s64, s33, 1
	s_lshl_b32 s64, s64, 22
	s_add_u32 s64, s64, s50
	s_add_u32 s36, s6, s64
	s_addc_u32 s37, s7, 0
	s_lshl_b32 s64, s33, 3
	s_add_u32 s64, s64, s29
	s_lshl_b32 s64, s64, 5
	s_add_u32 s64, s64, s30
	s_lshl_b32 s64, s64, 2
	s_add_u32 s40, s8, s64
	s_addc_u32 s41, s9, 0
	s_lshl_b32 s64, s33, 19
	s_add_u32 s72, s62, s64
	s_addc_u32 s73, s63, 0
	s_waitcnt vmcnt(9)
	s_barrier
	s_waitcnt lgkmcnt(2)
	v_mfma_f32_32x32x16_f16 v[0:15], v[176:179], a[224:227], v[0:15]
	ds_read_b128 a[224:227], v192 offset:0
	v_mfma_f32_32x32x16_f16 v[16:31], v[176:179], a[228:231], v[16:31]
	ds_read_b128 a[228:231], v192 offset:1024
	v_mfma_f32_32x32x16_f16 v[0:15], v[180:183], a[232:235], v[0:15]
	ds_read_b128 a[232:235], v192 offset:2048
	v_mfma_f32_32x32x16_f16 v[16:31], v[180:183], a[236:239], v[16:31]
	ds_read_b128 a[236:239], v192 offset:3072
	global_load_lds_dwordx4 v227, s[34:35] offset:3072 sc1
	v_mfma_f32_32x32x16_f16 v[0:15], v[184:187], a[240:243], v[0:15]
	ds_read_b128 a[240:243], v192 offset:4096
	v_mfma_f32_32x32x16_f16 v[16:31], v[184:187], a[244:247], v[16:31]
	ds_read_b128 a[244:247], v192 offset:5120
	s_waitcnt lgkmcnt(2)
	v_mfma_f32_32x32x16_f16 v[0:15], v[188:191], a[248:251], v[0:15]
	ds_read_b128 a[248:251], v192 offset:6144
	s_mov_b32 m0, s56
	v_mfma_f32_32x32x16_f16 v[16:31], v[188:191], a[252:255], v[16:31]
	ds_read_b128 a[252:255], v192 offset:7168
	global_load_lds_dwordx4 v242, s[34:35] sc1
	s_nop 5
	s_waitcnt lgkmcnt(2)
	v_mfma_f32_32x32x16_f16 v[32:47], a[0:3], a[224:227], v[32:47]
	ds_read_b128 a[224:227], v192 offset:8192
	v_exp_f32_e32 v200, v0
	v_mfma_f32_32x32x16_f16 v[48:63], a[0:3], a[228:231], v[48:63]
	ds_read_b128 a[228:231], v192 offset:9216
	global_load_dword v251, v196, s[38:39] sc1
	v_exp_f32_e32 v201, v1
	v_add_f32_e32 v200, 1.0, v200
	v_mfma_f32_32x32x16_f16 v[32:47], a[4:7], a[232:235], v[32:47]
	ds_read_b128 a[232:235], v192 offset:10240
	v_exp_f32_e32 v202, v2
	v_add_f32_e32 v201, 1.0, v201
	v_mfma_f32_32x32x16_f16 v[48:63], a[4:7], a[236:239], v[48:63]
	ds_read_b128 a[236:239], v192 offset:11264
	global_load_lds_dwordx4 v242, s[34:35] offset:1024 sc1
	v_exp_f32_e32 v203, v3
	v_add_f32_e32 v202, 1.0, v202
	v_mfma_f32_32x32x16_f16 v[32:47], a[8:11], a[240:243], v[32:47]
	ds_read_b128 a[240:243], v192 offset:12288
	v_exp_f32_e32 v204, v4
	v_add_f32_e32 v203, 1.0, v203
	v_mfma_f32_32x32x16_f16 v[48:63], a[8:11], a[244:247], v[48:63]
	ds_read_b128 a[244:247], v192 offset:13312
	v_exp_f32_e32 v205, v5
	v_add_f32_e32 v204, 1.0, v204
	s_waitcnt lgkmcnt(2)
	v_mfma_f32_32x32x16_f16 v[32:47], a[12:15], a[248:251], v[32:47]
	ds_read_b128 a[248:251], v192 offset:14336
	v_exp_f32_e32 v206, v6
	v_add_f32_e32 v205, 1.0, v205
	v_mfma_f32_32x32x16_f16 v[48:63], a[12:15], a[252:255], v[48:63]
	ds_read_b128 a[252:255], v192 offset:15360
	global_load_lds_dwordx4 v242, s[34:35] offset:2048 sc1
	v_exp_f32_e32 v207, v7
	v_add_f32_e32 v206, 1.0, v206
	v_mfma_f32_32x32x16_f16 v[32:47], a[16:19], a[224:227], v[32:47]
	ds_read_b128 a[224:227], v192 offset:16384
	v_exp_f32_e32 v208, v8
	v_add_f32_e32 v207, 1.0, v207
	v_mfma_f32_32x32x16_f16 v[48:63], a[16:19], a[228:231], v[48:63]
	ds_read_b128 a[228:231], v192 offset:17408
	v_exp_f32_e32 v209, v9
	v_add_f32_e32 v208, 1.0, v208
	v_mfma_f32_32x32x16_f16 v[32:47], a[20:23], a[232:235], v[32:47]
	ds_read_b128 a[232:235], v192 offset:18432
	v_exp_f32_e32 v210, v10
	v_add_f32_e32 v209, 1.0, v209
	v_mfma_f32_32x32x16_f16 v[48:63], a[20:23], a[236:239], v[48:63]
	ds_read_b128 a[236:239], v192 offset:19456
	global_load_lds_dwordx4 v242, s[34:35] offset:3072 sc1
	v_exp_f32_e32 v211, v11
	v_add_f32_e32 v210, 1.0, v210
	s_waitcnt lgkmcnt(2)
	v_mfma_f32_32x32x16_f16 v[32:47], a[24:27], a[240:243], v[32:47]
	ds_read_b128 a[240:243], v192 offset:20480
	v_exp_f32_e32 v212, v12
	v_add_f32_e32 v211, 1.0, v211
	v_mfma_f32_32x32x16_f16 v[48:63], a[24:27], a[244:247], v[48:63]
	ds_read_b128 a[244:247], v192 offset:21504
	v_exp_f32_e32 v213, v13
	v_add_f32_e32 v212, 1.0, v212
	v_mfma_f32_32x32x16_f16 v[32:47], a[28:31], a[248:251], v[32:47]
	ds_read_b128 a[248:251], v192 offset:22528
	v_exp_f32_e32 v214, v14
	v_add_f32_e32 v213, 1.0, v213
	s_mov_b32 m0, s57
	v_mfma_f32_32x32x16_f16 v[48:63], a[28:31], a[252:255], v[48:63]
	ds_read_b128 a[252:255], v192 offset:23552
	global_load_lds_dwordx4 v243, s[34:35] sc1
	v_exp_f32_e32 v215, v15
	v_add_f32_e32 v214, 1.0, v214
	v_mfma_f32_32x32x16_f16 v[32:47], a[32:35], a[224:227], v[32:47]
	ds_read_b128 a[224:227], v192 offset:24576
	v_add_f32_e32 v215, 1.0, v215
	v_rcp_f32_e32 v200, v200
	v_mfma_f32_32x32x16_f16 v[48:63], a[32:35], a[228:231], v[48:63]
	ds_read_b128 a[228:231], v192 offset:25600
	v_rcp_f32_e32 v201, v201
	s_waitcnt lgkmcnt(2)
	v_mfma_f32_32x32x16_f16 v[32:47], a[36:39], a[232:235], v[32:47]
	ds_read_b128 a[232:235], v192 offset:26624
	v_rcp_f32_e32 v202, v202
	v_mfma_f32_32x32x16_f16 v[48:63], a[36:39], a[236:239], v[48:63]
	ds_read_b128 a[236:239], v192 offset:27648
	global_load_lds_dwordx4 v243, s[34:35] offset:1024 sc1
	v_rcp_f32_e32 v203, v203
	v_mfma_f32_32x32x16_f16 v[32:47], a[40:43], a[240:243], v[32:47]
	ds_read_b128 a[240:243], v192 offset:28672
	v_rcp_f32_e32 v204, v204
	v_mfma_f32_32x32x16_f16 v[48:63], a[40:43], a[244:247], v[48:63]
	ds_read_b128 a[244:247], v192 offset:29696
	v_rcp_f32_e32 v205, v205
	v_mul_f32_e32 v204, v204, v128
	v_mfma_f32_32x32x16_f16 v[32:47], a[44:47], a[248:251], v[32:47]
	ds_read_b128 a[248:251], v192 offset:30720
	v_rcp_f32_e32 v206, v206
	v_mul_f32_e32 v205, v205, v129
	v_mfma_f32_32x32x16_f16 v[48:63], a[44:47], a[252:255], v[48:63]
	ds_read_b128 a[252:255], v192 offset:31744
	global_load_lds_dwordx4 v243, s[34:35] offset:2048 sc1
	v_rcp_f32_e32 v207, v207
	v_mul_f32_e32 v206, v206, v130
	s_waitcnt vmcnt(8)
	s_barrier
	s_waitcnt lgkmcnt(2)
	v_mfma_f32_32x32x16_f16 v[32:47], a[48:51], a[224:227], v[32:47]
	ds_read_b128 a[224:227], v192 offset:32768
	v_rcp_f32_e32 v208, v208
	v_mul_f32_e32 v207, v207, v131
	v_mfma_f32_32x32x16_f16 v[48:63], a[48:51], a[228:231], v[48:63]
	ds_read_b128 a[228:231], v192 offset:33792
	v_rcp_f32_e32 v209, v209
	v_fmamk_f32 v208, v208, 0xc0b8aa3b, v198
	v_mfma_f32_32x32x16_f16 v[32:47], a[52:55], a[232:235], v[32:47]
	ds_read_b128 a[232:235], v192 offset:34816
	v_rcp_f32_e32 v210, v210
	v_fmamk_f32 v209, v209, 0xc0b8aa3b, v198
	v_fma_f32 v128, v200, v208, v204
	v_mfma_f32_32x32x16_f16 v[48:63], a[52:55], a[236:239], v[48:63]
	ds_read_b128 a[236:239], v192 offset:35840
	global_load_lds_dwordx4 v243, s[34:35] offset:3072 sc1
	v_rcp_f32_e32 v211, v211
	v_fmamk_f32 v210, v210, 0xc0b8aa3b, v198
	v_fma_f32 v129, v201, v209, v205
	v_mfma_f32_32x32x16_f16 v[32:47], a[56:59], a[240:243], v[32:47]
	ds_read_b128 a[240:243], v192 offset:36864
	v_rcp_f32_e32 v212, v212
	v_fmamk_f32 v211, v211, 0xc0b8aa3b, v198
	v_fma_f32 v130, v202, v210, v206
	v_mfma_f32_32x32x16_f16 v[48:63], a[56:59], a[244:247], v[48:63]
	ds_read_b128 a[244:247], v192 offset:37888
	v_rcp_f32_e32 v213, v213
	v_fma_f32 v131, v203, v211, v207
	s_waitcnt lgkmcnt(2)
	v_mfma_f32_32x32x16_f16 v[32:47], a[60:63], a[248:251], v[32:47]
	ds_read_b128 a[248:251], v192 offset:38912
	v_rcp_f32_e32 v214, v214
	s_mov_b32 m0, s58
	v_mfma_f32_32x32x16_f16 v[48:63], a[60:63], a[252:255], v[48:63]
	ds_read_b128 a[252:255], v192 offset:39936
	global_load_lds_dwordx4 v244, s[34:35] sc1
	v_rcp_f32_e32 v215, v215
	v_mfma_f32_32x32x16_f16 v[32:47], a[64:67], a[224:227], v[32:47]
	ds_read_b128 a[224:227], v192 offset:40960
	v_exp_f32_e32 v200, v128
	v_mfma_f32_32x32x16_f16 v[48:63], a[64:67], a[228:231], v[48:63]
	ds_read_b128 a[228:231], v192 offset:41984
	v_exp_f32_e32 v201, v129
	v_add_f32_e32 v200, 1.0, v200
	v_mfma_f32_32x32x16_f16 v[32:47], a[68:71], a[232:235], v[32:47]
	ds_read_b128 a[232:235], v192 offset:43008
	v_exp_f32_e32 v202, v130
	v_add_f32_e32 v201, 1.0, v201
	v_mfma_f32_32x32x16_f16 v[48:63], a[68:71], a[236:239], v[48:63]
	ds_read_b128 a[236:239], v192 offset:44032
	global_load_lds_dwordx4 v244, s[34:35] offset:1024 sc1
	v_exp_f32_e32 v203, v131
	v_add_f32_e32 v202, 1.0, v202
	s_waitcnt lgkmcnt(2)
	v_mfma_f32_32x32x16_f16 v[32:47], a[72:75], a[240:243], v[32:47]
	ds_read_b128 a[240:243], v192 offset:45056
	v_add_f32_e32 v203, 1.0, v203
	v_rcp_f32_e32 v200, v200
	v_mfma_f32_32x32x16_f16 v[48:63], a[72:75], a[244:247], v[48:63]
	ds_read_b128 a[244:247], v192 offset:46080
	v_rcp_f32_e32 v201, v201
	v_fma_f32 v200, v200, 2.0, -1.0
	v_mfma_f32_32x32x16_f16 v[32:47], a[76:79], a[248:251], v[32:47]
	ds_read_b128 a[248:251], v192 offset:47104
	v_rcp_f32_e32 v202, v202
	v_fma_f32 v201, v201, 2.0, -1.0
	v_mul_f32_e32 v216, v212, v200
	v_mfma_f32_32x32x16_f16 v[48:63], a[76:79], a[252:255], v[48:63]
	ds_read_b128 a[252:255], v192 offset:48128
	global_load_lds_dwordx4 v244, s[34:35] offset:2048 sc1
	v_rcp_f32_e32 v203, v203
	v_fma_f32 v202, v202, 2.0, -1.0
	v_mul_f32_e32 v217, v213, v201
	v_mfma_f32_32x32x16_f16 v[32:47], a[80:83], a[224:227], v[32:47]
	ds_read_b128 a[224:227], v192 offset:49152
	v_fma_f32 v203, v203, 2.0, -1.0
	v_mul_f32_e32 v218, v214, v202
	v_exp_f32_e32 v200, v16
	v_mfma_f32_32x32x16_f16 v[48:63], a[80:83], a[228:231], v[48:63]
	ds_read_b128 a[228:231], v192 offset:50176
	v_mul_f32_e32 v219, v215, v203
	v_mul_f32_e32 v236, v216, v228
	v_exp_f32_e32 v201, v17
	s_waitcnt lgkmcnt(2)
	v_mfma_f32_32x32x16_f16 v[32:47], a[84:87], a[232:235], v[32:47]
	ds_read_b128 a[232:235], v192 offset:51200
	v_mul_f32_e32 v237, v216, v232
	v_fmac_f32_e32 v236, v217, v229
	v_exp_f32_e32 v202, v18
	v_mfma_f32_32x32x16_f16 v[48:63], a[84:87], a[236:239], v[48:63]
	ds_read_b128 a[236:239], v192 offset:52224
	global_load_lds_dwordx4 v244, s[34:35] offset:3072 sc1
	v_fmac_f32_e32 v237, v217, v233
	v_fmac_f32_e32 v236, v218, v230
	v_exp_f32_e32 v203, v19
	v_mfma_f32_32x32x16_f16 v[32:47], a[88:91], a[240:243], v[32:47]
	ds_read_b128 a[240:243], v192 offset:53248
	v_fmac_f32_e32 v237, v218, v234
	v_fmac_f32_e32 v236, v219, v231
	v_exp_f32_e32 v204, v20
	v_mfma_f32_32x32x16_f16 v[48:63], a[88:91], a[244:247], v[48:63]
	ds_read_b128 a[244:247], v192 offset:54272
	v_fmac_f32_e32 v237, v219, v235
	v_mov_b32_e32 v238, v236
	v_exp_f32_e32 v205, v21
	v_mfma_f32_32x32x16_f16 v[32:47], a[92:95], a[248:251], v[32:47]
	ds_read_b128 a[248:251], v192 offset:55296
	v_mov_b32_e32 v239, v236
	v_mov_b32_e32 v240, v237
	v_exp_f32_e32 v206, v22
	s_mov_b32 m0, s59
	v_mfma_f32_32x32x16_f16 v[48:63], a[92:95], a[252:255], v[48:63]
	ds_read_b128 a[252:255], v192 offset:56320
	global_load_lds_dwordx4 v245, s[34:35] sc1
	v_mov_b32_e32 v241, v237
	v_cvt_pk_f16_f32 v220, v216, v217
	v_exp_f32_e32 v207, v23
	s_waitcnt lgkmcnt(2)
	v_mfma_f32_32x32x16_f16 v[32:47], a[96:99], a[224:227], v[32:47]
	ds_read_b128 a[224:227], v192 offset:57344
	s_nop 1
	v_permlane32_swap_b32_e32 v238, v239
	v_permlane32_swap_b32_e32 v240, v241
	v_add_f32_e32 v238, v238, v239
	v_add_f32_e32 v239, v240, v241
	ds_write_b64 v248, v[238:239] offset:0
	v_exp_f32_e32 v208, v24
	v_mfma_f32_32x32x16_f16 v[48:63], a[96:99], a[228:231], v[48:63]
	ds_read_b128 a[228:231], v192 offset:58368
	v_cvt_pk_f16_f32 v221, v218, v219
	v_exp_f32_e32 v209, v25
	v_add_f32_e32 v200, 1.0, v200
	v_mfma_f32_32x32x16_f16 v[32:47], a[100:103], a[232:235], v[32:47]
	ds_read_b128 a[232:235], v192 offset:59392
	v_exp_f32_e32 v210, v26
	v_add_f32_e32 v201, 1.0, v201
	v_add_f32_e32 v202, 1.0, v202
	v_mfma_f32_32x32x16_f16 v[48:63], a[100:103], a[236:239], v[48:63]
	ds_read_b128 a[236:239], v192 offset:60416
	global_load_lds_dwordx4 v245, s[34:35] offset:1024 sc1
	v_exp_f32_e32 v211, v27
	v_add_f32_e32 v203, 1.0, v203
	v_add_f32_e32 v204, 1.0, v204
	v_mfma_f32_32x32x16_f16 v[32:47], a[104:107], a[240:243], v[32:47]
	ds_read_b128 a[240:243], v192 offset:61440
	v_exp_f32_e32 v212, v28
	v_add_f32_e32 v205, 1.0, v205
	v_add_f32_e32 v206, 1.0, v206
	v_mfma_f32_32x32x16_f16 v[48:63], a[104:107], a[244:247], v[48:63]
	ds_read_b128 a[244:247], v192 offset:62464
	v_exp_f32_e32 v213, v29
	v_add_f32_e32 v207, 1.0, v207
	v_add_f32_e32 v208, 1.0, v208
	s_waitcnt lgkmcnt(2)
	v_mfma_f32_32x32x16_f16 v[32:47], a[108:111], a[248:251], v[32:47]
	ds_read_b128 a[248:251], v192 offset:63488
	v_exp_f32_e32 v214, v30
	v_add_f32_e32 v209, 1.0, v209
	v_add_f32_e32 v210, 1.0, v210
	v_mfma_f32_32x32x16_f16 v[48:63], a[108:111], a[252:255], v[48:63]
	ds_read_b128 a[252:255], v192 offset:64512
	global_load_lds_dwordx4 v245, s[34:35] offset:2048 sc1
	v_exp_f32_e32 v215, v31
	v_add_f32_e32 v211, 1.0, v211
	v_add_f32_e32 v212, 1.0, v212
	s_waitcnt vmcnt(7)
	s_barrier
	v_mfma_f32_32x32x16_f16 v[32:47], a[112:115], a[224:227], v[32:47]
	ds_read_b128 a[224:227], v193 offset:0
	v_add_f32_e32 v213, 1.0, v213
	v_add_f32_e32 v214, 1.0, v214
	v_rcp_f32_e32 v200, v200
	v_mfma_f32_32x32x16_f16 v[48:63], a[112:115], a[228:231], v[48:63]
	ds_read_b128 a[228:231], v193 offset:1024
	v_add_f32_e32 v215, 1.0, v215
	v_rcp_f32_e32 v201, v201
	v_mfma_f32_32x32x16_f16 v[32:47], a[116:119], a[232:235], v[32:47]
	ds_read_b128 a[232:235], v193 offset:2048
	v_rcp_f32_e32 v202, v202
	v_mfma_f32_32x32x16_f16 v[48:63], a[116:119], a[236:239], v[48:63]
	ds_read_b128 a[236:239], v193 offset:3072
	global_load_lds_dwordx4 v245, s[34:35] offset:3072 sc1
	v_rcp_f32_e32 v203, v203
	s_waitcnt lgkmcnt(2)
	v_mfma_f32_32x32x16_f16 v[32:47], a[120:123], a[240:243], v[32:47]
	ds_read_b128 a[240:243], v193 offset:4096
	v_rcp_f32_e32 v204, v204
	s_add_u32 s46, s42, 0x6000
	s_addc_u32 s47, s43, 0
	global_load_dwordx4 v[96:99], v192, s[46:47] offset:0
	v_mfma_f32_32x32x16_f16 v[48:63], a[120:123], a[244:247], v[48:63]
	ds_read_b128 a[244:247], v193 offset:5120
	v_rcp_f32_e32 v205, v205
	v_mul_f32_e32 v204, v204, v132
	global_load_dwordx4 v[100:103], v192, s[46:47] offset:1024
	global_load_dwordx4 v[104:107], v192, s[46:47] offset:2048
	v_mfma_f32_32x32x16_f16 v[32:47], a[124:127], a[248:251], v[32:47]
	ds_read_b128 a[248:251], v193 offset:6144
	v_rcp_f32_e32 v206, v206
	v_mul_f32_e32 v205, v205, v133
	global_load_dwordx4 v[108:111], v192, s[46:47] offset:3072
	s_add_u32 s46, s42, 0x7000
	s_addc_u32 s47, s43, 0
	s_mov_b32 m0, s52
	v_mfma_f32_32x32x16_f16 v[48:63], a[124:127], a[252:255], v[48:63]
	ds_read_b128 a[252:255], v193 offset:7168
	v_cmp_gt_u32_e32 vcc, 3, v251
	s_cbranch_vccnz .LD_tpoll27
.LD_tok26:
	s_add_u32 s34, s34, 0x20000
	s_addc_u32 s35, s35, 0
	global_load_lds_dwordx4 v224, s[34:35] sc1
	v_rcp_f32_e32 v207, v207
	v_mul_f32_e32 v206, v206, v134
	global_load_dwordx4 v[112:115], v192, s[46:47] offset:0
	global_load_dwordx4 v[116:119], v192, s[46:47] offset:1024
	v_mfma_f32_32x32x16_f16 v[32:47], a[128:131], a[224:227], v[32:47]
	ds_read_b128 a[224:227], v193 offset:8192
	v_rcp_f32_e32 v208, v208
	v_mul_f32_e32 v207, v207, v135
	global_load_dwordx4 v[120:123], v192, s[46:47] offset:2048
	global_load_dwordx4 v[124:127], v192, s[46:47] offset:3072
	v_mfma_f32_32x32x16_f16 v[48:63], a[128:131], a[228:231], v[48:63]
	ds_read_b128 a[228:231], v193 offset:9216
	v_rcp_f32_e32 v209, v209
	v_fmamk_f32 v208, v208, 0xc0b8aa3b, v198
	s_waitcnt lgkmcnt(2)
	v_mfma_f32_32x32x16_f16 v[32:47], a[132:135], a[232:235], v[32:47]
	ds_read_b128 a[232:235], v193 offset:10240
	v_rcp_f32_e32 v210, v210
	v_fmamk_f32 v209, v209, 0xc0b8aa3b, v198
	v_fma_f32 v132, v200, v208, v204
	v_mfma_f32_32x32x16_f16 v[48:63], a[132:135], a[236:239], v[48:63]
	ds_read_b128 a[236:239], v193 offset:11264
	global_load_lds_dwordx4 v224, s[34:35] offset:1024 sc1
	v_rcp_f32_e32 v211, v211
	v_fmamk_f32 v210, v210, 0xc0b8aa3b, v198
	v_fma_f32 v133, v201, v209, v205
	v_mfma_f32_32x32x16_f16 v[32:47], a[136:139], a[240:243], v[32:47]
	ds_read_b128 a[240:243], v193 offset:12288
	v_rcp_f32_e32 v212, v212
	v_fmamk_f32 v211, v211, 0xc0b8aa3b, v198
	v_fma_f32 v134, v202, v210, v206
	v_mfma_f32_32x32x16_f16 v[48:63], a[136:139], a[244:247], v[48:63]
	ds_read_b128 a[244:247], v193 offset:13312
	v_rcp_f32_e32 v213, v213
	v_fma_f32 v135, v203, v211, v207
	v_mfma_f32_32x32x16_f16 v[32:47], a[140:143], a[248:251], v[32:47]
	ds_read_b128 a[248:251], v193 offset:14336
	v_rcp_f32_e32 v214, v214
	v_mfma_f32_32x32x16_f16 v[48:63], a[140:143], a[252:255], v[48:63]
	ds_read_b128 a[252:255], v193 offset:15360
	global_load_lds_dwordx4 v224, s[34:35] offset:2048 sc1
	v_rcp_f32_e32 v215, v215
	s_waitcnt lgkmcnt(2)
	v_mfma_f32_32x32x16_f16 v[32:47], a[144:147], a[224:227], v[32:47]
	ds_read_b128 a[224:227], v193 offset:16384
	v_exp_f32_e32 v200, v132
	v_mfma_f32_32x32x16_f16 v[48:63], a[144:147], a[228:231], v[48:63]
	ds_read_b128 a[228:231], v193 offset:17408
	v_exp_f32_e32 v201, v133
	v_add_f32_e32 v200, 1.0, v200
	v_mfma_f32_32x32x16_f16 v[32:47], a[148:151], a[232:235], v[32:47]
	ds_read_b128 a[232:235], v193 offset:18432
	v_exp_f32_e32 v202, v134
	v_add_f32_e32 v201, 1.0, v201
	v_mfma_f32_32x32x16_f16 v[48:63], a[148:151], a[236:239], v[48:63]
	ds_read_b128 a[236:239], v193 offset:19456
	global_load_lds_dwordx4 v224, s[34:35] offset:3072 sc1
	v_exp_f32_e32 v203, v135
	v_add_f32_e32 v202, 1.0, v202
	v_mfma_f32_32x32x16_f16 v[32:47], a[152:155], a[240:243], v[32:47]
	ds_read_b128 a[240:243], v193 offset:20480
	v_add_f32_e32 v203, 1.0, v203
	v_rcp_f32_e32 v200, v200
	v_mfma_f32_32x32x16_f16 v[48:63], a[152:155], a[244:247], v[48:63]
	ds_read_b128 a[244:247], v193 offset:21504
	v_rcp_f32_e32 v201, v201
	v_fma_f32 v200, v200, 2.0, -1.0
	s_waitcnt lgkmcnt(2)
	v_mfma_f32_32x32x16_f16 v[32:47], a[156:159], a[248:251], v[32:47]
	ds_read_b128 a[248:251], v193 offset:22528
	v_rcp_f32_e32 v202, v202
	v_fma_f32 v201, v201, 2.0, -1.0
	v_mul_f32_e32 v216, v212, v200
	s_mov_b32 m0, s53
	v_mfma_f32_32x32x16_f16 v[48:63], a[156:159], a[252:255], v[48:63]
	ds_read_b128 a[252:255], v193 offset:23552
	global_load_lds_dwordx4 v225, s[34:35] sc1
	v_rcp_f32_e32 v203, v203
	v_fma_f32 v202, v202, 2.0, -1.0
	v_mul_f32_e32 v217, v213, v201
	v_mfma_f32_32x32x16_f16 v[32:47], a[160:163], a[224:227], v[32:47]
	ds_read_b128 a[224:227], v193 offset:24576
	v_fma_f32 v203, v203, 2.0, -1.0
	v_mul_f32_e32 v218, v214, v202
	v_mfma_f32_32x32x16_f16 v[48:63], a[160:163], a[228:231], v[48:63]
	ds_read_b128 a[228:231], v193 offset:25600
	v_mul_f32_e32 v219, v215, v203
	v_mul_f32_e32 v236, v216, v228
	v_mfma_f32_32x32x16_f16 v[32:47], a[164:167], a[232:235], v[32:47]
	ds_read_b128 a[232:235], v193 offset:26624
	v_mul_f32_e32 v237, v216, v232
	v_fmac_f32_e32 v236, v217, v229
	v_mfma_f32_32x32x16_f16 v[48:63], a[164:167], a[236:239], v[48:63]
	ds_read_b128 a[236:239], v193 offset:27648
	global_load_lds_dwordx4 v225, s[34:35] offset:1024 sc1
	v_fmac_f32_e32 v237, v217, v233
	v_fmac_f32_e32 v236, v218, v230
	s_waitcnt lgkmcnt(2)
	v_mfma_f32_32x32x16_f16 v[32:47], a[168:171], a[240:243], v[32:47]
	ds_read_b128 a[240:243], v193 offset:28672
	v_fmac_f32_e32 v237, v218, v234
	v_fmac_f32_e32 v236, v219, v231
	v_mfma_f32_32x32x16_f16 v[48:63], a[168:171], a[244:247], v[48:63]
	ds_read_b128 a[244:247], v193 offset:29696
	v_fmac_f32_e32 v237, v219, v235
	v_mov_b32_e32 v238, v236
	v_mfma_f32_32x32x16_f16 v[32:47], a[172:175], a[248:251], v[32:47]
	ds_read_b128 a[248:251], v193 offset:30720
	v_mov_b32_e32 v239, v236
	v_mov_b32_e32 v240, v237
	v_mfma_f32_32x32x16_f16 v[48:63], a[172:175], a[252:255], v[48:63]
	ds_read_b128 a[252:255], v193 offset:31744
	global_load_lds_dwordx4 v225, s[34:35] offset:2048 sc1
	v_mov_b32_e32 v241, v237
	v_cvt_pk_f16_f32 v222, v216, v217
	s_waitcnt vmcnt(15)
	s_barrier
	v_mfma_f32_32x32x16_f16 v[32:47], a[176:179], a[224:227], v[32:47]
	ds_read_b128 a[224:227], v193 offset:32768
	s_nop 1
	v_permlane32_swap_b32_e32 v238, v239
	v_permlane32_swap_b32_e32 v240, v241
	v_add_f32_e32 v238, v238, v239
	v_add_f32_e32 v239, v240, v241
	ds_write_b64 v248, v[238:239] offset:256
	v_mfma_f32_32x32x16_f16 v[48:63], a[176:179], a[228:231], v[48:63]
	ds_read_b128 a[228:231], v193 offset:33792
	v_cvt_pk_f16_f32 v223, v218, v219
	s_waitcnt lgkmcnt(3)
	v_mfma_f32_32x32x16_f16 v[32:47], a[180:183], a[232:235], v[32:47]
	ds_read_b128 a[232:235], v193 offset:34816
	s_nop 1
	v_permlane32_swap_b32_e32 v220, v222
	v_permlane32_swap_b32_e32 v221, v223
	s_cmp_eq_u32 s31, 0
	s_cbranch_scc1 .LD_slow28
	global_store_dwordx4 v195, v[220:223], s[36:37] offset:0
.LD_join29:
	v_mfma_f32_32x32x16_f16 v[48:63], a[180:183], a[236:239], v[48:63]
	ds_read_b128 a[236:239], v193 offset:35840
	global_load_lds_dwordx4 v225, s[34:35] offset:3072 sc1
	v_mfma_f32_32x32x16_f16 v[32:47], a[184:187], a[240:243], v[32:47]
	ds_read_b128 a[240:243], v193 offset:36864
	v_mfma_f32_32x32x16_f16 v[48:63], a[184:187], a[244:247], v[48:63]
	ds_read_b128 a[244:247], v193 offset:37888
	v_mfma_f32_32x32x16_f16 v[32:47], a[188:191], a[248:251], v[32:47]
	ds_read_b128 a[248:251], v193 offset:38912
	s_mov_b32 m0, s54
	v_mfma_f32_32x32x16_f16 v[48:63], a[188:191], a[252:255], v[48:63]
	ds_read_b128 a[252:255], v193 offset:39936
	global_load_lds_dwordx4 v226, s[34:35] sc1
	s_waitcnt lgkmcnt(2)
	v_mfma_f32_32x32x16_f16 v[32:47], a[192:195], a[224:227], v[32:47]
	ds_read_b128 a[224:227], v193 offset:40960
	v_mfma_f32_32x32x16_f16 v[48:63], a[192:195], a[228:231], v[48:63]
	ds_read_b128 a[228:231], v193 offset:41984
	v_mfma_f32_32x32x16_f16 v[32:47], a[196:199], a[232:235], v[32:47]
	ds_read_b128 a[232:235], v193 offset:43008
	v_mfma_f32_32x32x16_f16 v[48:63], a[196:199], a[236:239], v[48:63]
	ds_read_b128 a[236:239], v193 offset:44032
	global_load_lds_dwordx4 v226, s[34:35] offset:1024 sc1
	v_mfma_f32_32x32x16_f16 v[32:47], a[200:203], a[240:243], v[32:47]
	ds_read_b128 a[240:243], v193 offset:45056
	v_mfma_f32_32x32x16_f16 v[48:63], a[200:203], a[244:247], v[48:63]
	ds_read_b128 a[244:247], v193 offset:46080
	s_waitcnt lgkmcnt(2)
	v_mfma_f32_32x32x16_f16 v[32:47], a[204:207], a[248:251], v[32:47]
	ds_read_b128 a[248:251], v193 offset:47104
	v_mfma_f32_32x32x16_f16 v[48:63], a[204:207], a[252:255], v[48:63]
	ds_read_b128 a[252:255], v193 offset:48128
	global_load_lds_dwordx4 v226, s[34:35] offset:2048 sc1
	s_waitcnt vmcnt(4)
	s_barrier
	v_mov_b32_e32 v199, 1
	s_cmp_eq_u32 s31, 0
	s_cbranch_scc1 .LD_slow30
	global_store_dword v197, v199, s[40:41]
.LD_join31:
	ds_read_b64 v[200:201], v249 offset:0
	ds_read_b64 v[202:203], v249 offset:2048
	ds_read_b64 v[204:205], v249 offset:4096
	ds_read_b64 v[206:207], v249 offset:6144
	v_mfma_f32_32x32x16_f16 v[32:47], a[208:211], a[224:227], v[32:47]
	ds_read_b128 a[224:227], v193 offset:49152
	v_mfma_f32_32x32x16_f16 v[48:63], a[208:211], a[228:231], v[48:63]
	ds_read_b128 a[228:231], v193 offset:50176
	v_mfma_f32_32x32x16_f16 v[32:47], a[212:215], a[232:235], v[32:47]
	ds_read_b128 a[232:235], v193 offset:51200
	v_mfma_f32_32x32x16_f16 v[48:63], a[212:215], a[236:239], v[48:63]
	ds_read_b128 a[236:239], v193 offset:52224
	global_load_lds_dwordx4 v226, s[34:35] offset:3072 sc1
	s_waitcnt lgkmcnt(2)
	v_mfma_f32_32x32x16_f16 v[32:47], a[216:219], a[240:243], v[32:47]
	ds_read_b128 a[240:243], v193 offset:53248
	v_mfma_f32_32x32x16_f16 v[48:63], a[216:219], a[244:247], v[48:63]
	ds_read_b128 a[244:247], v193 offset:54272
	v_mfma_f32_32x32x16_f16 v[32:47], a[220:223], a[248:251], v[32:47]
	ds_read_b128 a[248:251], v193 offset:55296
	s_mov_b32 m0, s55
	v_mfma_f32_32x32x16_f16 v[48:63], a[220:223], a[252:255], v[48:63]
	ds_read_b128 a[252:255], v193 offset:56320
	global_load_lds_dwordx4 v227, s[34:35] sc1
	v_mfma_f32_32x32x16_f16 v[32:47], v[160:163], a[224:227], v[32:47]
	ds_read_b128 a[224:227], v193 offset:57344
	v_mfma_f32_32x32x16_f16 v[48:63], v[160:163], a[228:231], v[48:63]
	ds_read_b128 a[228:231], v193 offset:58368
	s_waitcnt lgkmcnt(2)
	v_mfma_f32_32x32x16_f16 v[32:47], v[164:167], a[232:235], v[32:47]
	ds_read_b128 a[232:235], v193 offset:59392
	v_mfma_f32_32x32x16_f16 v[48:63], v[164:167], a[236:239], v[48:63]
	ds_read_b128 a[236:239], v193 offset:60416
	global_load_lds_dwordx4 v227, s[34:35] offset:1024 sc1
	v_add_f32_e32 v200, v200, v202
	v_add_f32_e32 v201, v201, v203
	v_add_f32_e32 v200, v200, v204
	v_add_f32_e32 v201, v201, v205
	v_add_f32_e32 v200, v200, v206
	v_add_f32_e32 v201, v201, v207
	global_store_dwordx2 v250, v[200:201], s[72:73]
	v_mfma_f32_32x32x16_f16 v[32:47], v[168:171], a[240:243], v[32:47]
	ds_read_b128 a[240:243], v193 offset:61440
	v_mfma_f32_32x32x16_f16 v[48:63], v[168:171], a[244:247], v[48:63]
	ds_read_b128 a[244:247], v193 offset:62464
	v_mfma_f32_32x32x16_f16 v[32:47], v[172:175], a[248:251], v[32:47]
	ds_read_b128 a[248:251], v193 offset:63488
	v_mfma_f32_32x32x16_f16 v[48:63], v[172:175], a[252:255], v[48:63]
	ds_read_b128 a[252:255], v193 offset:64512
	global_load_lds_dwordx4 v227, s[34:35] offset:2048 sc1
	s_and_b32 s64, s33, 1
	s_lshl_b32 s64, s64, 22
	s_add_u32 s64, s64, s50
	s_add_u32 s64, s64, 0x20000
	s_add_u32 s36, s6, s64
	s_addc_u32 s37, s7, 0
	s_lshl_b32 s64, s33, 3
	s_add_u32 s64, s64, s29
	s_lshl_b32 s64, s64, 5
	s_add_u32 s64, s64, s30
	s_lshl_b32 s64, s64, 2
	s_add_u32 s40, s8, s64
	s_addc_u32 s41, s9, 0
	s_lshl_b32 s64, s33, 19
	s_add_u32 s64, s64, 0x200
	s_add_u32 s72, s62, s64
	s_addc_u32 s73, s63, 0
	s_waitcnt vmcnt(9)
	s_barrier
	s_waitcnt lgkmcnt(2)
	v_mfma_f32_32x32x16_f16 v[32:47], v[176:179], a[224:227], v[32:47]
	ds_read_b128 a[224:227], v192 offset:0
	v_mfma_f32_32x32x16_f16 v[48:63], v[176:179], a[228:231], v[48:63]
	ds_read_b128 a[228:231], v192 offset:1024
	v_mfma_f32_32x32x16_f16 v[32:47], v[180:183], a[232:235], v[32:47]
	ds_read_b128 a[232:235], v192 offset:2048
	v_mfma_f32_32x32x16_f16 v[48:63], v[180:183], a[236:239], v[48:63]
	ds_read_b128 a[236:239], v192 offset:3072
	global_load_lds_dwordx4 v227, s[34:35] offset:3072 sc1
	v_mfma_f32_32x32x16_f16 v[32:47], v[184:187], a[240:243], v[32:47]
	ds_read_b128 a[240:243], v192 offset:4096
	v_mfma_f32_32x32x16_f16 v[48:63], v[184:187], a[244:247], v[48:63]
	ds_read_b128 a[244:247], v192 offset:5120
	s_waitcnt lgkmcnt(2)
	v_mfma_f32_32x32x16_f16 v[32:47], v[188:191], a[248:251], v[32:47]
	ds_read_b128 a[248:251], v192 offset:6144
	s_mov_b32 m0, s56
	v_mfma_f32_32x32x16_f16 v[48:63], v[188:191], a[252:255], v[48:63]
	ds_read_b128 a[252:255], v192 offset:7168
	global_load_lds_dwordx4 v242, s[34:35] sc1
	s_nop 5
	s_waitcnt lgkmcnt(2)
	v_mfma_f32_32x32x16_f16 v[64:79], a[0:3], a[224:227], v[64:79]
	ds_read_b128 a[224:227], v192 offset:8192
	v_exp_f32_e32 v200, v32
	v_mfma_f32_32x32x16_f16 v[80:95], a[0:3], a[228:231], v[80:95]
	ds_read_b128 a[228:231], v192 offset:9216
	global_load_dword v251, v196, s[38:39] sc1
	v_exp_f32_e32 v201, v33
	v_add_f32_e32 v200, 1.0, v200
	v_mfma_f32_32x32x16_f16 v[64:79], a[4:7], a[232:235], v[64:79]
	ds_read_b128 a[232:235], v192 offset:10240
	v_exp_f32_e32 v202, v34
	v_add_f32_e32 v201, 1.0, v201
	v_mfma_f32_32x32x16_f16 v[80:95], a[4:7], a[236:239], v[80:95]
	ds_read_b128 a[236:239], v192 offset:11264
	global_load_lds_dwordx4 v242, s[34:35] offset:1024 sc1
	v_exp_f32_e32 v203, v35
	v_add_f32_e32 v202, 1.0, v202
	v_mfma_f32_32x32x16_f16 v[64:79], a[8:11], a[240:243], v[64:79]
	ds_read_b128 a[240:243], v192 offset:12288
	v_exp_f32_e32 v204, v36
	v_add_f32_e32 v203, 1.0, v203
	v_mfma_f32_32x32x16_f16 v[80:95], a[8:11], a[244:247], v[80:95]
	ds_read_b128 a[244:247], v192 offset:13312
	v_exp_f32_e32 v205, v37
	v_add_f32_e32 v204, 1.0, v204
	s_waitcnt lgkmcnt(2)
	v_mfma_f32_32x32x16_f16 v[64:79], a[12:15], a[248:251], v[64:79]
	ds_read_b128 a[248:251], v192 offset:14336
	v_exp_f32_e32 v206, v38
	v_add_f32_e32 v205, 1.0, v205
	v_mfma_f32_32x32x16_f16 v[80:95], a[12:15], a[252:255], v[80:95]
	ds_read_b128 a[252:255], v192 offset:15360
	global_load_lds_dwordx4 v242, s[34:35] offset:2048 sc1
	v_exp_f32_e32 v207, v39
	v_add_f32_e32 v206, 1.0, v206
	v_mfma_f32_32x32x16_f16 v[64:79], a[16:19], a[224:227], v[64:79]
	ds_read_b128 a[224:227], v192 offset:16384
	v_exp_f32_e32 v208, v40
	v_add_f32_e32 v207, 1.0, v207
	v_mfma_f32_32x32x16_f16 v[80:95], a[16:19], a[228:231], v[80:95]
	ds_read_b128 a[228:231], v192 offset:17408
	v_exp_f32_e32 v209, v41
	v_add_f32_e32 v208, 1.0, v208
	v_mfma_f32_32x32x16_f16 v[64:79], a[20:23], a[232:235], v[64:79]
	ds_read_b128 a[232:235], v192 offset:18432
	v_exp_f32_e32 v210, v42
	v_add_f32_e32 v209, 1.0, v209
	v_mfma_f32_32x32x16_f16 v[80:95], a[20:23], a[236:239], v[80:95]
	ds_read_b128 a[236:239], v192 offset:19456
	global_load_lds_dwordx4 v242, s[34:35] offset:3072 sc1
	v_exp_f32_e32 v211, v43
	v_add_f32_e32 v210, 1.0, v210
	s_waitcnt lgkmcnt(2)
	v_mfma_f32_32x32x16_f16 v[64:79], a[24:27], a[240:243], v[64:79]
	ds_read_b128 a[240:243], v192 offset:20480
	v_exp_f32_e32 v212, v44
	v_add_f32_e32 v211, 1.0, v211
	v_mfma_f32_32x32x16_f16 v[80:95], a[24:27], a[244:247], v[80:95]
	ds_read_b128 a[244:247], v192 offset:21504
	v_exp_f32_e32 v213, v45
	v_add_f32_e32 v212, 1.0, v212
	v_mfma_f32_32x32x16_f16 v[64:79], a[28:31], a[248:251], v[64:79]
	ds_read_b128 a[248:251], v192 offset:22528
	v_exp_f32_e32 v214, v46
	v_add_f32_e32 v213, 1.0, v213
	s_mov_b32 m0, s57
	v_mfma_f32_32x32x16_f16 v[80:95], a[28:31], a[252:255], v[80:95]
	ds_read_b128 a[252:255], v192 offset:23552
	global_load_lds_dwordx4 v243, s[34:35] sc1
	v_exp_f32_e32 v215, v47
	v_add_f32_e32 v214, 1.0, v214
	v_mfma_f32_32x32x16_f16 v[64:79], a[32:35], a[224:227], v[64:79]
	ds_read_b128 a[224:227], v192 offset:24576
	v_add_f32_e32 v215, 1.0, v215
	v_rcp_f32_e32 v200, v200
	v_mfma_f32_32x32x16_f16 v[80:95], a[32:35], a[228:231], v[80:95]
	ds_read_b128 a[228:231], v192 offset:25600
	v_rcp_f32_e32 v201, v201
	s_waitcnt lgkmcnt(2)
	v_mfma_f32_32x32x16_f16 v[64:79], a[36:39], a[232:235], v[64:79]
	ds_read_b128 a[232:235], v192 offset:26624
	v_rcp_f32_e32 v202, v202
	v_mfma_f32_32x32x16_f16 v[80:95], a[36:39], a[236:239], v[80:95]
	ds_read_b128 a[236:239], v192 offset:27648
	global_load_lds_dwordx4 v243, s[34:35] offset:1024 sc1
	v_rcp_f32_e32 v203, v203
	v_mfma_f32_32x32x16_f16 v[64:79], a[40:43], a[240:243], v[64:79]
	ds_read_b128 a[240:243], v192 offset:28672
	v_rcp_f32_e32 v204, v204
	v_mfma_f32_32x32x16_f16 v[80:95], a[40:43], a[244:247], v[80:95]
	ds_read_b128 a[244:247], v192 offset:29696
	v_rcp_f32_e32 v205, v205
	v_mul_f32_e32 v204, v204, v136
	v_mfma_f32_32x32x16_f16 v[64:79], a[44:47], a[248:251], v[64:79]
	ds_read_b128 a[248:251], v192 offset:30720
	v_rcp_f32_e32 v206, v206
	v_mul_f32_e32 v205, v205, v137
	v_mfma_f32_32x32x16_f16 v[80:95], a[44:47], a[252:255], v[80:95]
	ds_read_b128 a[252:255], v192 offset:31744
	global_load_lds_dwordx4 v243, s[34:35] offset:2048 sc1
	v_rcp_f32_e32 v207, v207
	v_mul_f32_e32 v206, v206, v138
	s_waitcnt vmcnt(8)
	s_barrier
	s_waitcnt lgkmcnt(2)
	v_mfma_f32_32x32x16_f16 v[64:79], a[48:51], a[224:227], v[64:79]
	ds_read_b128 a[224:227], v192 offset:32768
	v_rcp_f32_e32 v208, v208
	v_mul_f32_e32 v207, v207, v139
	v_mfma_f32_32x32x16_f16 v[80:95], a[48:51], a[228:231], v[80:95]
	ds_read_b128 a[228:231], v192 offset:33792
	v_rcp_f32_e32 v209, v209
	v_fmamk_f32 v208, v208, 0xc0b8aa3b, v198
	v_mfma_f32_32x32x16_f16 v[64:79], a[52:55], a[232:235], v[64:79]
	ds_read_b128 a[232:235], v192 offset:34816
	v_rcp_f32_e32 v210, v210
	v_fmamk_f32 v209, v209, 0xc0b8aa3b, v198
	v_fma_f32 v136, v200, v208, v204
	v_mfma_f32_32x32x16_f16 v[80:95], a[52:55], a[236:239], v[80:95]
	ds_read_b128 a[236:239], v192 offset:35840
	global_load_lds_dwordx4 v243, s[34:35] offset:3072 sc1
	v_rcp_f32_e32 v211, v211
	v_fmamk_f32 v210, v210, 0xc0b8aa3b, v198
	v_fma_f32 v137, v201, v209, v205
	v_mfma_f32_32x32x16_f16 v[64:79], a[56:59], a[240:243], v[64:79]
	ds_read_b128 a[240:243], v192 offset:36864
	v_rcp_f32_e32 v212, v212
	v_fmamk_f32 v211, v211, 0xc0b8aa3b, v198
	v_fma_f32 v138, v202, v210, v206
	v_mfma_f32_32x32x16_f16 v[80:95], a[56:59], a[244:247], v[80:95]
	ds_read_b128 a[244:247], v192 offset:37888
	v_rcp_f32_e32 v213, v213
	v_fma_f32 v139, v203, v211, v207
	s_waitcnt lgkmcnt(2)
	v_mfma_f32_32x32x16_f16 v[64:79], a[60:63], a[248:251], v[64:79]
	ds_read_b128 a[248:251], v192 offset:38912
	v_rcp_f32_e32 v214, v214
	s_mov_b32 m0, s58
	v_mfma_f32_32x32x16_f16 v[80:95], a[60:63], a[252:255], v[80:95]
	ds_read_b128 a[252:255], v192 offset:39936
	global_load_lds_dwordx4 v244, s[34:35] sc1
	v_rcp_f32_e32 v215, v215
	v_mfma_f32_32x32x16_f16 v[64:79], a[64:67], a[224:227], v[64:79]
	ds_read_b128 a[224:227], v192 offset:40960
	v_exp_f32_e32 v200, v136
	v_mfma_f32_32x32x16_f16 v[80:95], a[64:67], a[228:231], v[80:95]
	ds_read_b128 a[228:231], v192 offset:41984
	v_exp_f32_e32 v201, v137
	v_add_f32_e32 v200, 1.0, v200
	v_mfma_f32_32x32x16_f16 v[64:79], a[68:71], a[232:235], v[64:79]
	ds_read_b128 a[232:235], v192 offset:43008
	v_exp_f32_e32 v202, v138
	v_add_f32_e32 v201, 1.0, v201
	v_mfma_f32_32x32x16_f16 v[80:95], a[68:71], a[236:239], v[80:95]
	ds_read_b128 a[236:239], v192 offset:44032
	global_load_lds_dwordx4 v244, s[34:35] offset:1024 sc1
	v_exp_f32_e32 v203, v139
	v_add_f32_e32 v202, 1.0, v202
	s_waitcnt lgkmcnt(2)
	v_mfma_f32_32x32x16_f16 v[64:79], a[72:75], a[240:243], v[64:79]
	ds_read_b128 a[240:243], v192 offset:45056
	v_add_f32_e32 v203, 1.0, v203
	v_rcp_f32_e32 v200, v200
	v_mfma_f32_32x32x16_f16 v[80:95], a[72:75], a[244:247], v[80:95]
	ds_read_b128 a[244:247], v192 offset:46080
	v_rcp_f32_e32 v201, v201
	v_fma_f32 v200, v200, 2.0, -1.0
	v_mfma_f32_32x32x16_f16 v[64:79], a[76:79], a[248:251], v[64:79]
	ds_read_b128 a[248:251], v192 offset:47104
	v_rcp_f32_e32 v202, v202
	v_fma_f32 v201, v201, 2.0, -1.0
	v_mul_f32_e32 v216, v212, v200
	v_mfma_f32_32x32x16_f16 v[80:95], a[76:79], a[252:255], v[80:95]
	ds_read_b128 a[252:255], v192 offset:48128
	global_load_lds_dwordx4 v244, s[34:35] offset:2048 sc1
	v_rcp_f32_e32 v203, v203
	v_fma_f32 v202, v202, 2.0, -1.0
	v_mul_f32_e32 v217, v213, v201
	v_mfma_f32_32x32x16_f16 v[64:79], a[80:83], a[224:227], v[64:79]
	ds_read_b128 a[224:227], v192 offset:49152
	v_fma_f32 v203, v203, 2.0, -1.0
	v_mul_f32_e32 v218, v214, v202
	v_exp_f32_e32 v200, v48
	v_mfma_f32_32x32x16_f16 v[80:95], a[80:83], a[228:231], v[80:95]
	ds_read_b128 a[228:231], v192 offset:50176
	v_mul_f32_e32 v219, v215, v203
	v_mul_f32_e32 v236, v216, v228
	v_exp_f32_e32 v201, v49
	s_waitcnt lgkmcnt(2)
	v_mfma_f32_32x32x16_f16 v[64:79], a[84:87], a[232:235], v[64:79]
	ds_read_b128 a[232:235], v192 offset:51200
	v_mul_f32_e32 v237, v216, v232
	v_fmac_f32_e32 v236, v217, v229
	v_exp_f32_e32 v202, v50
	v_mfma_f32_32x32x16_f16 v[80:95], a[84:87], a[236:239], v[80:95]
	ds_read_b128 a[236:239], v192 offset:52224
	global_load_lds_dwordx4 v244, s[34:35] offset:3072 sc1
	v_fmac_f32_e32 v237, v217, v233
	v_fmac_f32_e32 v236, v218, v230
	v_exp_f32_e32 v203, v51
	v_mfma_f32_32x32x16_f16 v[64:79], a[88:91], a[240:243], v[64:79]
	ds_read_b128 a[240:243], v192 offset:53248
	v_fmac_f32_e32 v237, v218, v234
	v_fmac_f32_e32 v236, v219, v231
	v_exp_f32_e32 v204, v52
	v_mfma_f32_32x32x16_f16 v[80:95], a[88:91], a[244:247], v[80:95]
	ds_read_b128 a[244:247], v192 offset:54272
	v_fmac_f32_e32 v237, v219, v235
	v_mov_b32_e32 v238, v236
	v_exp_f32_e32 v205, v53
	v_mfma_f32_32x32x16_f16 v[64:79], a[92:95], a[248:251], v[64:79]
	ds_read_b128 a[248:251], v192 offset:55296
	v_mov_b32_e32 v239, v236
	v_mov_b32_e32 v240, v237
	v_exp_f32_e32 v206, v54
	s_mov_b32 m0, s59
	v_mfma_f32_32x32x16_f16 v[80:95], a[92:95], a[252:255], v[80:95]
	ds_read_b128 a[252:255], v192 offset:56320
	global_load_lds_dwordx4 v245, s[34:35] sc1
	v_mov_b32_e32 v241, v237
	v_cvt_pk_f16_f32 v220, v216, v217
	v_exp_f32_e32 v207, v55
	s_waitcnt lgkmcnt(2)
	v_mfma_f32_32x32x16_f16 v[64:79], a[96:99], a[224:227], v[64:79]
	ds_read_b128 a[224:227], v192 offset:57344
	s_nop 1
	v_permlane32_swap_b32_e32 v238, v239
	v_permlane32_swap_b32_e32 v240, v241
	v_add_f32_e32 v238, v238, v239
	v_add_f32_e32 v239, v240, v241
	ds_write_b64 v248, v[238:239] offset:512
	v_exp_f32_e32 v208, v56
	v_mfma_f32_32x32x16_f16 v[80:95], a[96:99], a[228:231], v[80:95]
	ds_read_b128 a[228:231], v192 offset:58368
	v_cvt_pk_f16_f32 v221, v218, v219
	v_exp_f32_e32 v209, v57
	v_add_f32_e32 v200, 1.0, v200
	v_mfma_f32_32x32x16_f16 v[64:79], a[100:103], a[232:235], v[64:79]
	ds_read_b128 a[232:235], v192 offset:59392
	v_exp_f32_e32 v210, v58
	v_add_f32_e32 v201, 1.0, v201
	v_add_f32_e32 v202, 1.0, v202
	v_mfma_f32_32x32x16_f16 v[80:95], a[100:103], a[236:239], v[80:95]
	ds_read_b128 a[236:239], v192 offset:60416
	global_load_lds_dwordx4 v245, s[34:35] offset:1024 sc1
	v_exp_f32_e32 v211, v59
	v_add_f32_e32 v203, 1.0, v203
	v_add_f32_e32 v204, 1.0, v204
	v_mfma_f32_32x32x16_f16 v[64:79], a[104:107], a[240:243], v[64:79]
	ds_read_b128 a[240:243], v192 offset:61440
	v_exp_f32_e32 v212, v60
	v_add_f32_e32 v205, 1.0, v205
	v_add_f32_e32 v206, 1.0, v206
	v_mfma_f32_32x32x16_f16 v[80:95], a[104:107], a[244:247], v[80:95]
	ds_read_b128 a[244:247], v192 offset:62464
	v_exp_f32_e32 v213, v61
	v_add_f32_e32 v207, 1.0, v207
	v_add_f32_e32 v208, 1.0, v208
	s_waitcnt lgkmcnt(2)
	v_mfma_f32_32x32x16_f16 v[64:79], a[108:111], a[248:251], v[64:79]
	ds_read_b128 a[248:251], v192 offset:63488
	v_exp_f32_e32 v214, v62
	v_add_f32_e32 v209, 1.0, v209
	v_add_f32_e32 v210, 1.0, v210
	v_mfma_f32_32x32x16_f16 v[80:95], a[108:111], a[252:255], v[80:95]
	ds_read_b128 a[252:255], v192 offset:64512
	global_load_lds_dwordx4 v245, s[34:35] offset:2048 sc1
	v_exp_f32_e32 v215, v63
	v_add_f32_e32 v211, 1.0, v211
	v_add_f32_e32 v212, 1.0, v212
	s_waitcnt vmcnt(7)
	s_barrier
	v_mfma_f32_32x32x16_f16 v[64:79], a[112:115], a[224:227], v[64:79]
	ds_read_b128 a[224:227], v193 offset:0
	v_add_f32_e32 v213, 1.0, v213
	v_add_f32_e32 v214, 1.0, v214
	v_rcp_f32_e32 v200, v200
	v_mfma_f32_32x32x16_f16 v[80:95], a[112:115], a[228:231], v[80:95]
	ds_read_b128 a[228:231], v193 offset:1024
	v_add_f32_e32 v215, 1.0, v215
	v_rcp_f32_e32 v201, v201
	v_mfma_f32_32x32x16_f16 v[64:79], a[116:119], a[232:235], v[64:79]
	ds_read_b128 a[232:235], v193 offset:2048
	v_rcp_f32_e32 v202, v202
	v_mfma_f32_32x32x16_f16 v[80:95], a[116:119], a[236:239], v[80:95]
	ds_read_b128 a[236:239], v193 offset:3072
	global_load_lds_dwordx4 v245, s[34:35] offset:3072 sc1
	v_rcp_f32_e32 v203, v203
	s_waitcnt lgkmcnt(2)
	v_mfma_f32_32x32x16_f16 v[64:79], a[120:123], a[240:243], v[64:79]
	ds_read_b128 a[240:243], v193 offset:4096
	v_rcp_f32_e32 v204, v204
	s_add_u32 s46, s42, 0x0
	s_addc_u32 s47, s43, 0
	global_load_dwordx4 v[0:3], v192, s[46:47] offset:0
	v_mfma_f32_32x32x16_f16 v[80:95], a[120:123], a[244:247], v[80:95]
	ds_read_b128 a[244:247], v193 offset:5120
	v_rcp_f32_e32 v205, v205
	v_mul_f32_e32 v204, v204, v140
	global_load_dwordx4 v[4:7], v192, s[46:47] offset:1024
	global_load_dwordx4 v[8:11], v192, s[46:47] offset:2048
	v_mfma_f32_32x32x16_f16 v[64:79], a[124:127], a[248:251], v[64:79]
	ds_read_b128 a[248:251], v193 offset:6144
	v_rcp_f32_e32 v206, v206
	v_mul_f32_e32 v205, v205, v141
	global_load_dwordx4 v[12:15], v192, s[46:47] offset:3072
	s_add_u32 s46, s42, 0x1000
	s_addc_u32 s47, s43, 0
	s_mov_b32 m0, s52
	v_mfma_f32_32x32x16_f16 v[80:95], a[124:127], a[252:255], v[80:95]
	ds_read_b128 a[252:255], v193 offset:7168
	v_cmp_gt_u32_e32 vcc, 4, v251
	s_cbranch_vccnz .LD_tpoll33
.LD_tok32:
	s_add_u32 s34, s34, 0x20000
	s_addc_u32 s35, s35, 0
	global_load_lds_dwordx4 v224, s[34:35] sc1
	v_rcp_f32_e32 v207, v207
	v_mul_f32_e32 v206, v206, v142
	global_load_dwordx4 v[16:19], v192, s[46:47] offset:0
	global_load_dwordx4 v[20:23], v192, s[46:47] offset:1024
	v_mfma_f32_32x32x16_f16 v[64:79], a[128:131], a[224:227], v[64:79]
	ds_read_b128 a[224:227], v193 offset:8192
	v_rcp_f32_e32 v208, v208
	v_mul_f32_e32 v207, v207, v143
	global_load_dwordx4 v[24:27], v192, s[46:47] offset:2048
	global_load_dwordx4 v[28:31], v192, s[46:47] offset:3072
	v_mfma_f32_32x32x16_f16 v[80:95], a[128:131], a[228:231], v[80:95]
	ds_read_b128 a[228:231], v193 offset:9216
	v_rcp_f32_e32 v209, v209
	v_fmamk_f32 v208, v208, 0xc0b8aa3b, v198
	s_waitcnt lgkmcnt(2)
	v_mfma_f32_32x32x16_f16 v[64:79], a[132:135], a[232:235], v[64:79]
	ds_read_b128 a[232:235], v193 offset:10240
	v_rcp_f32_e32 v210, v210
	v_fmamk_f32 v209, v209, 0xc0b8aa3b, v198
	v_fma_f32 v140, v200, v208, v204
	v_mfma_f32_32x32x16_f16 v[80:95], a[132:135], a[236:239], v[80:95]
	ds_read_b128 a[236:239], v193 offset:11264
	global_load_lds_dwordx4 v224, s[34:35] offset:1024 sc1
	v_rcp_f32_e32 v211, v211
	v_fmamk_f32 v210, v210, 0xc0b8aa3b, v198
	v_fma_f32 v141, v201, v209, v205
	v_mfma_f32_32x32x16_f16 v[64:79], a[136:139], a[240:243], v[64:79]
	ds_read_b128 a[240:243], v193 offset:12288
	v_rcp_f32_e32 v212, v212
	v_fmamk_f32 v211, v211, 0xc0b8aa3b, v198
	v_fma_f32 v142, v202, v210, v206
	v_mfma_f32_32x32x16_f16 v[80:95], a[136:139], a[244:247], v[80:95]
	ds_read_b128 a[244:247], v193 offset:13312
	v_rcp_f32_e32 v213, v213
	v_fma_f32 v143, v203, v211, v207
	v_mfma_f32_32x32x16_f16 v[64:79], a[140:143], a[248:251], v[64:79]
	ds_read_b128 a[248:251], v193 offset:14336
	v_rcp_f32_e32 v214, v214
	v_mfma_f32_32x32x16_f16 v[80:95], a[140:143], a[252:255], v[80:95]
	ds_read_b128 a[252:255], v193 offset:15360
	global_load_lds_dwordx4 v224, s[34:35] offset:2048 sc1
	v_rcp_f32_e32 v215, v215
	s_waitcnt lgkmcnt(2)
	v_mfma_f32_32x32x16_f16 v[64:79], a[144:147], a[224:227], v[64:79]
	ds_read_b128 a[224:227], v193 offset:16384
	v_exp_f32_e32 v200, v140
	v_mfma_f32_32x32x16_f16 v[80:95], a[144:147], a[228:231], v[80:95]
	ds_read_b128 a[228:231], v193 offset:17408
	v_exp_f32_e32 v201, v141
	v_add_f32_e32 v200, 1.0, v200
	v_mfma_f32_32x32x16_f16 v[64:79], a[148:151], a[232:235], v[64:79]
	ds_read_b128 a[232:235], v193 offset:18432
	v_exp_f32_e32 v202, v142
	v_add_f32_e32 v201, 1.0, v201
	v_mfma_f32_32x32x16_f16 v[80:95], a[148:151], a[236:239], v[80:95]
	ds_read_b128 a[236:239], v193 offset:19456
	global_load_lds_dwordx4 v224, s[34:35] offset:3072 sc1
	v_exp_f32_e32 v203, v143
	v_add_f32_e32 v202, 1.0, v202
	v_mfma_f32_32x32x16_f16 v[64:79], a[152:155], a[240:243], v[64:79]
	ds_read_b128 a[240:243], v193 offset:20480
	v_add_f32_e32 v203, 1.0, v203
	v_rcp_f32_e32 v200, v200
	v_mfma_f32_32x32x16_f16 v[80:95], a[152:155], a[244:247], v[80:95]
	ds_read_b128 a[244:247], v193 offset:21504
	v_rcp_f32_e32 v201, v201
	v_fma_f32 v200, v200, 2.0, -1.0
	s_waitcnt lgkmcnt(2)
	v_mfma_f32_32x32x16_f16 v[64:79], a[156:159], a[248:251], v[64:79]
	ds_read_b128 a[248:251], v193 offset:22528
	v_rcp_f32_e32 v202, v202
	v_fma_f32 v201, v201, 2.0, -1.0
	v_mul_f32_e32 v216, v212, v200
	s_mov_b32 m0, s53
	v_mfma_f32_32x32x16_f16 v[80:95], a[156:159], a[252:255], v[80:95]
	ds_read_b128 a[252:255], v193 offset:23552
	global_load_lds_dwordx4 v225, s[34:35] sc1
	v_rcp_f32_e32 v203, v203
	v_fma_f32 v202, v202, 2.0, -1.0
	v_mul_f32_e32 v217, v213, v201
	v_mfma_f32_32x32x16_f16 v[64:79], a[160:163], a[224:227], v[64:79]
	ds_read_b128 a[224:227], v193 offset:24576
	v_fma_f32 v203, v203, 2.0, -1.0
	v_mul_f32_e32 v218, v214, v202
	v_mfma_f32_32x32x16_f16 v[80:95], a[160:163], a[228:231], v[80:95]
	ds_read_b128 a[228:231], v193 offset:25600
	v_mul_f32_e32 v219, v215, v203
	v_mul_f32_e32 v236, v216, v228
	v_mfma_f32_32x32x16_f16 v[64:79], a[164:167], a[232:235], v[64:79]
	ds_read_b128 a[232:235], v193 offset:26624
	v_mul_f32_e32 v237, v216, v232
	v_fmac_f32_e32 v236, v217, v229
	v_mfma_f32_32x32x16_f16 v[80:95], a[164:167], a[236:239], v[80:95]
	ds_read_b128 a[236:239], v193 offset:27648
	global_load_lds_dwordx4 v225, s[34:35] offset:1024 sc1
	v_fmac_f32_e32 v237, v217, v233
	v_fmac_f32_e32 v236, v218, v230
	s_waitcnt lgkmcnt(2)
	v_mfma_f32_32x32x16_f16 v[64:79], a[168:171], a[240:243], v[64:79]
	ds_read_b128 a[240:243], v193 offset:28672
	v_fmac_f32_e32 v237, v218, v234
	v_fmac_f32_e32 v236, v219, v231
	v_mfma_f32_32x32x16_f16 v[80:95], a[168:171], a[244:247], v[80:95]
	ds_read_b128 a[244:247], v193 offset:29696
	v_fmac_f32_e32 v237, v219, v235
	v_mov_b32_e32 v238, v236
	v_mfma_f32_32x32x16_f16 v[64:79], a[172:175], a[248:251], v[64:79]
	ds_read_b128 a[248:251], v193 offset:30720
	v_mov_b32_e32 v239, v236
	v_mov_b32_e32 v240, v237
	v_mfma_f32_32x32x16_f16 v[80:95], a[172:175], a[252:255], v[80:95]
	ds_read_b128 a[252:255], v193 offset:31744
	global_load_lds_dwordx4 v225, s[34:35] offset:2048 sc1
	v_mov_b32_e32 v241, v237
	v_cvt_pk_f16_f32 v222, v216, v217
	s_waitcnt vmcnt(15)
	s_barrier
	v_mfma_f32_32x32x16_f16 v[64:79], a[176:179], a[224:227], v[64:79]
	ds_read_b128 a[224:227], v193 offset:32768
	s_nop 1
	v_permlane32_swap_b32_e32 v238, v239
	v_permlane32_swap_b32_e32 v240, v241
	v_add_f32_e32 v238, v238, v239
	v_add_f32_e32 v239, v240, v241
	ds_write_b64 v248, v[238:239] offset:768
	v_mfma_f32_32x32x16_f16 v[80:95], a[176:179], a[228:231], v[80:95]
	ds_read_b128 a[228:231], v193 offset:33792
	v_cvt_pk_f16_f32 v223, v218, v219
	s_waitcnt lgkmcnt(3)
	v_mfma_f32_32x32x16_f16 v[64:79], a[180:183], a[232:235], v[64:79]
	ds_read_b128 a[232:235], v193 offset:34816
	s_nop 1
	v_permlane32_swap_b32_e32 v220, v222
	v_permlane32_swap_b32_e32 v221, v223
	s_cmp_eq_u32 s31, 0
	s_cbranch_scc1 .LD_slow34
	global_store_dwordx4 v195, v[220:223], s[36:37] offset:0
.LD_join35:
	v_mfma_f32_32x32x16_f16 v[80:95], a[180:183], a[236:239], v[80:95]
	ds_read_b128 a[236:239], v193 offset:35840
	global_load_lds_dwordx4 v225, s[34:35] offset:3072 sc1
	v_mfma_f32_32x32x16_f16 v[64:79], a[184:187], a[240:243], v[64:79]
	ds_read_b128 a[240:243], v193 offset:36864
	v_mfma_f32_32x32x16_f16 v[80:95], a[184:187], a[244:247], v[80:95]
	ds_read_b128 a[244:247], v193 offset:37888
	v_mfma_f32_32x32x16_f16 v[64:79], a[188:191], a[248:251], v[64:79]
	ds_read_b128 a[248:251], v193 offset:38912
	s_mov_b32 m0, s54
	v_mfma_f32_32x32x16_f16 v[80:95], a[188:191], a[252:255], v[80:95]
	ds_read_b128 a[252:255], v193 offset:39936
	global_load_lds_dwordx4 v226, s[34:35] sc1
	s_waitcnt lgkmcnt(2)
	v_mfma_f32_32x32x16_f16 v[64:79], a[192:195], a[224:227], v[64:79]
	ds_read_b128 a[224:227], v193 offset:40960
	v_mfma_f32_32x32x16_f16 v[80:95], a[192:195], a[228:231], v[80:95]
	ds_read_b128 a[228:231], v193 offset:41984
	v_mfma_f32_32x32x16_f16 v[64:79], a[196:199], a[232:235], v[64:79]
	ds_read_b128 a[232:235], v193 offset:43008
	v_mfma_f32_32x32x16_f16 v[80:95], a[196:199], a[236:239], v[80:95]
	ds_read_b128 a[236:239], v193 offset:44032
	global_load_lds_dwordx4 v226, s[34:35] offset:1024 sc1
	v_mfma_f32_32x32x16_f16 v[64:79], a[200:203], a[240:243], v[64:79]
	ds_read_b128 a[240:243], v193 offset:45056
	v_mfma_f32_32x32x16_f16 v[80:95], a[200:203], a[244:247], v[80:95]
	ds_read_b128 a[244:247], v193 offset:46080
	s_waitcnt lgkmcnt(2)
	v_mfma_f32_32x32x16_f16 v[64:79], a[204:207], a[248:251], v[64:79]
	ds_read_b128 a[248:251], v193 offset:47104
	v_mfma_f32_32x32x16_f16 v[80:95], a[204:207], a[252:255], v[80:95]
	ds_read_b128 a[252:255], v193 offset:48128
	global_load_lds_dwordx4 v226, s[34:35] offset:2048 sc1
	s_waitcnt vmcnt(4)
	s_barrier
	v_mov_b32_e32 v199, 2
	s_cmp_eq_u32 s31, 0
	s_cbranch_scc1 .LD_slow36
	global_store_dword v197, v199, s[40:41]
.LD_join37:
	ds_read_b64 v[200:201], v249 offset:512
	ds_read_b64 v[202:203], v249 offset:2560
	ds_read_b64 v[204:205], v249 offset:4608
	ds_read_b64 v[206:207], v249 offset:6656
	v_mfma_f32_32x32x16_f16 v[64:79], a[208:211], a[224:227], v[64:79]
	ds_read_b128 a[224:227], v193 offset:49152
	v_mfma_f32_32x32x16_f16 v[80:95], a[208:211], a[228:231], v[80:95]
	ds_read_b128 a[228:231], v193 offset:50176
	v_mfma_f32_32x32x16_f16 v[64:79], a[212:215], a[232:235], v[64:79]
	ds_read_b128 a[232:235], v193 offset:51200
	v_mfma_f32_32x32x16_f16 v[80:95], a[212:215], a[236:239], v[80:95]
	ds_read_b128 a[236:239], v193 offset:52224
	global_load_lds_dwordx4 v226, s[34:35] offset:3072 sc1
	s_waitcnt lgkmcnt(2)
	v_mfma_f32_32x32x16_f16 v[64:79], a[216:219], a[240:243], v[64:79]
	ds_read_b128 a[240:243], v193 offset:53248
	v_mfma_f32_32x32x16_f16 v[80:95], a[216:219], a[244:247], v[80:95]
	ds_read_b128 a[244:247], v193 offset:54272
	v_mfma_f32_32x32x16_f16 v[64:79], a[220:223], a[248:251], v[64:79]
	ds_read_b128 a[248:251], v193 offset:55296
	s_mov_b32 m0, s55
	v_mfma_f32_32x32x16_f16 v[80:95], a[220:223], a[252:255], v[80:95]
	ds_read_b128 a[252:255], v193 offset:56320
	global_load_lds_dwordx4 v227, s[34:35] sc1
	v_mfma_f32_32x32x16_f16 v[64:79], v[160:163], a[224:227], v[64:79]
	ds_read_b128 a[224:227], v193 offset:57344
	v_mfma_f32_32x32x16_f16 v[80:95], v[160:163], a[228:231], v[80:95]
	ds_read_b128 a[228:231], v193 offset:58368
	s_waitcnt lgkmcnt(2)
	v_mfma_f32_32x32x16_f16 v[64:79], v[164:167], a[232:235], v[64:79]
	ds_read_b128 a[232:235], v193 offset:59392
	v_mfma_f32_32x32x16_f16 v[80:95], v[164:167], a[236:239], v[80:95]
	ds_read_b128 a[236:239], v193 offset:60416
	global_load_lds_dwordx4 v227, s[34:35] offset:1024 sc1
	v_add_f32_e32 v200, v200, v202
	v_add_f32_e32 v201, v201, v203
	v_add_f32_e32 v200, v200, v204
	v_add_f32_e32 v201, v201, v205
	v_add_f32_e32 v200, v200, v206
	v_add_f32_e32 v201, v201, v207
	global_store_dwordx2 v250, v[200:201], s[72:73]
	v_mfma_f32_32x32x16_f16 v[64:79], v[168:171], a[240:243], v[64:79]
	ds_read_b128 a[240:243], v193 offset:61440
	v_mfma_f32_32x32x16_f16 v[80:95], v[168:171], a[244:247], v[80:95]
	ds_read_b128 a[244:247], v193 offset:62464
	v_mfma_f32_32x32x16_f16 v[64:79], v[172:175], a[248:251], v[64:79]
	ds_read_b128 a[248:251], v193 offset:63488
	v_mfma_f32_32x32x16_f16 v[80:95], v[172:175], a[252:255], v[80:95]
	ds_read_b128 a[252:255], v193 offset:64512
	global_load_lds_dwordx4 v227, s[34:35] offset:2048 sc1
	s_and_b32 s64, s33, 1
	s_lshl_b32 s64, s64, 22
	s_add_u32 s64, s64, s50
	s_add_u32 s64, s64, 0x40000
	s_add_u32 s36, s6, s64
	s_addc_u32 s37, s7, 0
	s_lshl_b32 s64, s33, 3
	s_add_u32 s64, s64, s29
	s_lshl_b32 s64, s64, 5
	s_add_u32 s64, s64, s30
	s_lshl_b32 s64, s64, 2
	s_add_u32 s40, s8, s64
	s_addc_u32 s41, s9, 0
	s_lshl_b32 s64, s33, 19
	s_add_u32 s64, s64, 0x400
	s_add_u32 s72, s62, s64
	s_addc_u32 s73, s63, 0
	s_waitcnt vmcnt(9)
	s_barrier
	s_waitcnt lgkmcnt(2)
	v_mfma_f32_32x32x16_f16 v[64:79], v[176:179], a[224:227], v[64:79]
	ds_read_b128 a[224:227], v192 offset:0
	v_mfma_f32_32x32x16_f16 v[80:95], v[176:179], a[228:231], v[80:95]
	ds_read_b128 a[228:231], v192 offset:1024
	v_mfma_f32_32x32x16_f16 v[64:79], v[180:183], a[232:235], v[64:79]
	ds_read_b128 a[232:235], v192 offset:2048
	v_mfma_f32_32x32x16_f16 v[80:95], v[180:183], a[236:239], v[80:95]
	ds_read_b128 a[236:239], v192 offset:3072
	global_load_lds_dwordx4 v227, s[34:35] offset:3072 sc1
	v_mfma_f32_32x32x16_f16 v[64:79], v[184:187], a[240:243], v[64:79]
	ds_read_b128 a[240:243], v192 offset:4096
	v_mfma_f32_32x32x16_f16 v[80:95], v[184:187], a[244:247], v[80:95]
	ds_read_b128 a[244:247], v192 offset:5120
	s_waitcnt lgkmcnt(2)
	v_mfma_f32_32x32x16_f16 v[64:79], v[188:191], a[248:251], v[64:79]
	ds_read_b128 a[248:251], v192 offset:6144
	s_mov_b32 m0, s56
	v_mfma_f32_32x32x16_f16 v[80:95], v[188:191], a[252:255], v[80:95]
	ds_read_b128 a[252:255], v192 offset:7168
	global_load_lds_dwordx4 v242, s[34:35] sc1
	s_nop 5
	s_waitcnt lgkmcnt(2)
	v_mfma_f32_32x32x16_f16 v[96:111], a[0:3], a[224:227], v[96:111]
	ds_read_b128 a[224:227], v192 offset:8192
	v_exp_f32_e32 v200, v64
	v_mfma_f32_32x32x16_f16 v[112:127], a[0:3], a[228:231], v[112:127]
	ds_read_b128 a[228:231], v192 offset:9216
	s_lshl_b32 s64, s33, 3
	s_add_u32 s64, s64, s29
	s_lshl_b32 s64, s64, 7
	s_add_u32 s38, s8, s64
	s_addc_u32 s39, s9, 0
	global_load_dword v251, v196, s[38:39] sc1
	v_exp_f32_e32 v201, v65
	v_add_f32_e32 v200, 1.0, v200
	v_mfma_f32_32x32x16_f16 v[96:111], a[4:7], a[232:235], v[96:111]
	ds_read_b128 a[232:235], v192 offset:10240
	v_exp_f32_e32 v202, v66
	v_add_f32_e32 v201, 1.0, v201
	v_mfma_f32_32x32x16_f16 v[112:127], a[4:7], a[236:239], v[112:127]
	ds_read_b128 a[236:239], v192 offset:11264
	global_load_lds_dwordx4 v242, s[34:35] offset:1024 sc1
	v_exp_f32_e32 v203, v67
	v_add_f32_e32 v202, 1.0, v202
	v_mfma_f32_32x32x16_f16 v[96:111], a[8:11], a[240:243], v[96:111]
	ds_read_b128 a[240:243], v192 offset:12288
	v_exp_f32_e32 v204, v68
	v_add_f32_e32 v203, 1.0, v203
	v_mfma_f32_32x32x16_f16 v[112:127], a[8:11], a[244:247], v[112:127]
	ds_read_b128 a[244:247], v192 offset:13312
	v_exp_f32_e32 v205, v69
	v_add_f32_e32 v204, 1.0, v204
	s_waitcnt lgkmcnt(2)
	v_mfma_f32_32x32x16_f16 v[96:111], a[12:15], a[248:251], v[96:111]
	ds_read_b128 a[248:251], v192 offset:14336
	v_exp_f32_e32 v206, v70
	v_add_f32_e32 v205, 1.0, v205
	v_mfma_f32_32x32x16_f16 v[112:127], a[12:15], a[252:255], v[112:127]
	ds_read_b128 a[252:255], v192 offset:15360
	global_load_lds_dwordx4 v242, s[34:35] offset:2048 sc1
	v_exp_f32_e32 v207, v71
	v_add_f32_e32 v206, 1.0, v206
	v_mfma_f32_32x32x16_f16 v[96:111], a[16:19], a[224:227], v[96:111]
	ds_read_b128 a[224:227], v192 offset:16384
	v_exp_f32_e32 v208, v72
	v_add_f32_e32 v207, 1.0, v207
	v_mfma_f32_32x32x16_f16 v[112:127], a[16:19], a[228:231], v[112:127]
	ds_read_b128 a[228:231], v192 offset:17408
	v_exp_f32_e32 v209, v73
	v_add_f32_e32 v208, 1.0, v208
	v_mfma_f32_32x32x16_f16 v[96:111], a[20:23], a[232:235], v[96:111]
	ds_read_b128 a[232:235], v192 offset:18432
	v_exp_f32_e32 v210, v74
	v_add_f32_e32 v209, 1.0, v209
	v_mfma_f32_32x32x16_f16 v[112:127], a[20:23], a[236:239], v[112:127]
	ds_read_b128 a[236:239], v192 offset:19456
	global_load_lds_dwordx4 v242, s[34:35] offset:3072 sc1
	v_exp_f32_e32 v211, v75
	v_add_f32_e32 v210, 1.0, v210
	s_waitcnt lgkmcnt(2)
	v_mfma_f32_32x32x16_f16 v[96:111], a[24:27], a[240:243], v[96:111]
	ds_read_b128 a[240:243], v192 offset:20480
	v_exp_f32_e32 v212, v76
	v_add_f32_e32 v211, 1.0, v211
	v_mfma_f32_32x32x16_f16 v[112:127], a[24:27], a[244:247], v[112:127]
	ds_read_b128 a[244:247], v192 offset:21504
	v_exp_f32_e32 v213, v77
	v_add_f32_e32 v212, 1.0, v212
	v_mfma_f32_32x32x16_f16 v[96:111], a[28:31], a[248:251], v[96:111]
	ds_read_b128 a[248:251], v192 offset:22528
	v_exp_f32_e32 v214, v78
	v_add_f32_e32 v213, 1.0, v213
	s_mov_b32 m0, s57
	v_mfma_f32_32x32x16_f16 v[112:127], a[28:31], a[252:255], v[112:127]
	ds_read_b128 a[252:255], v192 offset:23552
	global_load_lds_dwordx4 v243, s[34:35] sc1
	v_exp_f32_e32 v215, v79
	v_add_f32_e32 v214, 1.0, v214
	v_mfma_f32_32x32x16_f16 v[96:111], a[32:35], a[224:227], v[96:111]
	ds_read_b128 a[224:227], v192 offset:24576
	v_add_f32_e32 v215, 1.0, v215
	v_rcp_f32_e32 v200, v200
	v_mfma_f32_32x32x16_f16 v[112:127], a[32:35], a[228:231], v[112:127]
	ds_read_b128 a[228:231], v192 offset:25600
	v_rcp_f32_e32 v201, v201
	s_waitcnt lgkmcnt(2)
	v_mfma_f32_32x32x16_f16 v[96:111], a[36:39], a[232:235], v[96:111]
	ds_read_b128 a[232:235], v192 offset:26624
	v_rcp_f32_e32 v202, v202
	v_mfma_f32_32x32x16_f16 v[112:127], a[36:39], a[236:239], v[112:127]
	ds_read_b128 a[236:239], v192 offset:27648
	global_load_lds_dwordx4 v243, s[34:35] offset:1024 sc1
	v_rcp_f32_e32 v203, v203
	v_mfma_f32_32x32x16_f16 v[96:111], a[40:43], a[240:243], v[96:111]
	ds_read_b128 a[240:243], v192 offset:28672
	v_rcp_f32_e32 v204, v204
	v_mfma_f32_32x32x16_f16 v[112:127], a[40:43], a[244:247], v[112:127]
	ds_read_b128 a[244:247], v192 offset:29696
	v_rcp_f32_e32 v205, v205
	v_mul_f32_e32 v204, v204, v144
	v_mfma_f32_32x32x16_f16 v[96:111], a[44:47], a[248:251], v[96:111]
	ds_read_b128 a[248:251], v192 offset:30720
	v_rcp_f32_e32 v206, v206
	v_mul_f32_e32 v205, v205, v145
	v_mfma_f32_32x32x16_f16 v[112:127], a[44:47], a[252:255], v[112:127]
	ds_read_b128 a[252:255], v192 offset:31744
	global_load_lds_dwordx4 v243, s[34:35] offset:2048 sc1
	v_rcp_f32_e32 v207, v207
	v_mul_f32_e32 v206, v206, v146
	s_waitcnt vmcnt(8)
	s_barrier
	s_waitcnt lgkmcnt(2)
	v_mfma_f32_32x32x16_f16 v[96:111], a[48:51], a[224:227], v[96:111]
	ds_read_b128 a[224:227], v192 offset:32768
	v_rcp_f32_e32 v208, v208
	v_mul_f32_e32 v207, v207, v147
	v_mfma_f32_32x32x16_f16 v[112:127], a[48:51], a[228:231], v[112:127]
	ds_read_b128 a[228:231], v192 offset:33792
	v_rcp_f32_e32 v209, v209
	v_fmamk_f32 v208, v208, 0xc0b8aa3b, v198
	v_mfma_f32_32x32x16_f16 v[96:111], a[52:55], a[232:235], v[96:111]
	ds_read_b128 a[232:235], v192 offset:34816
	v_rcp_f32_e32 v210, v210
	v_fmamk_f32 v209, v209, 0xc0b8aa3b, v198
	v_fma_f32 v144, v200, v208, v204
	v_mfma_f32_32x32x16_f16 v[112:127], a[52:55], a[236:239], v[112:127]
	ds_read_b128 a[236:239], v192 offset:35840
	global_load_lds_dwordx4 v243, s[34:35] offset:3072 sc1
	v_rcp_f32_e32 v211, v211
	v_fmamk_f32 v210, v210, 0xc0b8aa3b, v198
	v_fma_f32 v145, v201, v209, v205
	v_mfma_f32_32x32x16_f16 v[96:111], a[56:59], a[240:243], v[96:111]
	ds_read_b128 a[240:243], v192 offset:36864
	v_rcp_f32_e32 v212, v212
	v_fmamk_f32 v211, v211, 0xc0b8aa3b, v198
	v_fma_f32 v146, v202, v210, v206
	v_mfma_f32_32x32x16_f16 v[112:127], a[56:59], a[244:247], v[112:127]
	ds_read_b128 a[244:247], v192 offset:37888
	v_rcp_f32_e32 v213, v213
	v_fma_f32 v147, v203, v211, v207
	s_waitcnt lgkmcnt(2)
	v_mfma_f32_32x32x16_f16 v[96:111], a[60:63], a[248:251], v[96:111]
	ds_read_b128 a[248:251], v192 offset:38912
	v_rcp_f32_e32 v214, v214
	s_mov_b32 m0, s58
	v_mfma_f32_32x32x16_f16 v[112:127], a[60:63], a[252:255], v[112:127]
	ds_read_b128 a[252:255], v192 offset:39936
	global_load_lds_dwordx4 v244, s[34:35] sc1
	v_rcp_f32_e32 v215, v215
	v_mfma_f32_32x32x16_f16 v[96:111], a[64:67], a[224:227], v[96:111]
	ds_read_b128 a[224:227], v192 offset:40960
	v_exp_f32_e32 v200, v144
	v_mfma_f32_32x32x16_f16 v[112:127], a[64:67], a[228:231], v[112:127]
	ds_read_b128 a[228:231], v192 offset:41984
	v_exp_f32_e32 v201, v145
	v_add_f32_e32 v200, 1.0, v200
	v_mfma_f32_32x32x16_f16 v[96:111], a[68:71], a[232:235], v[96:111]
	ds_read_b128 a[232:235], v192 offset:43008
	v_exp_f32_e32 v202, v146
	v_add_f32_e32 v201, 1.0, v201
	v_mfma_f32_32x32x16_f16 v[112:127], a[68:71], a[236:239], v[112:127]
	ds_read_b128 a[236:239], v192 offset:44032
	global_load_lds_dwordx4 v244, s[34:35] offset:1024 sc1
	v_exp_f32_e32 v203, v147
	v_add_f32_e32 v202, 1.0, v202
	s_waitcnt lgkmcnt(2)
	v_mfma_f32_32x32x16_f16 v[96:111], a[72:75], a[240:243], v[96:111]
	ds_read_b128 a[240:243], v192 offset:45056
	v_add_f32_e32 v203, 1.0, v203
	v_rcp_f32_e32 v200, v200
	v_mfma_f32_32x32x16_f16 v[112:127], a[72:75], a[244:247], v[112:127]
	ds_read_b128 a[244:247], v192 offset:46080
	v_rcp_f32_e32 v201, v201
	v_fma_f32 v200, v200, 2.0, -1.0
	v_mfma_f32_32x32x16_f16 v[96:111], a[76:79], a[248:251], v[96:111]
	ds_read_b128 a[248:251], v192 offset:47104
	v_rcp_f32_e32 v202, v202
	v_fma_f32 v201, v201, 2.0, -1.0
	v_mul_f32_e32 v216, v212, v200
	v_mfma_f32_32x32x16_f16 v[112:127], a[76:79], a[252:255], v[112:127]
	ds_read_b128 a[252:255], v192 offset:48128
	global_load_lds_dwordx4 v244, s[34:35] offset:2048 sc1
	v_rcp_f32_e32 v203, v203
	v_fma_f32 v202, v202, 2.0, -1.0
	v_mul_f32_e32 v217, v213, v201
	v_mfma_f32_32x32x16_f16 v[96:111], a[80:83], a[224:227], v[96:111]
	ds_read_b128 a[224:227], v192 offset:49152
	v_fma_f32 v203, v203, 2.0, -1.0
	v_mul_f32_e32 v218, v214, v202
	v_exp_f32_e32 v200, v80
	v_mfma_f32_32x32x16_f16 v[112:127], a[80:83], a[228:231], v[112:127]
	ds_read_b128 a[228:231], v192 offset:50176
	v_mul_f32_e32 v219, v215, v203
	v_mul_f32_e32 v236, v216, v228
	v_exp_f32_e32 v201, v81
	s_waitcnt lgkmcnt(2)
	v_mfma_f32_32x32x16_f16 v[96:111], a[84:87], a[232:235], v[96:111]
	ds_read_b128 a[232:235], v192 offset:51200
	v_mul_f32_e32 v237, v216, v232
	v_fmac_f32_e32 v236, v217, v229
	v_exp_f32_e32 v202, v82
	v_mfma_f32_32x32x16_f16 v[112:127], a[84:87], a[236:239], v[112:127]
	ds_read_b128 a[236:239], v192 offset:52224
	global_load_lds_dwordx4 v244, s[34:35] offset:3072 sc1
	v_fmac_f32_e32 v237, v217, v233
	v_fmac_f32_e32 v236, v218, v230
	v_exp_f32_e32 v203, v83
	v_mfma_f32_32x32x16_f16 v[96:111], a[88:91], a[240:243], v[96:111]
	ds_read_b128 a[240:243], v192 offset:53248
	v_fmac_f32_e32 v237, v218, v234
	v_fmac_f32_e32 v236, v219, v231
	v_exp_f32_e32 v204, v84
	v_mfma_f32_32x32x16_f16 v[112:127], a[88:91], a[244:247], v[112:127]
	ds_read_b128 a[244:247], v192 offset:54272
	v_fmac_f32_e32 v237, v219, v235
	v_mov_b32_e32 v238, v236
	v_exp_f32_e32 v205, v85
	v_mfma_f32_32x32x16_f16 v[96:111], a[92:95], a[248:251], v[96:111]
	ds_read_b128 a[248:251], v192 offset:55296
	v_mov_b32_e32 v239, v236
	v_mov_b32_e32 v240, v237
	v_exp_f32_e32 v206, v86
	s_mov_b32 m0, s59
	v_mfma_f32_32x32x16_f16 v[112:127], a[92:95], a[252:255], v[112:127]
	ds_read_b128 a[252:255], v192 offset:56320
	global_load_lds_dwordx4 v245, s[34:35] sc1
	v_mov_b32_e32 v241, v237
	v_cvt_pk_f16_f32 v220, v216, v217
	v_exp_f32_e32 v207, v87
	s_waitcnt lgkmcnt(2)
	v_mfma_f32_32x32x16_f16 v[96:111], a[96:99], a[224:227], v[96:111]
	ds_read_b128 a[224:227], v192 offset:57344
	s_nop 1
	v_permlane32_swap_b32_e32 v238, v239
	v_permlane32_swap_b32_e32 v240, v241
	v_add_f32_e32 v238, v238, v239
	v_add_f32_e32 v239, v240, v241
	ds_write_b64 v248, v[238:239] offset:1024
	v_exp_f32_e32 v208, v88
	v_mfma_f32_32x32x16_f16 v[112:127], a[96:99], a[228:231], v[112:127]
	ds_read_b128 a[228:231], v192 offset:58368
	v_cvt_pk_f16_f32 v221, v218, v219
	v_exp_f32_e32 v209, v89
	v_add_f32_e32 v200, 1.0, v200
	v_mfma_f32_32x32x16_f16 v[96:111], a[100:103], a[232:235], v[96:111]
	ds_read_b128 a[232:235], v192 offset:59392
	v_exp_f32_e32 v210, v90
	v_add_f32_e32 v201, 1.0, v201
	v_add_f32_e32 v202, 1.0, v202
	v_mfma_f32_32x32x16_f16 v[112:127], a[100:103], a[236:239], v[112:127]
	ds_read_b128 a[236:239], v192 offset:60416
	global_load_lds_dwordx4 v245, s[34:35] offset:1024 sc1
	v_exp_f32_e32 v211, v91
	v_add_f32_e32 v203, 1.0, v203
	v_add_f32_e32 v204, 1.0, v204
	v_mfma_f32_32x32x16_f16 v[96:111], a[104:107], a[240:243], v[96:111]
	ds_read_b128 a[240:243], v192 offset:61440
	v_exp_f32_e32 v212, v92
	v_add_f32_e32 v205, 1.0, v205
	v_add_f32_e32 v206, 1.0, v206
	v_mfma_f32_32x32x16_f16 v[112:127], a[104:107], a[244:247], v[112:127]
	ds_read_b128 a[244:247], v192 offset:62464
	v_exp_f32_e32 v213, v93
	v_add_f32_e32 v207, 1.0, v207
	v_add_f32_e32 v208, 1.0, v208
	s_waitcnt lgkmcnt(2)
	v_mfma_f32_32x32x16_f16 v[96:111], a[108:111], a[248:251], v[96:111]
	ds_read_b128 a[248:251], v192 offset:63488
	v_exp_f32_e32 v214, v94
	v_add_f32_e32 v209, 1.0, v209
	v_add_f32_e32 v210, 1.0, v210
	v_mfma_f32_32x32x16_f16 v[112:127], a[108:111], a[252:255], v[112:127]
	ds_read_b128 a[252:255], v192 offset:64512
	global_load_lds_dwordx4 v245, s[34:35] offset:2048 sc1
	v_exp_f32_e32 v215, v95
	v_add_f32_e32 v211, 1.0, v211
	v_add_f32_e32 v212, 1.0, v212
	s_waitcnt vmcnt(7)
	s_barrier
	v_mfma_f32_32x32x16_f16 v[96:111], a[112:115], a[224:227], v[96:111]
	ds_read_b128 a[224:227], v193 offset:0
	v_add_f32_e32 v213, 1.0, v213
	v_add_f32_e32 v214, 1.0, v214
	v_rcp_f32_e32 v200, v200
	v_mfma_f32_32x32x16_f16 v[112:127], a[112:115], a[228:231], v[112:127]
	ds_read_b128 a[228:231], v193 offset:1024
	v_add_f32_e32 v215, 1.0, v215
	v_rcp_f32_e32 v201, v201
	v_mfma_f32_32x32x16_f16 v[96:111], a[116:119], a[232:235], v[96:111]
	ds_read_b128 a[232:235], v193 offset:2048
	v_rcp_f32_e32 v202, v202
	v_mfma_f32_32x32x16_f16 v[112:127], a[116:119], a[236:239], v[112:127]
	ds_read_b128 a[236:239], v193 offset:3072
	global_load_lds_dwordx4 v245, s[34:35] offset:3072 sc1
	v_rcp_f32_e32 v203, v203
	s_waitcnt lgkmcnt(2)
	v_mfma_f32_32x32x16_f16 v[96:111], a[120:123], a[240:243], v[96:111]
	ds_read_b128 a[240:243], v193 offset:4096
	v_rcp_f32_e32 v204, v204
	s_add_u32 s46, s42, 0x2000
	s_addc_u32 s47, s43, 0
	global_load_dwordx4 v[32:35], v192, s[46:47] offset:0
	v_mfma_f32_32x32x16_f16 v[112:127], a[120:123], a[244:247], v[112:127]
	ds_read_b128 a[244:247], v193 offset:5120
	v_rcp_f32_e32 v205, v205
	v_mul_f32_e32 v204, v204, v148
	global_load_dwordx4 v[36:39], v192, s[46:47] offset:1024
	global_load_dwordx4 v[40:43], v192, s[46:47] offset:2048
	v_mfma_f32_32x32x16_f16 v[96:111], a[124:127], a[248:251], v[96:111]
	ds_read_b128 a[248:251], v193 offset:6144
	v_rcp_f32_e32 v206, v206
	v_mul_f32_e32 v205, v205, v149
	global_load_dwordx4 v[44:47], v192, s[46:47] offset:3072
	s_add_u32 s46, s42, 0x3000
	s_addc_u32 s47, s43, 0
	s_mov_b32 m0, s52
	v_mfma_f32_32x32x16_f16 v[112:127], a[124:127], a[252:255], v[112:127]
	ds_read_b128 a[252:255], v193 offset:7168
	v_cmp_gt_u32_e32 vcc, 1, v251
	s_cbranch_vccnz .LD_tpoll39
.LD_tok38:
	s_and_b32 s64, s33, 1
	s_lshl_b32 s64, s64, 22
	s_add_u32 s64, s64, s49
	s_add_u32 s34, s6, s64
	s_addc_u32 s35, s7, 0
	global_load_lds_dwordx4 v224, s[34:35] sc1
	v_rcp_f32_e32 v207, v207
	v_mul_f32_e32 v206, v206, v150
	global_load_dwordx4 v[48:51], v192, s[46:47] offset:0
	global_load_dwordx4 v[52:55], v192, s[46:47] offset:1024
	v_mfma_f32_32x32x16_f16 v[96:111], a[128:131], a[224:227], v[96:111]
	ds_read_b128 a[224:227], v193 offset:8192
	v_rcp_f32_e32 v208, v208
	v_mul_f32_e32 v207, v207, v151
	global_load_dwordx4 v[56:59], v192, s[46:47] offset:2048
	global_load_dwordx4 v[60:63], v192, s[46:47] offset:3072
	v_mfma_f32_32x32x16_f16 v[112:127], a[128:131], a[228:231], v[112:127]
	ds_read_b128 a[228:231], v193 offset:9216
	v_rcp_f32_e32 v209, v209
	v_fmamk_f32 v208, v208, 0xc0b8aa3b, v198
	s_waitcnt lgkmcnt(2)
	v_mfma_f32_32x32x16_f16 v[96:111], a[132:135], a[232:235], v[96:111]
	ds_read_b128 a[232:235], v193 offset:10240
	v_rcp_f32_e32 v210, v210
	v_fmamk_f32 v209, v209, 0xc0b8aa3b, v198
	v_fma_f32 v148, v200, v208, v204
	v_mfma_f32_32x32x16_f16 v[112:127], a[132:135], a[236:239], v[112:127]
	ds_read_b128 a[236:239], v193 offset:11264
	global_load_lds_dwordx4 v224, s[34:35] offset:1024 sc1
	v_rcp_f32_e32 v211, v211
	v_fmamk_f32 v210, v210, 0xc0b8aa3b, v198
	v_fma_f32 v149, v201, v209, v205
	v_mfma_f32_32x32x16_f16 v[96:111], a[136:139], a[240:243], v[96:111]
	ds_read_b128 a[240:243], v193 offset:12288
	v_rcp_f32_e32 v212, v212
	v_fmamk_f32 v211, v211, 0xc0b8aa3b, v198
	v_fma_f32 v150, v202, v210, v206
	v_mfma_f32_32x32x16_f16 v[112:127], a[136:139], a[244:247], v[112:127]
	ds_read_b128 a[244:247], v193 offset:13312
	v_rcp_f32_e32 v213, v213
	v_fma_f32 v151, v203, v211, v207
	v_mfma_f32_32x32x16_f16 v[96:111], a[140:143], a[248:251], v[96:111]
	ds_read_b128 a[248:251], v193 offset:14336
	v_rcp_f32_e32 v214, v214
	v_mfma_f32_32x32x16_f16 v[112:127], a[140:143], a[252:255], v[112:127]
	ds_read_b128 a[252:255], v193 offset:15360
	global_load_lds_dwordx4 v224, s[34:35] offset:2048 sc1
	v_rcp_f32_e32 v215, v215
	s_waitcnt lgkmcnt(2)
	v_mfma_f32_32x32x16_f16 v[96:111], a[144:147], a[224:227], v[96:111]
	ds_read_b128 a[224:227], v193 offset:16384
	v_exp_f32_e32 v200, v148
	v_mfma_f32_32x32x16_f16 v[112:127], a[144:147], a[228:231], v[112:127]
	ds_read_b128 a[228:231], v193 offset:17408
	v_exp_f32_e32 v201, v149
	v_add_f32_e32 v200, 1.0, v200
	v_mfma_f32_32x32x16_f16 v[96:111], a[148:151], a[232:235], v[96:111]
	ds_read_b128 a[232:235], v193 offset:18432
	v_exp_f32_e32 v202, v150
	v_add_f32_e32 v201, 1.0, v201
	v_mfma_f32_32x32x16_f16 v[112:127], a[148:151], a[236:239], v[112:127]
	ds_read_b128 a[236:239], v193 offset:19456
	global_load_lds_dwordx4 v224, s[34:35] offset:3072 sc1
	v_exp_f32_e32 v203, v151
	v_add_f32_e32 v202, 1.0, v202
	v_mfma_f32_32x32x16_f16 v[96:111], a[152:155], a[240:243], v[96:111]
	ds_read_b128 a[240:243], v193 offset:20480
	v_add_f32_e32 v203, 1.0, v203
	v_rcp_f32_e32 v200, v200
	v_mfma_f32_32x32x16_f16 v[112:127], a[152:155], a[244:247], v[112:127]
	ds_read_b128 a[244:247], v193 offset:21504
	v_rcp_f32_e32 v201, v201
	v_fma_f32 v200, v200, 2.0, -1.0
	s_waitcnt lgkmcnt(2)
	v_mfma_f32_32x32x16_f16 v[96:111], a[156:159], a[248:251], v[96:111]
	ds_read_b128 a[248:251], v193 offset:22528
	v_rcp_f32_e32 v202, v202
	v_fma_f32 v201, v201, 2.0, -1.0
	v_mul_f32_e32 v216, v212, v200
	s_mov_b32 m0, s53
	v_mfma_f32_32x32x16_f16 v[112:127], a[156:159], a[252:255], v[112:127]
	ds_read_b128 a[252:255], v193 offset:23552
	global_load_lds_dwordx4 v225, s[34:35] sc1
	v_rcp_f32_e32 v203, v203
	v_fma_f32 v202, v202, 2.0, -1.0
	v_mul_f32_e32 v217, v213, v201
	v_mfma_f32_32x32x16_f16 v[96:111], a[160:163], a[224:227], v[96:111]
	ds_read_b128 a[224:227], v193 offset:24576
	v_fma_f32 v203, v203, 2.0, -1.0
	v_mul_f32_e32 v218, v214, v202
	v_mfma_f32_32x32x16_f16 v[112:127], a[160:163], a[228:231], v[112:127]
	ds_read_b128 a[228:231], v193 offset:25600
	v_mul_f32_e32 v219, v215, v203
	v_mul_f32_e32 v236, v216, v228
	v_mfma_f32_32x32x16_f16 v[96:111], a[164:167], a[232:235], v[96:111]
	ds_read_b128 a[232:235], v193 offset:26624
	v_mul_f32_e32 v237, v216, v232
	v_fmac_f32_e32 v236, v217, v229
	v_mfma_f32_32x32x16_f16 v[112:127], a[164:167], a[236:239], v[112:127]
	ds_read_b128 a[236:239], v193 offset:27648
	global_load_lds_dwordx4 v225, s[34:35] offset:1024 sc1
	v_fmac_f32_e32 v237, v217, v233
	v_fmac_f32_e32 v236, v218, v230
	s_waitcnt lgkmcnt(2)
	v_mfma_f32_32x32x16_f16 v[96:111], a[168:171], a[240:243], v[96:111]
	ds_read_b128 a[240:243], v193 offset:28672
	v_fmac_f32_e32 v237, v218, v234
	v_fmac_f32_e32 v236, v219, v231
	v_mfma_f32_32x32x16_f16 v[112:127], a[168:171], a[244:247], v[112:127]
	ds_read_b128 a[244:247], v193 offset:29696
	v_fmac_f32_e32 v237, v219, v235
	v_mov_b32_e32 v238, v236
	v_mfma_f32_32x32x16_f16 v[96:111], a[172:175], a[248:251], v[96:111]
	ds_read_b128 a[248:251], v193 offset:30720
	v_mov_b32_e32 v239, v236
	v_mov_b32_e32 v240, v237
	v_mfma_f32_32x32x16_f16 v[112:127], a[172:175], a[252:255], v[112:127]
	ds_read_b128 a[252:255], v193 offset:31744
	global_load_lds_dwordx4 v225, s[34:35] offset:2048 sc1
	v_mov_b32_e32 v241, v237
	v_cvt_pk_f16_f32 v222, v216, v217
	s_waitcnt vmcnt(15)
	s_barrier
	v_mfma_f32_32x32x16_f16 v[96:111], a[176:179], a[224:227], v[96:111]
	ds_read_b128 a[224:227], v193 offset:32768
	s_nop 1
	v_permlane32_swap_b32_e32 v238, v239
	v_permlane32_swap_b32_e32 v240, v241
	v_add_f32_e32 v238, v238, v239
	v_add_f32_e32 v239, v240, v241
	ds_write_b64 v248, v[238:239] offset:1280
	v_mfma_f32_32x32x16_f16 v[112:127], a[176:179], a[228:231], v[112:127]
	ds_read_b128 a[228:231], v193 offset:33792
	v_cvt_pk_f16_f32 v223, v218, v219
	s_waitcnt lgkmcnt(3)
	v_mfma_f32_32x32x16_f16 v[96:111], a[180:183], a[232:235], v[96:111]
	ds_read_b128 a[232:235], v193 offset:34816
	s_nop 1
	v_permlane32_swap_b32_e32 v220, v222
	v_permlane32_swap_b32_e32 v221, v223
	s_cmp_eq_u32 s31, 0
	s_cbranch_scc1 .LD_slow40
	global_store_dwordx4 v195, v[220:223], s[36:37] offset:0
.LD_join41:
	v_mfma_f32_32x32x16_f16 v[112:127], a[180:183], a[236:239], v[112:127]
	ds_read_b128 a[236:239], v193 offset:35840
	global_load_lds_dwordx4 v225, s[34:35] offset:3072 sc1
	v_mfma_f32_32x32x16_f16 v[96:111], a[184:187], a[240:243], v[96:111]
	ds_read_b128 a[240:243], v193 offset:36864
	v_mfma_f32_32x32x16_f16 v[112:127], a[184:187], a[244:247], v[112:127]
	ds_read_b128 a[244:247], v193 offset:37888
	v_mfma_f32_32x32x16_f16 v[96:111], a[188:191], a[248:251], v[96:111]
	ds_read_b128 a[248:251], v193 offset:38912
	s_mov_b32 m0, s54
	v_mfma_f32_32x32x16_f16 v[112:127], a[188:191], a[252:255], v[112:127]
	ds_read_b128 a[252:255], v193 offset:39936
	global_load_lds_dwordx4 v226, s[34:35] sc1
	s_waitcnt lgkmcnt(2)
	v_mfma_f32_32x32x16_f16 v[96:111], a[192:195], a[224:227], v[96:111]
	ds_read_b128 a[224:227], v193 offset:40960
	v_mfma_f32_32x32x16_f16 v[112:127], a[192:195], a[228:231], v[112:127]
	ds_read_b128 a[228:231], v193 offset:41984
	v_mfma_f32_32x32x16_f16 v[96:111], a[196:199], a[232:235], v[96:111]
	ds_read_b128 a[232:235], v193 offset:43008
	v_mfma_f32_32x32x16_f16 v[112:127], a[196:199], a[236:239], v[112:127]
	ds_read_b128 a[236:239], v193 offset:44032
	global_load_lds_dwordx4 v226, s[34:35] offset:1024 sc1
	v_mfma_f32_32x32x16_f16 v[96:111], a[200:203], a[240:243], v[96:111]
	ds_read_b128 a[240:243], v193 offset:45056
	v_mfma_f32_32x32x16_f16 v[112:127], a[200:203], a[244:247], v[112:127]
	ds_read_b128 a[244:247], v193 offset:46080
	s_waitcnt lgkmcnt(2)
	v_mfma_f32_32x32x16_f16 v[96:111], a[204:207], a[248:251], v[96:111]
	ds_read_b128 a[248:251], v193 offset:47104
	v_mfma_f32_32x32x16_f16 v[112:127], a[204:207], a[252:255], v[112:127]
	ds_read_b128 a[252:255], v193 offset:48128
	global_load_lds_dwordx4 v226, s[34:35] offset:2048 sc1
	s_waitcnt vmcnt(4)
	s_barrier
	v_mov_b32_e32 v199, 3
	s_cmp_eq_u32 s31, 0
	s_cbranch_scc1 .LD_slow42
	global_store_dword v197, v199, s[40:41]
.LD_join43:
	ds_read_b64 v[200:201], v249 offset:1024
	ds_read_b64 v[202:203], v249 offset:3072
	ds_read_b64 v[204:205], v249 offset:5120
	ds_read_b64 v[206:207], v249 offset:7168
	v_mfma_f32_32x32x16_f16 v[96:111], a[208:211], a[224:227], v[96:111]
	ds_read_b128 a[224:227], v193 offset:49152
	v_mfma_f32_32x32x16_f16 v[112:127], a[208:211], a[228:231], v[112:127]
	ds_read_b128 a[228:231], v193 offset:50176
	v_mfma_f32_32x32x16_f16 v[96:111], a[212:215], a[232:235], v[96:111]
	ds_read_b128 a[232:235], v193 offset:51200
	v_mfma_f32_32x32x16_f16 v[112:127], a[212:215], a[236:239], v[112:127]
	ds_read_b128 a[236:239], v193 offset:52224
	global_load_lds_dwordx4 v226, s[34:35] offset:3072 sc1
	s_waitcnt lgkmcnt(2)
	v_mfma_f32_32x32x16_f16 v[96:111], a[216:219], a[240:243], v[96:111]
	ds_read_b128 a[240:243], v193 offset:53248
	v_mfma_f32_32x32x16_f16 v[112:127], a[216:219], a[244:247], v[112:127]
	ds_read_b128 a[244:247], v193 offset:54272
	v_mfma_f32_32x32x16_f16 v[96:111], a[220:223], a[248:251], v[96:111]
	ds_read_b128 a[248:251], v193 offset:55296
	s_mov_b32 m0, s55
	v_mfma_f32_32x32x16_f16 v[112:127], a[220:223], a[252:255], v[112:127]
	ds_read_b128 a[252:255], v193 offset:56320
	global_load_lds_dwordx4 v227, s[34:35] sc1
	v_mfma_f32_32x32x16_f16 v[96:111], v[160:163], a[224:227], v[96:111]
	ds_read_b128 a[224:227], v193 offset:57344
	v_mfma_f32_32x32x16_f16 v[112:127], v[160:163], a[228:231], v[112:127]
	ds_read_b128 a[228:231], v193 offset:58368
	s_waitcnt lgkmcnt(2)
	v_mfma_f32_32x32x16_f16 v[96:111], v[164:167], a[232:235], v[96:111]
	ds_read_b128 a[232:235], v193 offset:59392
	v_mfma_f32_32x32x16_f16 v[112:127], v[164:167], a[236:239], v[112:127]
	ds_read_b128 a[236:239], v193 offset:60416
	global_load_lds_dwordx4 v227, s[34:35] offset:1024 sc1
	v_add_f32_e32 v200, v200, v202
	v_add_f32_e32 v201, v201, v203
	v_add_f32_e32 v200, v200, v204
	v_add_f32_e32 v201, v201, v205
	v_add_f32_e32 v200, v200, v206
	v_add_f32_e32 v201, v201, v207
	global_store_dwordx2 v250, v[200:201], s[72:73]
	v_mfma_f32_32x32x16_f16 v[96:111], v[168:171], a[240:243], v[96:111]
	ds_read_b128 a[240:243], v193 offset:61440
	v_mfma_f32_32x32x16_f16 v[112:127], v[168:171], a[244:247], v[112:127]
	ds_read_b128 a[244:247], v193 offset:62464
	v_mfma_f32_32x32x16_f16 v[96:111], v[172:175], a[248:251], v[96:111]
	ds_read_b128 a[248:251], v193 offset:63488
	v_mfma_f32_32x32x16_f16 v[112:127], v[172:175], a[252:255], v[112:127]
	ds_read_b128 a[252:255], v193 offset:64512
	global_load_lds_dwordx4 v227, s[34:35] offset:2048 sc1
	s_waitcnt vmcnt(9)
	s_barrier
	s_waitcnt lgkmcnt(2)
	v_mfma_f32_32x32x16_f16 v[96:111], v[176:179], a[224:227], v[96:111]
	ds_read_b128 a[224:227], v192 offset:0
	v_mfma_f32_32x32x16_f16 v[112:127], v[176:179], a[228:231], v[112:127]
	ds_read_b128 a[228:231], v192 offset:1024
	v_mfma_f32_32x32x16_f16 v[96:111], v[180:183], a[232:235], v[96:111]
	ds_read_b128 a[232:235], v192 offset:2048
	v_mfma_f32_32x32x16_f16 v[112:127], v[180:183], a[236:239], v[112:127]
	ds_read_b128 a[236:239], v192 offset:3072
	global_load_lds_dwordx4 v227, s[34:35] offset:3072 sc1
	v_mfma_f32_32x32x16_f16 v[96:111], v[184:187], a[240:243], v[96:111]
	ds_read_b128 a[240:243], v192 offset:4096
	v_mfma_f32_32x32x16_f16 v[112:127], v[184:187], a[244:247], v[112:127]
	ds_read_b128 a[244:247], v192 offset:5120
	s_waitcnt lgkmcnt(2)
	v_mfma_f32_32x32x16_f16 v[96:111], v[188:191], a[248:251], v[96:111]
	ds_read_b128 a[248:251], v192 offset:6144
	s_mov_b32 m0, s56
	v_mfma_f32_32x32x16_f16 v[112:127], v[188:191], a[252:255], v[112:127]
	ds_read_b128 a[252:255], v192 offset:7168
	global_load_lds_dwordx4 v242, s[34:35] sc1
	s_add_u32 s33, s33, 1
	s_cmp_lt_u32 s33, s28
	s_cbranch_scc1 .LD_loop16
